# K-loop load phases: address add placed between the m0 write and its LDS-DMA load (80 s_nop pads gone)
# baseline (speedup 1.0000x reference)
; #define GM_STAGE(bufoff, gbase, voff) do { _Pragma("unroll") for (int _i = 0; _i < 2; ++_i) \
;         __builtin_amdgcn_global_load_lds((const unsigned*)((const char*)(gbase) + (voff)[_i]), (LAS unsigned*)(lds + (bufoff) + ldsw + _i * 8192), 16, 0, 0); } while (0)
; #define GM_LDA(dst, b, h) do { _Pragma("unroll") for (int m = 0; m < 4; ++m) _Pragma("unroll") for (int k = 0; k < 2; ++k) dst[m][k] = *(const LAS s16x8*)(lds + GM_SA(b, h) + aoff + m * 2048 + k * 1024); } while (0)
; #define GM_LDB(dst, b, h) do { _Pragma("unroll") for (int n = 0; n < 2; ++n) _Pragma("unroll") for (int k = 0; k < 2; ++k) dst[n][k] = *(const LAS s16x8*)(lds + GM_SB(b, h) + boff + n * 2048 + k * 1024); } while (0)
; #define GM_MMA(ai, bj, At, Bt) do { __builtin_amdgcn_s_setprio(1); _Pragma("unroll") for (int m = 0; m < 4; ++m) _Pragma("unroll") for (int n = 0; n < 2; ++n) _Pragma("unroll") for (int k = 0; k < 2; ++k) \
;         acc[ai][bj][m][n] = mma16<BF>(Bt[n][k], At[m][k], acc[ai][bj][m][n]); __builtin_amdgcn_s_setprio(0); } while (0)
; #define GM_WAIT_V(n) asm volatile("s_waitcnt vmcnt(" #n ")" ::: "memory")
; #define GM_WAIT_L(n) asm volatile("s_waitcnt lgkmcnt(" #n ")" ::: "memory")
; #define GM_BAR __builtin_amdgcn_s_barrier()
; template <bool BF, bool GATHER = false, class Epi, class Hook>
; __device__ __forceinline__ void gemm_phase(LAS unsigned char* lds, const Gemm g, const Order& S, const Epi& E, Hook& HK) {
;     ...
;         for (int t = 0; t < nt; t += 2) {
;             const bool last = (t == nt - 2);
;             const char* a1 = cA + (size_t)(t + 1) * kstep;
;             const char* a2 = last ? nA : cA + (size_t)(t + 2) * kstep; const char* b2 = last ? nB : cB + (size_t)(t + 2) * kstep;
;             const char* a3 = a2 + kstep; const char* b3 = b2 + kstep;
;             unsigned s0[2], s1[2];
;             if constexpr (GATHER) { s0[0] = last ? nA0[0] : gA0[0]; s0[1] = last ? nA0[1] : gA0[1]; s1[0] = last ? nA1[0] : gA1[0]; s1[1] = last ? nA1[1] : gA1[1]; }
;             GM_LDB(B0, 0, 0); GM_LDB(B1, 0, 1); GM_SCHED; GM_LDA(At, 0, 0); GM_STA_H1(GM_SA(1, 1), a1, gA1);
;             GM_WAIT_V(8); GM_WAIT_L(0); GM_BAR; GM_MMA(0, 0, At, B0); GM_MMA(0, 1, At, B1); GM_BAR; GM_SCHED;
;             GM_LDA(At, 0, 1); GM_STAGE(GM_SB(0, 0), b2, voffB); GM_STAGE(GM_SB(0, 1), b2 + hstepB, voffB); GM_STA_H0(GM_SA(0, 0), a2, s0);
.LBB0_380:
	s_add_u32 s28, s2, 0xfffc0080
	s_addc_u32 s29, s3, -1
	s_cmp_eq_u32 s51, 12
	s_cselect_b32 s31, s9, s29
	s_cselect_b32 s30, s19, s28
	s_cselect_b32 s29, s21, s50
	s_cselect_b32 s28, s48, s49
	s_add_i32 m0, s27, 0xc000
	v_lshl_add_u64 v[150:151], s[2:3], 0, v[138:139]
	global_load_lds_dwordx4 v[150:151], off
	s_add_i32 m0, s27, 0xe000
	v_lshl_add_u64 v[150:151], s[2:3], 0, v[140:141]
	global_load_lds_dwordx4 v[150:151], off
	ds_read_b128 v[146:149], v158
	ds_read_b128 v[162:165], v158 offset:1024
	ds_read_b128 v[166:169], v158 offset:2048
	ds_read_b128 v[170:173], v158 offset:3072
	ds_read_b128 v[174:177], v159
	ds_read_b128 v[178:181], v159 offset:1024
	ds_read_b128 v[182:185], v159 offset:2048
	ds_read_b128 v[186:189], v159 offset:3072
	ds_read_b128 v[190:193], v160
	ds_read_b128 v[194:197], v160 offset:1024
	ds_read_b128 v[198:201], v160 offset:2048
	ds_read_b128 v[202:205], v160 offset:3072
	ds_read_b128 v[206:209], v160 offset:4096
	ds_read_b128 v[210:213], v160 offset:5120
	ds_read_b128 v[214:217], v160 offset:6144
	ds_read_b128 v[218:221], v160 offset:7168
	s_waitcnt vmcnt(8)
	s_waitcnt lgkmcnt(0)
	s_barrier
	v_mfma_f32_16x16x32_f16 v[126:129], v[146:149], v[190:193], v[126:129]
	v_mfma_f32_16x16x32_f16 v[122:125], v[166:169], v[190:193], v[122:125]
	v_mfma_f32_16x16x32_f16 v[110:113], v[146:149], v[198:201], v[110:113]
	v_mfma_f32_16x16x32_f16 v[106:109], v[166:169], v[198:201], v[106:109]
	v_mfma_f32_16x16x32_f16 v[94:97], v[146:149], v[206:209], v[94:97]
	v_mfma_f32_16x16x32_f16 v[90:93], v[166:169], v[206:209], v[90:93]
	v_mfma_f32_16x16x32_f16 v[78:81], v[146:149], v[214:217], v[78:81]
	v_mfma_f32_16x16x32_f16 v[74:77], v[166:169], v[214:217], v[74:77]
	v_mfma_f32_16x16x32_f16 v[126:129], v[162:165], v[194:197], v[126:129]
	v_mfma_f32_16x16x32_f16 v[122:125], v[170:173], v[194:197], v[122:125]
	v_mfma_f32_16x16x32_f16 v[110:113], v[162:165], v[202:205], v[110:113]
	v_mfma_f32_16x16x32_f16 v[106:109], v[170:173], v[202:205], v[106:109]
	v_mfma_f32_16x16x32_f16 v[94:97], v[162:165], v[210:213], v[94:97]
	v_mfma_f32_16x16x32_f16 v[90:93], v[170:173], v[210:213], v[90:93]
	v_mfma_f32_16x16x32_f16 v[78:81], v[162:165], v[218:221], v[78:81]
	v_mfma_f32_16x16x32_f16 v[74:77], v[170:173], v[218:221], v[74:77]
	v_mfma_f32_16x16x32_f16 v[118:121], v[174:177], v[190:193], v[118:121]
	v_mfma_f32_16x16x32_f16 v[114:117], v[182:185], v[190:193], v[114:117]
	v_mfma_f32_16x16x32_f16 v[102:105], v[174:177], v[198:201], v[102:105]
	v_mfma_f32_16x16x32_f16 v[98:101], v[182:185], v[198:201], v[98:101]
	v_mfma_f32_16x16x32_f16 v[86:89], v[174:177], v[206:209], v[86:89]
	v_mfma_f32_16x16x32_f16 v[82:85], v[182:185], v[206:209], v[82:85]
	v_mfma_f32_16x16x32_f16 v[70:73], v[174:177], v[214:217], v[70:73]
	v_mfma_f32_16x16x32_f16 v[66:69], v[182:185], v[214:217], v[66:69]
	v_mfma_f32_16x16x32_f16 v[118:121], v[178:181], v[194:197], v[118:121]
	v_mfma_f32_16x16x32_f16 v[114:117], v[186:189], v[194:197], v[114:117]
	v_mfma_f32_16x16x32_f16 v[102:105], v[178:181], v[202:205], v[102:105]
	v_mfma_f32_16x16x32_f16 v[98:101], v[186:189], v[202:205], v[98:101]
	v_mfma_f32_16x16x32_f16 v[86:89], v[178:181], v[210:213], v[86:89]
	v_mfma_f32_16x16x32_f16 v[82:85], v[186:189], v[210:213], v[82:85]
	v_mfma_f32_16x16x32_f16 v[70:73], v[178:181], v[218:221], v[70:73]
	v_mfma_f32_16x16x32_f16 v[66:69], v[186:189], v[218:221], v[66:69]
	s_barrier
	s_add_i32 s52, s45, s35
	s_mov_b32 m0, s52
	v_lshl_add_u64 v[150:151], s[28:29], 0, v[132:133]
	global_load_lds_dwordx4 v[150:151], off
	s_add_i32 m0, s52, 0x2000
	s_add_u32 s52, s28, 0x40000
	v_lshl_add_u64 v[222:223], s[28:29], 0, v[136:137]
	s_addc_u32 s53, s29, 0
	s_add_i32 s54, s46, s35
	global_load_lds_dwordx4 v[222:223], off
	v_lshl_add_u64 v[224:225], s[52:53], 0, v[132:133]
	s_mov_b32 m0, s54
	v_lshl_add_u64 v[226:227], s[30:31], 0, v[134:135]
	global_load_lds_dwordx4 v[224:225], off
	s_add_i32 m0, s54, 0x2000
	v_lshl_add_u64 v[224:225], s[52:53], 0, v[136:137]
	global_load_lds_dwordx4 v[224:225], off
	s_mov_b32 m0, s27
	v_lshl_add_u64 v[224:225], s[30:31], 0, v[130:131]
	global_load_lds_dwordx4 v[224:225], off
	s_mov_b32 m0, s36
	s_nop 0
	global_load_lds_dwordx4 v[226:227], off
	ds_read_b128 v[190:193], v160 offset:16384
	ds_read_b128 v[194:197], v160 offset:17408
	ds_read_b128 v[198:201], v160 offset:18432
	ds_read_b128 v[202:205], v160 offset:19456
	ds_read_b128 v[206:209], v160 offset:20480
	ds_read_b128 v[210:213], v160 offset:21504
	ds_read_b128 v[214:217], v160 offset:22528
	ds_read_b128 v[218:221], v160 offset:23552
	s_waitcnt vmcnt(8)
	s_waitcnt lgkmcnt(0)
	s_barrier
; #define GM_LDA(dst, b, h) do { _Pragma("unroll") for (int m = 0; m < 4; ++m) _Pragma("unroll") for (int k = 0; k < 2; ++k) dst[m][k] = *(const LAS s16x8*)(lds + GM_SA(b, h) + aoff + m * 2048 + k * 1024); } while (0)
; #define GM_LDB(dst, b, h) do { _Pragma("unroll") for (int n = 0; n < 2; ++n) _Pragma("unroll") for (int k = 0; k < 2; ++k) dst[n][k] = *(const LAS s16x8*)(lds + GM_SB(b, h) + boff + n * 2048 + k * 1024); } while (0)
; #define GM_MMA(ai, bj, At, Bt) do { __builtin_amdgcn_s_setprio(1); _Pragma("unroll") for (int m = 0; m < 4; ++m) _Pragma("unroll") for (int n = 0; n < 2; ++n) _Pragma("unroll") for (int k = 0; k < 2; ++k) \
;         acc[ai][bj][m][n] = mma16<BF>(Bt[n][k], At[m][k], acc[ai][bj][m][n]); __builtin_amdgcn_s_setprio(0); } while (0)
; #define GM_WAIT_V(n) asm volatile("s_waitcnt vmcnt(" #n ")" ::: "memory")
; #define GM_WAIT_L(n) asm volatile("s_waitcnt lgkmcnt(" #n ")" ::: "memory")
; #define GM_BAR __builtin_amdgcn_s_barrier()
; #define GM_SCHED __builtin_amdgcn_sched_barrier(0)
; #define GM_STA_H1(buf, p, o1) do { if constexpr (GATHER) GM_STAGE(buf, p, o1); else GM_STAGE(buf, (p) + hstepB, voffA); } while (0)
; template <bool BF, bool GATHER = false, class Epi, class Hook>
; __device__ __forceinline__ void gemm_phase(LAS unsigned char* lds, const Gemm g, const Order& S, const Epi& E, Hook& HK) {
;     ...
;             GM_WAIT_V(8); GM_WAIT_L(0); GM_BAR; GM_MMA(1, 0, At, B0); GM_MMA(1, 1, At, B1); GM_BAR; GM_SCHED;
;             GM_LDB(B0, 1, 0); GM_LDB(B1, 1, 1); GM_SCHED; GM_LDA(At, 1, 0); GM_STA_H1(GM_SA(0, 1), a2, s1);
;             GM_WAIT_V(8); GM_WAIT_L(0); GM_BAR; GM_MMA(0, 0, At, B0); GM_MMA(0, 1, At, B1); GM_BAR; GM_SCHED;
	v_mfma_f32_16x16x32_f16 v[62:65], v[146:149], v[190:193], v[62:65]
	v_mfma_f32_16x16x32_f16 v[58:61], v[166:169], v[190:193], v[58:61]
	v_mfma_f32_16x16x32_f16 v[46:49], v[146:149], v[198:201], v[46:49]
	v_mfma_f32_16x16x32_f16 v[42:45], v[166:169], v[198:201], v[42:45]
	v_mfma_f32_16x16x32_f16 v[30:33], v[146:149], v[206:209], v[30:33]
	v_mfma_f32_16x16x32_f16 v[26:29], v[166:169], v[206:209], v[26:29]
	v_mfma_f32_16x16x32_f16 v[14:17], v[146:149], v[214:217], v[14:17]
	v_mfma_f32_16x16x32_f16 v[10:13], v[166:169], v[214:217], v[10:13]
	v_mfma_f32_16x16x32_f16 v[62:65], v[162:165], v[194:197], v[62:65]
	v_mfma_f32_16x16x32_f16 v[58:61], v[170:173], v[194:197], v[58:61]
	v_mfma_f32_16x16x32_f16 v[46:49], v[162:165], v[202:205], v[46:49]
	v_mfma_f32_16x16x32_f16 v[42:45], v[170:173], v[202:205], v[42:45]
	v_mfma_f32_16x16x32_f16 v[30:33], v[162:165], v[210:213], v[30:33]
	v_mfma_f32_16x16x32_f16 v[26:29], v[170:173], v[210:213], v[26:29]
	v_mfma_f32_16x16x32_f16 v[14:17], v[162:165], v[218:221], v[14:17]
	v_mfma_f32_16x16x32_f16 v[10:13], v[170:173], v[218:221], v[10:13]
	v_mfma_f32_16x16x32_f16 v[54:57], v[174:177], v[190:193], v[54:57]
	v_mfma_f32_16x16x32_f16 v[50:53], v[182:185], v[190:193], v[50:53]
	v_mfma_f32_16x16x32_f16 v[38:41], v[174:177], v[198:201], v[38:41]
	v_mfma_f32_16x16x32_f16 v[34:37], v[182:185], v[198:201], v[34:37]
	v_mfma_f32_16x16x32_f16 v[22:25], v[174:177], v[206:209], v[22:25]
	v_mfma_f32_16x16x32_f16 v[18:21], v[182:185], v[206:209], v[18:21]
	v_mfma_f32_16x16x32_f16 v[6:9], v[174:177], v[214:217], v[6:9]
	v_mfma_f32_16x16x32_f16 v[2:5], v[182:185], v[214:217], v[2:5]
	v_mfma_f32_16x16x32_f16 v[54:57], v[178:181], v[194:197], v[54:57]
	v_mfma_f32_16x16x32_f16 v[50:53], v[186:189], v[194:197], v[50:53]
	v_mfma_f32_16x16x32_f16 v[38:41], v[178:181], v[202:205], v[38:41]
	v_mfma_f32_16x16x32_f16 v[34:37], v[186:189], v[202:205], v[34:37]
	v_mfma_f32_16x16x32_f16 v[22:25], v[178:181], v[210:213], v[22:25]
	v_mfma_f32_16x16x32_f16 v[18:21], v[186:189], v[210:213], v[18:21]
	v_mfma_f32_16x16x32_f16 v[6:9], v[178:181], v[218:221], v[6:9]
	v_mfma_f32_16x16x32_f16 v[2:5], v[186:189], v[218:221], v[2:5]
	s_barrier
	s_add_u32 s30, s30, 0x40000
	s_addc_u32 s31, s31, 0
	s_mov_b32 m0, s37
	v_lshl_add_u64 v[228:229], s[30:31], 0, v[130:131]
	global_load_lds_dwordx4 v[228:229], off
	s_mov_b32 m0, s38
	v_lshl_add_u64 v[228:229], s[30:31], 0, v[134:135]
	global_load_lds_dwordx4 v[228:229], off
	s_mov_b32 s53, 0x1c000
	s_mov_b32 s52, 0x18000
	v_add_u32_e32 v244, s52, v153
	v_add_u32_e32 v245, s53, v153
	ds_read_b128 v[146:149], v244
	ds_read_b128 v[162:165], v244 offset:1024
	ds_read_b128 v[166:169], v244 offset:2048
	ds_read_b128 v[170:173], v244 offset:3072
	ds_read_b128 v[174:177], v245
	ds_read_b128 v[178:181], v245 offset:1024
	ds_read_b128 v[182:185], v245 offset:2048
	ds_read_b128 v[186:189], v245 offset:3072
	ds_read_b128 v[190:193], v160 offset:32768
	ds_read_b128 v[194:197], v160 offset:33792
	ds_read_b128 v[198:201], v160 offset:34816
	ds_read_b128 v[202:205], v160 offset:35840
	ds_read_b128 v[206:209], v160 offset:36864
	ds_read_b128 v[210:213], v160 offset:37888
	ds_read_b128 v[214:217], v160 offset:38912
	ds_read_b128 v[218:221], v160 offset:39936
	s_waitcnt vmcnt(8)
	s_waitcnt lgkmcnt(0)
	s_barrier
	v_mfma_f32_16x16x32_f16 v[126:129], v[146:149], v[190:193], v[126:129]
	v_mfma_f32_16x16x32_f16 v[122:125], v[166:169], v[190:193], v[122:125]
	v_mfma_f32_16x16x32_f16 v[110:113], v[146:149], v[198:201], v[110:113]
	v_mfma_f32_16x16x32_f16 v[106:109], v[166:169], v[198:201], v[106:109]
	v_mfma_f32_16x16x32_f16 v[94:97], v[146:149], v[206:209], v[94:97]
	v_mfma_f32_16x16x32_f16 v[90:93], v[166:169], v[206:209], v[90:93]
	v_mfma_f32_16x16x32_f16 v[78:81], v[146:149], v[214:217], v[78:81]
	v_mfma_f32_16x16x32_f16 v[74:77], v[166:169], v[214:217], v[74:77]
	v_mfma_f32_16x16x32_f16 v[126:129], v[162:165], v[194:197], v[126:129]
	v_mfma_f32_16x16x32_f16 v[122:125], v[170:173], v[194:197], v[122:125]
	v_mfma_f32_16x16x32_f16 v[110:113], v[162:165], v[202:205], v[110:113]
	v_mfma_f32_16x16x32_f16 v[106:109], v[170:173], v[202:205], v[106:109]
	v_mfma_f32_16x16x32_f16 v[94:97], v[162:165], v[210:213], v[94:97]
	v_mfma_f32_16x16x32_f16 v[90:93], v[170:173], v[210:213], v[90:93]
	v_mfma_f32_16x16x32_f16 v[78:81], v[162:165], v[218:221], v[78:81]
	v_mfma_f32_16x16x32_f16 v[74:77], v[170:173], v[218:221], v[74:77]
	v_mfma_f32_16x16x32_f16 v[118:121], v[174:177], v[190:193], v[118:121]
	v_mfma_f32_16x16x32_f16 v[114:117], v[182:185], v[190:193], v[114:117]
	v_mfma_f32_16x16x32_f16 v[102:105], v[174:177], v[198:201], v[102:105]
	v_mfma_f32_16x16x32_f16 v[98:101], v[182:185], v[198:201], v[98:101]
	v_mfma_f32_16x16x32_f16 v[86:89], v[174:177], v[206:209], v[86:89]
	v_mfma_f32_16x16x32_f16 v[82:85], v[182:185], v[206:209], v[82:85]
	v_mfma_f32_16x16x32_f16 v[70:73], v[174:177], v[214:217], v[70:73]
	v_mfma_f32_16x16x32_f16 v[66:69], v[182:185], v[214:217], v[66:69]
	v_mfma_f32_16x16x32_f16 v[118:121], v[178:181], v[194:197], v[118:121]
	v_mfma_f32_16x16x32_f16 v[114:117], v[186:189], v[194:197], v[114:117]
	v_mfma_f32_16x16x32_f16 v[102:105], v[178:181], v[202:205], v[102:105]
	v_mfma_f32_16x16x32_f16 v[98:101], v[186:189], v[202:205], v[98:101]
	v_mfma_f32_16x16x32_f16 v[86:89], v[178:181], v[210:213], v[86:89]
	v_mfma_f32_16x16x32_f16 v[82:85], v[186:189], v[210:213], v[82:85]
	v_mfma_f32_16x16x32_f16 v[70:73], v[178:181], v[218:221], v[70:73]
	v_mfma_f32_16x16x32_f16 v[66:69], v[186:189], v[218:221], v[66:69]
	s_barrier
; #define GM_STAGE(bufoff, gbase, voff) do { _Pragma("unroll") for (int _i = 0; _i < 2; ++_i) \
;         __builtin_amdgcn_global_load_lds((const unsigned*)((const char*)(gbase) + (voff)[_i]), (LAS unsigned*)(lds + (bufoff) + ldsw + _i * 8192), 16, 0, 0); } while (0)
; #define GM_LDA(dst, b, h) do { _Pragma("unroll") for (int m = 0; m < 4; ++m) _Pragma("unroll") for (int k = 0; k < 2; ++k) dst[m][k] = *(const LAS s16x8*)(lds + GM_SA(b, h) + aoff + m * 2048 + k * 1024); } while (0)
; #define GM_MMA(ai, bj, At, Bt) do { __builtin_amdgcn_s_setprio(1); _Pragma("unroll") for (int m = 0; m < 4; ++m) _Pragma("unroll") for (int n = 0; n < 2; ++n) _Pragma("unroll") for (int k = 0; k < 2; ++k) \
;         acc[ai][bj][m][n] = mma16<BF>(Bt[n][k], At[m][k], acc[ai][bj][m][n]); __builtin_amdgcn_s_setprio(0); } while (0)
; #define GM_WAIT_V(n) asm volatile("s_waitcnt vmcnt(" #n ")" ::: "memory")
; #define GM_WAIT_L(n) asm volatile("s_waitcnt lgkmcnt(" #n ")" ::: "memory")
; #define GM_BAR __builtin_amdgcn_s_barrier()
; #define GM_SCHED __builtin_amdgcn_sched_barrier(0)
; #define GM_STA_H0(buf, p, o0) do { if constexpr (GATHER) GM_STAGE(buf, p, o0); else GM_STAGE(buf, p, voffA); } while (0)
; template <bool BF, bool GATHER = false, class Epi, class Hook>
; __device__ __forceinline__ void gemm_phase(LAS unsigned char* lds, const Gemm g, const Order& S, const Epi& E, Hook& HK) {
;     ...
;             GM_LDA(At, 1, 1); GM_STAGE(GM_SB(1, 0), b3, voffB); GM_STAGE(GM_SB(1, 1), b3 + hstepB, voffB); GM_STA_H0(GM_SA(1, 0), a3, s0);
;             GM_WAIT_V(8); GM_WAIT_L(0); GM_BAR; GM_MMA(1, 0, At, B0); GM_MMA(1, 1, At, B1); GM_BAR; GM_SCHED;
;         }
;         if (wr == 0) GM_BAR;
	s_add_i32 s30, s52, s35
	s_mov_b32 m0, s30
	v_lshl_add_u64 v[150:151], v[150:151], 0, s[14:15]
	global_load_lds_dwordx4 v[150:151], off
	s_add_i32 m0, s30, 0x2000
	s_add_u32 s28, s28, 0x40080
	v_lshl_add_u64 v[150:151], v[222:223], 0, s[14:15]
	s_addc_u32 s29, s29, 0
	s_add_i32 s30, s53, s35
	global_load_lds_dwordx4 v[150:151], off
	s_mov_b32 m0, s30
	v_lshl_add_u64 v[150:151], s[28:29], 0, v[132:133]
	global_load_lds_dwordx4 v[150:151], off
	s_add_i32 m0, s30, 0x2000
	v_lshl_add_u64 v[150:151], s[28:29], 0, v[136:137]
	global_load_lds_dwordx4 v[150:151], off
	s_mov_b32 m0, s42
	v_lshl_add_u64 v[150:151], v[224:225], 0, s[14:15]
	global_load_lds_dwordx4 v[150:151], off
	s_mov_b32 m0, s43
	v_lshl_add_u64 v[150:151], v[226:227], 0, s[14:15]
	global_load_lds_dwordx4 v[150:151], off
	ds_read_b128 v[190:193], v160 offset:49152
	ds_read_b128 v[194:197], v160 offset:50176
	ds_read_b128 v[198:201], v160 offset:51200
	ds_read_b128 v[202:205], v160 offset:52224
	ds_read_b128 v[206:209], v160 offset:53248
	ds_read_b128 v[210:213], v160 offset:54272
	ds_read_b128 v[214:217], v160 offset:55296
	ds_read_b128 v[218:221], v160 offset:56320
	s_waitcnt vmcnt(8)
	s_waitcnt lgkmcnt(0)
	s_barrier
	v_mfma_f32_16x16x32_f16 v[62:65], v[146:149], v[190:193], v[62:65]
	v_mfma_f32_16x16x32_f16 v[58:61], v[166:169], v[190:193], v[58:61]
	v_mfma_f32_16x16x32_f16 v[46:49], v[146:149], v[198:201], v[46:49]
	v_mfma_f32_16x16x32_f16 v[42:45], v[166:169], v[198:201], v[42:45]
	v_mfma_f32_16x16x32_f16 v[30:33], v[146:149], v[206:209], v[30:33]
	v_mfma_f32_16x16x32_f16 v[26:29], v[166:169], v[206:209], v[26:29]
	v_mfma_f32_16x16x32_f16 v[14:17], v[146:149], v[214:217], v[14:17]
	v_mfma_f32_16x16x32_f16 v[10:13], v[166:169], v[214:217], v[10:13]
	v_mfma_f32_16x16x32_f16 v[62:65], v[162:165], v[194:197], v[62:65]
	v_mfma_f32_16x16x32_f16 v[58:61], v[170:173], v[194:197], v[58:61]
	v_mfma_f32_16x16x32_f16 v[46:49], v[162:165], v[202:205], v[46:49]
	v_mfma_f32_16x16x32_f16 v[42:45], v[170:173], v[202:205], v[42:45]
	v_mfma_f32_16x16x32_f16 v[30:33], v[162:165], v[210:213], v[30:33]
	v_mfma_f32_16x16x32_f16 v[26:29], v[170:173], v[210:213], v[26:29]
	v_mfma_f32_16x16x32_f16 v[14:17], v[162:165], v[218:221], v[14:17]
	v_mfma_f32_16x16x32_f16 v[10:13], v[170:173], v[218:221], v[10:13]
	v_mfma_f32_16x16x32_f16 v[54:57], v[174:177], v[190:193], v[54:57]
	v_mfma_f32_16x16x32_f16 v[50:53], v[182:185], v[190:193], v[50:53]
	v_mfma_f32_16x16x32_f16 v[38:41], v[174:177], v[198:201], v[38:41]
	v_mfma_f32_16x16x32_f16 v[34:37], v[182:185], v[198:201], v[34:37]
	v_mfma_f32_16x16x32_f16 v[22:25], v[174:177], v[206:209], v[22:25]
	v_mfma_f32_16x16x32_f16 v[18:21], v[182:185], v[206:209], v[18:21]
	v_mfma_f32_16x16x32_f16 v[6:9], v[174:177], v[214:217], v[6:9]
	v_mfma_f32_16x16x32_f16 v[2:5], v[182:185], v[214:217], v[2:5]
	v_mfma_f32_16x16x32_f16 v[54:57], v[178:181], v[194:197], v[54:57]
	v_mfma_f32_16x16x32_f16 v[50:53], v[186:189], v[194:197], v[50:53]
	v_mfma_f32_16x16x32_f16 v[38:41], v[178:181], v[202:205], v[38:41]
	v_mfma_f32_16x16x32_f16 v[34:37], v[186:189], v[202:205], v[34:37]
	v_mfma_f32_16x16x32_f16 v[22:25], v[178:181], v[210:213], v[22:25]
	v_mfma_f32_16x16x32_f16 v[18:21], v[186:189], v[210:213], v[18:21]
	v_mfma_f32_16x16x32_f16 v[6:9], v[178:181], v[218:221], v[6:9]
	v_mfma_f32_16x16x32_f16 v[2:5], v[186:189], v[218:221], v[2:5]
	s_barrier
	s_add_i32 s51, s51, 2
	s_add_u32 s2, s2, 0x100
	s_addc_u32 s3, s3, 0
	s_add_u32 s49, s49, 0x100
	s_addc_u32 s50, s50, 0
	s_cmp_gt_u32 s51, 13
	s_cbranch_scc0 .LBB0_380
	s_and_b64 vcc, exec, s[16:17]
	s_cbranch_vccz .LBB0_383
	s_barrier

; #define GM_STAGE(bufoff, gbase, voff) do { _Pragma("unroll") for (int _i = 0; _i < 2; ++_i) \
;         __builtin_amdgcn_global_load_lds((const unsigned*)((const char*)(gbase) + (voff)[_i]), (LAS unsigned*)(lds + (bufoff) + ldsw + _i * 8192), 16, 0, 0); } while (0)
; #define GM_LDA(dst, b, h) do { _Pragma("unroll") for (int m = 0; m < 4; ++m) _Pragma("unroll") for (int k = 0; k < 2; ++k) dst[m][k] = *(const LAS s16x8*)(lds + GM_SA(b, h) + aoff + m * 2048 + k * 1024); } while (0)
; #define GM_LDB(dst, b, h) do { _Pragma("unroll") for (int n = 0; n < 2; ++n) _Pragma("unroll") for (int k = 0; k < 2; ++k) dst[n][k] = *(const LAS s16x8*)(lds + GM_SB(b, h) + boff + n * 2048 + k * 1024); } while (0)
; #define GM_MMA(ai, bj, At, Bt) do { __builtin_amdgcn_s_setprio(1); _Pragma("unroll") for (int m = 0; m < 4; ++m) _Pragma("unroll") for (int n = 0; n < 2; ++n) _Pragma("unroll") for (int k = 0; k < 2; ++k) \
;         acc[ai][bj][m][n] = mma16<BF>(Bt[n][k], At[m][k], acc[ai][bj][m][n]); __builtin_amdgcn_s_setprio(0); } while (0)
; #define GM_WAIT_V(n) asm volatile("s_waitcnt vmcnt(" #n ")" ::: "memory")
; #define GM_WAIT_L(n) asm volatile("s_waitcnt lgkmcnt(" #n ")" ::: "memory")
; #define GM_BAR __builtin_amdgcn_s_barrier()
; template <bool BF, bool GATHER = false, class Epi, class Hook>
; __device__ __forceinline__ void gemm_phase(LAS unsigned char* lds, const Gemm g, const Order& S, const Epi& E, Hook& HK) {
;     ...
;         for (int t = 0; t < nt; t += 2) {
;             const bool last = (t == nt - 2);
;             const char* a1 = cA + (size_t)(t + 1) * kstep;
;             const char* a2 = last ? nA : cA + (size_t)(t + 2) * kstep; const char* b2 = last ? nB : cB + (size_t)(t + 2) * kstep;
;             const char* a3 = a2 + kstep; const char* b3 = b2 + kstep;
;             unsigned s0[2], s1[2];
;             if constexpr (GATHER) { s0[0] = last ? nA0[0] : gA0[0]; s0[1] = last ? nA0[1] : gA0[1]; s1[0] = last ? nA1[0] : gA1[0]; s1[1] = last ? nA1[1] : gA1[1]; }
;             GM_LDB(B0, 0, 0); GM_LDB(B1, 0, 1); GM_SCHED; GM_LDA(At, 0, 0); GM_STA_H1(GM_SA(1, 1), a1, gA1);
;             GM_WAIT_V(8); GM_WAIT_L(0); GM_BAR; GM_MMA(0, 0, At, B0); GM_MMA(0, 1, At, B1); GM_BAR; GM_SCHED;
;             GM_LDA(At, 0, 1); GM_STAGE(GM_SB(0, 0), b2, voffB); GM_STAGE(GM_SB(0, 1), b2 + hstepB, voffB); GM_STA_H0(GM_SA(0, 0), a2, s0);
.LBB0_715:
	s_add_u32 s22, s20, 0xfffc0080
	s_addc_u32 s23, s21, -1
	s_cmp_eq_u32 s47, 12
	s_cselect_b32 s25, s13, s23
	s_cselect_b32 s24, s43, s22
	s_cselect_b32 s23, s15, s46
	s_cselect_b32 s22, s44, s45
	s_add_i32 m0, s30, 0xc000
	v_lshl_add_u64 v[216:217], s[20:21], 0, v[154:155]
	global_load_lds_dwordx4 v[216:217], off
	s_add_i32 m0, s30, 0xe000
	v_lshl_add_u64 v[216:217], s[20:21], 0, v[156:157]
	global_load_lds_dwordx4 v[216:217], off
	ds_read_b128 v[130:133], v168
	ds_read_b128 v[134:137], v168 offset:1024
	ds_read_b128 v[138:141], v168 offset:2048
	ds_read_b128 v[142:145], v168 offset:3072
	ds_read_b128 v[162:165], v169
	ds_read_b128 v[172:175], v169 offset:1024
	ds_read_b128 v[176:179], v169 offset:2048
	ds_read_b128 v[180:183], v169 offset:3072
	ds_read_b128 v[184:187], v170
	ds_read_b128 v[188:191], v170 offset:1024
	ds_read_b128 v[192:195], v170 offset:2048
	ds_read_b128 v[196:199], v170 offset:3072
	ds_read_b128 v[200:203], v170 offset:4096
	ds_read_b128 v[204:207], v170 offset:5120
	ds_read_b128 v[208:211], v170 offset:6144
	ds_read_b128 v[212:215], v170 offset:7168
	s_waitcnt vmcnt(8)
	s_waitcnt lgkmcnt(0)
	s_barrier
	v_mfma_f32_16x16x32_f16 v[126:129], v[130:133], v[184:187], v[126:129]
	v_mfma_f32_16x16x32_f16 v[122:125], v[138:141], v[184:187], v[122:125]
	v_mfma_f32_16x16x32_f16 v[110:113], v[130:133], v[192:195], v[110:113]
	v_mfma_f32_16x16x32_f16 v[106:109], v[138:141], v[192:195], v[106:109]
	v_mfma_f32_16x16x32_f16 v[94:97], v[130:133], v[200:203], v[94:97]
	v_mfma_f32_16x16x32_f16 v[90:93], v[138:141], v[200:203], v[90:93]
	v_mfma_f32_16x16x32_f16 v[78:81], v[130:133], v[208:211], v[78:81]
	v_mfma_f32_16x16x32_f16 v[74:77], v[138:141], v[208:211], v[74:77]
	v_mfma_f32_16x16x32_f16 v[126:129], v[134:137], v[188:191], v[126:129]
	v_mfma_f32_16x16x32_f16 v[122:125], v[142:145], v[188:191], v[122:125]
	v_mfma_f32_16x16x32_f16 v[110:113], v[134:137], v[196:199], v[110:113]
	v_mfma_f32_16x16x32_f16 v[106:109], v[142:145], v[196:199], v[106:109]
	v_mfma_f32_16x16x32_f16 v[94:97], v[134:137], v[204:207], v[94:97]
	v_mfma_f32_16x16x32_f16 v[90:93], v[142:145], v[204:207], v[90:93]
	v_mfma_f32_16x16x32_f16 v[78:81], v[134:137], v[212:215], v[78:81]
	v_mfma_f32_16x16x32_f16 v[74:77], v[142:145], v[212:215], v[74:77]
	v_mfma_f32_16x16x32_f16 v[118:121], v[162:165], v[184:187], v[118:121]
	v_mfma_f32_16x16x32_f16 v[114:117], v[176:179], v[184:187], v[114:117]
	v_mfma_f32_16x16x32_f16 v[102:105], v[162:165], v[192:195], v[102:105]
	v_mfma_f32_16x16x32_f16 v[98:101], v[176:179], v[192:195], v[98:101]
	v_mfma_f32_16x16x32_f16 v[86:89], v[162:165], v[200:203], v[86:89]
	v_mfma_f32_16x16x32_f16 v[82:85], v[176:179], v[200:203], v[82:85]
	v_mfma_f32_16x16x32_f16 v[70:73], v[162:165], v[208:211], v[70:73]
	v_mfma_f32_16x16x32_f16 v[66:69], v[176:179], v[208:211], v[66:69]
	v_mfma_f32_16x16x32_f16 v[118:121], v[172:175], v[188:191], v[118:121]
	v_mfma_f32_16x16x32_f16 v[114:117], v[180:183], v[188:191], v[114:117]
	v_mfma_f32_16x16x32_f16 v[102:105], v[172:175], v[196:199], v[102:105]
	v_mfma_f32_16x16x32_f16 v[98:101], v[180:183], v[196:199], v[98:101]
	v_mfma_f32_16x16x32_f16 v[86:89], v[172:175], v[204:207], v[86:89]
	v_mfma_f32_16x16x32_f16 v[82:85], v[180:183], v[204:207], v[82:85]
	v_mfma_f32_16x16x32_f16 v[70:73], v[172:175], v[212:215], v[70:73]
	v_mfma_f32_16x16x32_f16 v[66:69], v[180:183], v[212:215], v[66:69]
	s_barrier
	s_add_i32 s48, s41, s29
	s_mov_b32 m0, s48
	v_lshl_add_u64 v[216:217], s[22:23], 0, v[148:149]
	global_load_lds_dwordx4 v[216:217], off
	s_add_i32 m0, s48, 0x2000
	s_add_u32 s48, s22, 0x40000
	v_lshl_add_u64 v[218:219], s[22:23], 0, v[152:153]
	s_addc_u32 s49, s23, 0
	s_add_i32 s50, s42, s29
	global_load_lds_dwordx4 v[218:219], off
	v_lshl_add_u64 v[220:221], s[48:49], 0, v[148:149]
	s_mov_b32 m0, s50
	v_lshl_add_u64 v[222:223], s[24:25], 0, v[150:151]
	global_load_lds_dwordx4 v[220:221], off
	s_add_i32 m0, s50, 0x2000
	v_lshl_add_u64 v[220:221], s[48:49], 0, v[152:153]
	global_load_lds_dwordx4 v[220:221], off
	s_mov_b32 m0, s30
	v_lshl_add_u64 v[220:221], s[24:25], 0, v[146:147]
	global_load_lds_dwordx4 v[220:221], off
	s_mov_b32 m0, s31
	s_nop 0
	global_load_lds_dwordx4 v[222:223], off
	ds_read_b128 v[184:187], v170 offset:16384
	ds_read_b128 v[188:191], v170 offset:17408
	ds_read_b128 v[192:195], v170 offset:18432
	ds_read_b128 v[196:199], v170 offset:19456
	ds_read_b128 v[200:203], v170 offset:20480
	ds_read_b128 v[204:207], v170 offset:21504
	ds_read_b128 v[208:211], v170 offset:22528
	ds_read_b128 v[212:215], v170 offset:23552
	s_waitcnt vmcnt(8)
	s_waitcnt lgkmcnt(0)
	s_barrier
; #define GM_LDA(dst, b, h) do { _Pragma("unroll") for (int m = 0; m < 4; ++m) _Pragma("unroll") for (int k = 0; k < 2; ++k) dst[m][k] = *(const LAS s16x8*)(lds + GM_SA(b, h) + aoff + m * 2048 + k * 1024); } while (0)
; #define GM_LDB(dst, b, h) do { _Pragma("unroll") for (int n = 0; n < 2; ++n) _Pragma("unroll") for (int k = 0; k < 2; ++k) dst[n][k] = *(const LAS s16x8*)(lds + GM_SB(b, h) + boff + n * 2048 + k * 1024); } while (0)
; #define GM_MMA(ai, bj, At, Bt) do { __builtin_amdgcn_s_setprio(1); _Pragma("unroll") for (int m = 0; m < 4; ++m) _Pragma("unroll") for (int n = 0; n < 2; ++n) _Pragma("unroll") for (int k = 0; k < 2; ++k) \
;         acc[ai][bj][m][n] = mma16<BF>(Bt[n][k], At[m][k], acc[ai][bj][m][n]); __builtin_amdgcn_s_setprio(0); } while (0)
; #define GM_WAIT_V(n) asm volatile("s_waitcnt vmcnt(" #n ")" ::: "memory")
; #define GM_WAIT_L(n) asm volatile("s_waitcnt lgkmcnt(" #n ")" ::: "memory")
; #define GM_BAR __builtin_amdgcn_s_barrier()
; #define GM_SCHED __builtin_amdgcn_sched_barrier(0)
; #define GM_STA_H1(buf, p, o1) do { if constexpr (GATHER) GM_STAGE(buf, p, o1); else GM_STAGE(buf, (p) + hstepB, voffA); } while (0)
; template <bool BF, bool GATHER = false, class Epi, class Hook>
; __device__ __forceinline__ void gemm_phase(LAS unsigned char* lds, const Gemm g, const Order& S, const Epi& E, Hook& HK) {
;     ...
;             GM_WAIT_V(8); GM_WAIT_L(0); GM_BAR; GM_MMA(1, 0, At, B0); GM_MMA(1, 1, At, B1); GM_BAR; GM_SCHED;
;             GM_LDB(B0, 1, 0); GM_LDB(B1, 1, 1); GM_SCHED; GM_LDA(At, 1, 0); GM_STA_H1(GM_SA(0, 1), a2, s1);
;             GM_WAIT_V(8); GM_WAIT_L(0); GM_BAR; GM_MMA(0, 0, At, B0); GM_MMA(0, 1, At, B1); GM_BAR; GM_SCHED;
	v_mfma_f32_16x16x32_f16 v[62:65], v[130:133], v[184:187], v[62:65]
	v_mfma_f32_16x16x32_f16 v[58:61], v[138:141], v[184:187], v[58:61]
	v_mfma_f32_16x16x32_f16 v[46:49], v[130:133], v[192:195], v[46:49]
	v_mfma_f32_16x16x32_f16 v[42:45], v[138:141], v[192:195], v[42:45]
	v_mfma_f32_16x16x32_f16 v[30:33], v[130:133], v[200:203], v[30:33]
	v_mfma_f32_16x16x32_f16 v[26:29], v[138:141], v[200:203], v[26:29]
	v_mfma_f32_16x16x32_f16 v[14:17], v[130:133], v[208:211], v[14:17]
	v_mfma_f32_16x16x32_f16 v[10:13], v[138:141], v[208:211], v[10:13]
	v_mfma_f32_16x16x32_f16 v[62:65], v[134:137], v[188:191], v[62:65]
	v_mfma_f32_16x16x32_f16 v[58:61], v[142:145], v[188:191], v[58:61]
	v_mfma_f32_16x16x32_f16 v[46:49], v[134:137], v[196:199], v[46:49]
	v_mfma_f32_16x16x32_f16 v[42:45], v[142:145], v[196:199], v[42:45]
	v_mfma_f32_16x16x32_f16 v[30:33], v[134:137], v[204:207], v[30:33]
	v_mfma_f32_16x16x32_f16 v[26:29], v[142:145], v[204:207], v[26:29]
	v_mfma_f32_16x16x32_f16 v[14:17], v[134:137], v[212:215], v[14:17]
	v_mfma_f32_16x16x32_f16 v[10:13], v[142:145], v[212:215], v[10:13]
	v_mfma_f32_16x16x32_f16 v[54:57], v[162:165], v[184:187], v[54:57]
	v_mfma_f32_16x16x32_f16 v[50:53], v[176:179], v[184:187], v[50:53]
	v_mfma_f32_16x16x32_f16 v[38:41], v[162:165], v[192:195], v[38:41]
	v_mfma_f32_16x16x32_f16 v[34:37], v[176:179], v[192:195], v[34:37]
	v_mfma_f32_16x16x32_f16 v[22:25], v[162:165], v[200:203], v[22:25]
	v_mfma_f32_16x16x32_f16 v[18:21], v[176:179], v[200:203], v[18:21]
	v_mfma_f32_16x16x32_f16 v[6:9], v[162:165], v[208:211], v[6:9]
	v_mfma_f32_16x16x32_f16 v[2:5], v[176:179], v[208:211], v[2:5]
	v_mfma_f32_16x16x32_f16 v[54:57], v[172:175], v[188:191], v[54:57]
	v_mfma_f32_16x16x32_f16 v[50:53], v[180:183], v[188:191], v[50:53]
	v_mfma_f32_16x16x32_f16 v[38:41], v[172:175], v[196:199], v[38:41]
	v_mfma_f32_16x16x32_f16 v[34:37], v[180:183], v[196:199], v[34:37]
	v_mfma_f32_16x16x32_f16 v[22:25], v[172:175], v[204:207], v[22:25]
	v_mfma_f32_16x16x32_f16 v[18:21], v[180:183], v[204:207], v[18:21]
	v_mfma_f32_16x16x32_f16 v[6:9], v[172:175], v[212:215], v[6:9]
	v_mfma_f32_16x16x32_f16 v[2:5], v[180:183], v[212:215], v[2:5]
	s_barrier
	s_add_u32 s24, s24, 0x40000
	s_addc_u32 s25, s25, 0
	s_mov_b32 m0, s33
	v_lshl_add_u64 v[224:225], s[24:25], 0, v[146:147]
	global_load_lds_dwordx4 v[224:225], off
	s_mov_b32 m0, s34
	v_lshl_add_u64 v[224:225], s[24:25], 0, v[150:151]
	global_load_lds_dwordx4 v[224:225], off
	s_mov_b32 s49, 0x1c000
	s_mov_b32 s48, 0x18000
	v_add_u32_e32 v244, s48, v166
	v_add_u32_e32 v245, s49, v166
	ds_read_b128 v[130:133], v244
	ds_read_b128 v[134:137], v244 offset:1024
	ds_read_b128 v[138:141], v244 offset:2048
	ds_read_b128 v[142:145], v244 offset:3072
	ds_read_b128 v[162:165], v245
	ds_read_b128 v[172:175], v245 offset:1024
	ds_read_b128 v[176:179], v245 offset:2048
	ds_read_b128 v[180:183], v245 offset:3072
	ds_read_b128 v[184:187], v170 offset:32768
	ds_read_b128 v[188:191], v170 offset:33792
	ds_read_b128 v[192:195], v170 offset:34816
	ds_read_b128 v[196:199], v170 offset:35840
	ds_read_b128 v[200:203], v170 offset:36864
	ds_read_b128 v[204:207], v170 offset:37888
	ds_read_b128 v[208:211], v170 offset:38912
	ds_read_b128 v[212:215], v170 offset:39936
	s_waitcnt vmcnt(8)
	s_waitcnt lgkmcnt(0)
	s_barrier
	v_mfma_f32_16x16x32_f16 v[126:129], v[130:133], v[184:187], v[126:129]
	v_mfma_f32_16x16x32_f16 v[122:125], v[138:141], v[184:187], v[122:125]
	v_mfma_f32_16x16x32_f16 v[110:113], v[130:133], v[192:195], v[110:113]
	v_mfma_f32_16x16x32_f16 v[106:109], v[138:141], v[192:195], v[106:109]
	v_mfma_f32_16x16x32_f16 v[94:97], v[130:133], v[200:203], v[94:97]
	v_mfma_f32_16x16x32_f16 v[90:93], v[138:141], v[200:203], v[90:93]
	v_mfma_f32_16x16x32_f16 v[78:81], v[130:133], v[208:211], v[78:81]
	v_mfma_f32_16x16x32_f16 v[74:77], v[138:141], v[208:211], v[74:77]
	v_mfma_f32_16x16x32_f16 v[126:129], v[134:137], v[188:191], v[126:129]
	v_mfma_f32_16x16x32_f16 v[122:125], v[142:145], v[188:191], v[122:125]
	v_mfma_f32_16x16x32_f16 v[110:113], v[134:137], v[196:199], v[110:113]
	v_mfma_f32_16x16x32_f16 v[106:109], v[142:145], v[196:199], v[106:109]
	v_mfma_f32_16x16x32_f16 v[94:97], v[134:137], v[204:207], v[94:97]
	v_mfma_f32_16x16x32_f16 v[90:93], v[142:145], v[204:207], v[90:93]
	v_mfma_f32_16x16x32_f16 v[78:81], v[134:137], v[212:215], v[78:81]
	v_mfma_f32_16x16x32_f16 v[74:77], v[142:145], v[212:215], v[74:77]
	v_mfma_f32_16x16x32_f16 v[118:121], v[162:165], v[184:187], v[118:121]
	v_mfma_f32_16x16x32_f16 v[114:117], v[176:179], v[184:187], v[114:117]
	v_mfma_f32_16x16x32_f16 v[102:105], v[162:165], v[192:195], v[102:105]
	v_mfma_f32_16x16x32_f16 v[98:101], v[176:179], v[192:195], v[98:101]
	v_mfma_f32_16x16x32_f16 v[86:89], v[162:165], v[200:203], v[86:89]
	v_mfma_f32_16x16x32_f16 v[82:85], v[176:179], v[200:203], v[82:85]
	v_mfma_f32_16x16x32_f16 v[70:73], v[162:165], v[208:211], v[70:73]
	v_mfma_f32_16x16x32_f16 v[66:69], v[176:179], v[208:211], v[66:69]
	v_mfma_f32_16x16x32_f16 v[118:121], v[172:175], v[188:191], v[118:121]
	v_mfma_f32_16x16x32_f16 v[114:117], v[180:183], v[188:191], v[114:117]
	v_mfma_f32_16x16x32_f16 v[102:105], v[172:175], v[196:199], v[102:105]
	v_mfma_f32_16x16x32_f16 v[98:101], v[180:183], v[196:199], v[98:101]
	v_mfma_f32_16x16x32_f16 v[86:89], v[172:175], v[204:207], v[86:89]
	v_mfma_f32_16x16x32_f16 v[82:85], v[180:183], v[204:207], v[82:85]
	v_mfma_f32_16x16x32_f16 v[70:73], v[172:175], v[212:215], v[70:73]
	v_mfma_f32_16x16x32_f16 v[66:69], v[180:183], v[212:215], v[66:69]
	s_barrier
; #define GM_STAGE(bufoff, gbase, voff) do { _Pragma("unroll") for (int _i = 0; _i < 2; ++_i) \
;         __builtin_amdgcn_global_load_lds((const unsigned*)((const char*)(gbase) + (voff)[_i]), (LAS unsigned*)(lds + (bufoff) + ldsw + _i * 8192), 16, 0, 0); } while (0)
; #define GM_LDA(dst, b, h) do { _Pragma("unroll") for (int m = 0; m < 4; ++m) _Pragma("unroll") for (int k = 0; k < 2; ++k) dst[m][k] = *(const LAS s16x8*)(lds + GM_SA(b, h) + aoff + m * 2048 + k * 1024); } while (0)
; #define GM_MMA(ai, bj, At, Bt) do { __builtin_amdgcn_s_setprio(1); _Pragma("unroll") for (int m = 0; m < 4; ++m) _Pragma("unroll") for (int n = 0; n < 2; ++n) _Pragma("unroll") for (int k = 0; k < 2; ++k) \
;         acc[ai][bj][m][n] = mma16<BF>(Bt[n][k], At[m][k], acc[ai][bj][m][n]); __builtin_amdgcn_s_setprio(0); } while (0)
; #define GM_WAIT_V(n) asm volatile("s_waitcnt vmcnt(" #n ")" ::: "memory")
; #define GM_WAIT_L(n) asm volatile("s_waitcnt lgkmcnt(" #n ")" ::: "memory")
; #define GM_BAR __builtin_amdgcn_s_barrier()
; #define GM_SCHED __builtin_amdgcn_sched_barrier(0)
; #define GM_STA_H0(buf, p, o0) do { if constexpr (GATHER) GM_STAGE(buf, p, o0); else GM_STAGE(buf, p, voffA); } while (0)
; template <bool BF, bool GATHER = false, class Epi, class Hook>
; __device__ __forceinline__ void gemm_phase(LAS unsigned char* lds, const Gemm g, const Order& S, const Epi& E, Hook& HK) {
;     ...
;             GM_LDA(At, 1, 1); GM_STAGE(GM_SB(1, 0), b3, voffB); GM_STAGE(GM_SB(1, 1), b3 + hstepB, voffB); GM_STA_H0(GM_SA(1, 0), a3, s0);
;             GM_WAIT_V(8); GM_WAIT_L(0); GM_BAR; GM_MMA(1, 0, At, B0); GM_MMA(1, 1, At, B1); GM_BAR; GM_SCHED;
;         }
;         if (wr == 0) GM_BAR;
	s_add_i32 s24, s48, s29
	s_mov_b32 m0, s24
	v_lshl_add_u64 v[216:217], v[216:217], 0, s[8:9]
	global_load_lds_dwordx4 v[216:217], off
	s_add_i32 m0, s24, 0x2000
	s_add_u32 s22, s22, 0x40080
	v_lshl_add_u64 v[216:217], v[218:219], 0, s[8:9]
	s_addc_u32 s23, s23, 0
	s_add_i32 s24, s49, s29
	global_load_lds_dwordx4 v[216:217], off
	s_mov_b32 m0, s24
	v_lshl_add_u64 v[216:217], s[22:23], 0, v[148:149]
	global_load_lds_dwordx4 v[216:217], off
	s_add_i32 m0, s24, 0x2000
	v_lshl_add_u64 v[216:217], s[22:23], 0, v[152:153]
	global_load_lds_dwordx4 v[216:217], off
	s_mov_b32 m0, s38
	v_lshl_add_u64 v[216:217], v[220:221], 0, s[8:9]
	global_load_lds_dwordx4 v[216:217], off
	s_mov_b32 m0, s39
	v_lshl_add_u64 v[216:217], v[222:223], 0, s[8:9]
	global_load_lds_dwordx4 v[216:217], off
	ds_read_b128 v[184:187], v170 offset:49152
	ds_read_b128 v[188:191], v170 offset:50176
	ds_read_b128 v[192:195], v170 offset:51200
	ds_read_b128 v[196:199], v170 offset:52224
	ds_read_b128 v[200:203], v170 offset:53248
	ds_read_b128 v[204:207], v170 offset:54272
	ds_read_b128 v[208:211], v170 offset:55296
	ds_read_b128 v[212:215], v170 offset:56320
	s_waitcnt vmcnt(8)
	s_waitcnt lgkmcnt(0)
	s_barrier
	v_mfma_f32_16x16x32_f16 v[62:65], v[130:133], v[184:187], v[62:65]
	v_mfma_f32_16x16x32_f16 v[58:61], v[138:141], v[184:187], v[58:61]
	v_mfma_f32_16x16x32_f16 v[46:49], v[130:133], v[192:195], v[46:49]
	v_mfma_f32_16x16x32_f16 v[42:45], v[138:141], v[192:195], v[42:45]
	v_mfma_f32_16x16x32_f16 v[30:33], v[130:133], v[200:203], v[30:33]
	v_mfma_f32_16x16x32_f16 v[26:29], v[138:141], v[200:203], v[26:29]
	v_mfma_f32_16x16x32_f16 v[14:17], v[130:133], v[208:211], v[14:17]
	v_mfma_f32_16x16x32_f16 v[10:13], v[138:141], v[208:211], v[10:13]
	v_mfma_f32_16x16x32_f16 v[62:65], v[134:137], v[188:191], v[62:65]
	v_mfma_f32_16x16x32_f16 v[58:61], v[142:145], v[188:191], v[58:61]
	v_mfma_f32_16x16x32_f16 v[46:49], v[134:137], v[196:199], v[46:49]
	v_mfma_f32_16x16x32_f16 v[42:45], v[142:145], v[196:199], v[42:45]
	v_mfma_f32_16x16x32_f16 v[30:33], v[134:137], v[204:207], v[30:33]
	v_mfma_f32_16x16x32_f16 v[26:29], v[142:145], v[204:207], v[26:29]
	v_mfma_f32_16x16x32_f16 v[14:17], v[134:137], v[212:215], v[14:17]
	v_mfma_f32_16x16x32_f16 v[10:13], v[142:145], v[212:215], v[10:13]
	v_mfma_f32_16x16x32_f16 v[54:57], v[162:165], v[184:187], v[54:57]
	v_mfma_f32_16x16x32_f16 v[50:53], v[176:179], v[184:187], v[50:53]
	v_mfma_f32_16x16x32_f16 v[38:41], v[162:165], v[192:195], v[38:41]
	v_mfma_f32_16x16x32_f16 v[34:37], v[176:179], v[192:195], v[34:37]
	v_mfma_f32_16x16x32_f16 v[22:25], v[162:165], v[200:203], v[22:25]
	v_mfma_f32_16x16x32_f16 v[18:21], v[176:179], v[200:203], v[18:21]
	v_mfma_f32_16x16x32_f16 v[6:9], v[162:165], v[208:211], v[6:9]
	v_mfma_f32_16x16x32_f16 v[2:5], v[176:179], v[208:211], v[2:5]
	v_mfma_f32_16x16x32_f16 v[54:57], v[172:175], v[188:191], v[54:57]
	v_mfma_f32_16x16x32_f16 v[50:53], v[180:183], v[188:191], v[50:53]
	v_mfma_f32_16x16x32_f16 v[38:41], v[172:175], v[196:199], v[38:41]
	v_mfma_f32_16x16x32_f16 v[34:37], v[180:183], v[196:199], v[34:37]
	v_mfma_f32_16x16x32_f16 v[22:25], v[172:175], v[204:207], v[22:25]
	v_mfma_f32_16x16x32_f16 v[18:21], v[180:183], v[204:207], v[18:21]
	v_mfma_f32_16x16x32_f16 v[6:9], v[172:175], v[212:215], v[6:9]
	v_mfma_f32_16x16x32_f16 v[2:5], v[180:183], v[212:215], v[2:5]
	s_barrier
	s_add_i32 s47, s47, 2
	s_add_u32 s20, s20, 0x100
	s_addc_u32 s21, s21, 0
	s_add_u32 s45, s45, 0x100
	s_addc_u32 s46, s46, 0
	s_cmp_gt_u32 s47, 13
	s_cbranch_scc0 .LBB0_715
	s_and_b64 vcc, exec, s[10:11]
	s_cbranch_vccz .LBB0_718
	s_barrier

; #define GM_STAGE(bufoff, gbase, voff) do { _Pragma("unroll") for (int _i = 0; _i < 2; ++_i) \
;         __builtin_amdgcn_global_load_lds((const unsigned*)((const char*)(gbase) + (voff)[_i]), (LAS unsigned*)(lds + (bufoff) + ldsw + _i * 8192), 16, 0, 0); } while (0)
; #define GM_LDA(dst, b, h) do { _Pragma("unroll") for (int m = 0; m < 4; ++m) _Pragma("unroll") for (int k = 0; k < 2; ++k) dst[m][k] = *(const LAS s16x8*)(lds + GM_SA(b, h) + aoff + m * 2048 + k * 1024); } while (0)
; #define GM_LDB(dst, b, h) do { _Pragma("unroll") for (int n = 0; n < 2; ++n) _Pragma("unroll") for (int k = 0; k < 2; ++k) dst[n][k] = *(const LAS s16x8*)(lds + GM_SB(b, h) + boff + n * 2048 + k * 1024); } while (0)
; #define GM_MMA(ai, bj, At, Bt) do { __builtin_amdgcn_s_setprio(1); _Pragma("unroll") for (int m = 0; m < 4; ++m) _Pragma("unroll") for (int n = 0; n < 2; ++n) _Pragma("unroll") for (int k = 0; k < 2; ++k) \
;         acc[ai][bj][m][n] = mma16<BF>(Bt[n][k], At[m][k], acc[ai][bj][m][n]); __builtin_amdgcn_s_setprio(0); } while (0)
; #define GM_WAIT_V(n) asm volatile("s_waitcnt vmcnt(" #n ")" ::: "memory")
; #define GM_WAIT_L(n) asm volatile("s_waitcnt lgkmcnt(" #n ")" ::: "memory")
; #define GM_BAR __builtin_amdgcn_s_barrier()
; #define GM_SCHED __builtin_amdgcn_sched_barrier(0)
; template <bool BF, bool GATHER = false, class Epi, class Hook>
; __device__ __forceinline__ void gemm_phase(LAS unsigned char* lds, const Gemm g, const Order& S, const Epi& E, Hook& HK) {
;     ...
;             const bool last = (t == nt - 2);
;             const char* a1 = cA + (size_t)(t + 1) * kstep;
;             const char* a2 = last ? nA : cA + (size_t)(t + 2) * kstep; const char* b2 = last ? nB : cB + (size_t)(t + 2) * kstep;
;             const char* a3 = a2 + kstep; const char* b3 = b2 + kstep;
;             unsigned s0[2], s1[2];
;             if constexpr (GATHER) { s0[0] = last ? nA0[0] : gA0[0]; s0[1] = last ? nA0[1] : gA0[1]; s1[0] = last ? nA1[0] : gA1[0]; s1[1] = last ? nA1[1] : gA1[1]; }
;             GM_LDB(B0, 0, 0); GM_LDB(B1, 0, 1); GM_SCHED; GM_LDA(At, 0, 0); GM_STA_H1(GM_SA(1, 1), a1, gA1);
;             GM_WAIT_V(8); GM_WAIT_L(0); GM_BAR; GM_MMA(0, 0, At, B0); GM_MMA(0, 1, At, B1); GM_BAR; GM_SCHED;
;             GM_LDA(At, 0, 1); GM_STAGE(GM_SB(0, 0), b2, voffB); GM_STAGE(GM_SB(0, 1), b2 + hstepB, voffB); GM_STA_H0(GM_SA(0, 0), a2, s0);
.LBB0_1011:
	s_add_u32 s22, s90, s2
	s_addc_u32 s23, s91, s3
	s_add_u32 s24, s22, 0x11e00100
	s_addc_u32 s25, s23, 0
	s_add_u32 s44, s21, s2
	s_addc_u32 s45, s42, s3
	s_cmpk_eq_i32 s2, 0x700
	s_cselect_b64 vcc, -1, 0
	s_and_b64 s[22:23], vcc, exec
	v_cndmask_b32_e32 v134, v142, v159, vcc
	s_cselect_b32 s25, s69, s25
	s_cselect_b32 s24, s68, s24
	v_cndmask_b32_e32 v228, v146, v162, vcc
	v_cndmask_b32_e32 v141, v158, v160, vcc
	v_cndmask_b32_e32 v145, v157, v161, vcc
	s_cselect_b32 s23, s1, s45
	s_cselect_b32 s22, s0, s44
	s_add_i32 m0, s28, 0xc000
	v_lshl_add_u64 v[230:231], v[150:151], 0, s[2:3]
	global_load_lds_dwordx4 v[230:231], off
	s_add_i32 m0, s28, 0xe000
	v_lshl_add_u64 v[230:231], v[148:149], 0, s[2:3]
	global_load_lds_dwordx4 v[230:231], off
	v_add_u32_e32 v244, s35, v156
	ds_read_b128 v[164:167], v244
	ds_read_b128 v[168:171], v244 offset:1024
	ds_read_b128 v[172:175], v244 offset:2048
	ds_read_b128 v[176:179], v244 offset:3072
	v_add_u32_e32 v244, s36, v156
	ds_read_b128 v[180:183], v244
	ds_read_b128 v[184:187], v244 offset:1024
	ds_read_b128 v[188:191], v244 offset:2048
	ds_read_b128 v[192:195], v244 offset:3072
	ds_read_b128 v[196:199], v147
	ds_read_b128 v[200:203], v147 offset:1024
	ds_read_b128 v[204:207], v147 offset:2048
	ds_read_b128 v[208:211], v147 offset:3072
	ds_read_b128 v[212:215], v147 offset:4096
	ds_read_b128 v[216:219], v147 offset:5120
	ds_read_b128 v[220:223], v147 offset:6144
	ds_read_b128 v[224:227], v147 offset:7168
	s_waitcnt vmcnt(8)
	s_waitcnt lgkmcnt(0)
	s_barrier
	v_mfma_f32_16x16x32_bf16 v[98:101], v[164:167], v[196:199], v[98:101]
	v_mfma_f32_16x16x32_bf16 v[94:97], v[172:175], v[196:199], v[94:97]
	v_mfma_f32_16x16x32_bf16 v[90:93], v[164:167], v[204:207], v[90:93]
	v_mfma_f32_16x16x32_bf16 v[86:89], v[172:175], v[204:207], v[86:89]
	v_mfma_f32_16x16x32_bf16 v[82:85], v[164:167], v[212:215], v[82:85]
	v_mfma_f32_16x16x32_bf16 v[78:81], v[172:175], v[212:215], v[78:81]
	v_mfma_f32_16x16x32_bf16 v[74:77], v[164:167], v[220:223], v[74:77]
	v_mfma_f32_16x16x32_bf16 v[70:73], v[172:175], v[220:223], v[70:73]
	v_mfma_f32_16x16x32_bf16 v[98:101], v[168:171], v[200:203], v[98:101]
	v_mfma_f32_16x16x32_bf16 v[94:97], v[176:179], v[200:203], v[94:97]
	v_mfma_f32_16x16x32_bf16 v[90:93], v[168:171], v[208:211], v[90:93]
	v_mfma_f32_16x16x32_bf16 v[86:89], v[176:179], v[208:211], v[86:89]
	v_mfma_f32_16x16x32_bf16 v[82:85], v[168:171], v[216:219], v[82:85]
	v_mfma_f32_16x16x32_bf16 v[78:81], v[176:179], v[216:219], v[78:81]
	v_mfma_f32_16x16x32_bf16 v[74:77], v[168:171], v[224:227], v[74:77]
	v_mfma_f32_16x16x32_bf16 v[70:73], v[176:179], v[224:227], v[70:73]
	v_mfma_f32_16x16x32_bf16 v[66:69], v[180:183], v[196:199], v[66:69]
	v_mfma_f32_16x16x32_bf16 v[62:65], v[188:191], v[196:199], v[62:65]
	v_mfma_f32_16x16x32_bf16 v[58:61], v[180:183], v[204:207], v[58:61]
	v_mfma_f32_16x16x32_bf16 v[54:57], v[188:191], v[204:207], v[54:57]
	v_mfma_f32_16x16x32_bf16 v[50:53], v[180:183], v[212:215], v[50:53]
	v_mfma_f32_16x16x32_bf16 v[46:49], v[188:191], v[212:215], v[46:49]
	v_mfma_f32_16x16x32_bf16 v[42:45], v[180:183], v[220:223], v[42:45]
	v_mfma_f32_16x16x32_bf16 v[38:41], v[188:191], v[220:223], v[38:41]
	v_mfma_f32_16x16x32_bf16 v[66:69], v[184:187], v[200:203], v[66:69]
	v_mfma_f32_16x16x32_bf16 v[62:65], v[192:195], v[200:203], v[62:65]
	v_mfma_f32_16x16x32_bf16 v[58:61], v[184:187], v[208:211], v[58:61]
	v_mfma_f32_16x16x32_bf16 v[54:57], v[192:195], v[208:211], v[54:57]
	v_mfma_f32_16x16x32_bf16 v[50:53], v[184:187], v[216:219], v[50:53]
	v_mfma_f32_16x16x32_bf16 v[46:49], v[192:195], v[216:219], v[46:49]
	v_mfma_f32_16x16x32_bf16 v[42:45], v[184:187], v[224:227], v[42:45]
	v_mfma_f32_16x16x32_bf16 v[38:41], v[192:195], v[224:227], v[38:41]
	s_barrier
	s_add_i32 s44, s35, s11
	s_mov_b32 m0, s44
	v_lshl_add_u64 v[230:231], s[22:23], 0, v[130:131]
	global_load_lds_dwordx4 v[230:231], off
	s_add_i32 m0, s44, 0x2000
	s_add_u32 s44, s22, 0x40000
	v_lshl_add_u64 v[232:233], s[22:23], 0, v[132:133]
	s_addc_u32 s45, s23, 0
	s_add_i32 s46, s36, s11
	global_load_lds_dwordx4 v[232:233], off
	v_lshl_add_u64 v[234:235], s[44:45], 0, v[130:131]
	s_mov_b32 m0, s46
	v_mov_b32_e32 v229, v135
	global_load_lds_dwordx4 v[234:235], off
	s_add_i32 m0, s46, 0x2000
	v_lshl_add_u64 v[234:235], s[44:45], 0, v[132:133]
	global_load_lds_dwordx4 v[234:235], off
	s_mov_b32 m0, s28
	v_lshl_add_u64 v[234:235], s[24:25], 0, v[134:135]
	global_load_lds_dwordx4 v134, s[24:25]
	s_mov_b32 m0, s29
	s_nop 0
	global_load_lds_dwordx4 v228, s[24:25]
	v_lshl_add_u64 v[228:229], s[24:25], 0, v[228:229]
	ds_read_b128 v[196:199], v147 offset:16384
	ds_read_b128 v[200:203], v147 offset:17408
	ds_read_b128 v[204:207], v147 offset:18432
	ds_read_b128 v[208:211], v147 offset:19456
	ds_read_b128 v[212:215], v147 offset:20480
	ds_read_b128 v[216:219], v147 offset:21504
	ds_read_b128 v[220:223], v147 offset:22528
	ds_read_b128 v[224:227], v147 offset:23552
	s_waitcnt vmcnt(8)
	s_waitcnt lgkmcnt(0)
	s_barrier
; #define GM_LDA(dst, b, h) do { _Pragma("unroll") for (int m = 0; m < 4; ++m) _Pragma("unroll") for (int k = 0; k < 2; ++k) dst[m][k] = *(const LAS s16x8*)(lds + GM_SA(b, h) + aoff + m * 2048 + k * 1024); } while (0)
; #define GM_LDB(dst, b, h) do { _Pragma("unroll") for (int n = 0; n < 2; ++n) _Pragma("unroll") for (int k = 0; k < 2; ++k) dst[n][k] = *(const LAS s16x8*)(lds + GM_SB(b, h) + boff + n * 2048 + k * 1024); } while (0)
; #define GM_MMA(ai, bj, At, Bt) do { __builtin_amdgcn_s_setprio(1); _Pragma("unroll") for (int m = 0; m < 4; ++m) _Pragma("unroll") for (int n = 0; n < 2; ++n) _Pragma("unroll") for (int k = 0; k < 2; ++k) \
;         acc[ai][bj][m][n] = mma16<BF>(Bt[n][k], At[m][k], acc[ai][bj][m][n]); __builtin_amdgcn_s_setprio(0); } while (0)
; #define GM_WAIT_V(n) asm volatile("s_waitcnt vmcnt(" #n ")" ::: "memory")
; #define GM_WAIT_L(n) asm volatile("s_waitcnt lgkmcnt(" #n ")" ::: "memory")
; #define GM_BAR __builtin_amdgcn_s_barrier()
; #define GM_SCHED __builtin_amdgcn_sched_barrier(0)
; #define GM_STA_H1(buf, p, o1) do { if constexpr (GATHER) GM_STAGE(buf, p, o1); else GM_STAGE(buf, (p) + hstepB, voffA); } while (0)
; template <bool BF, bool GATHER = false, class Epi, class Hook>
; __device__ __forceinline__ void gemm_phase(LAS unsigned char* lds, const Gemm g, const Order& S, const Epi& E, Hook& HK) {
;     ...
;             GM_WAIT_V(8); GM_WAIT_L(0); GM_BAR; GM_MMA(1, 0, At, B0); GM_MMA(1, 1, At, B1); GM_BAR; GM_SCHED;
;             GM_LDB(B0, 1, 0); GM_LDB(B1, 1, 1); GM_SCHED; GM_LDA(At, 1, 0); GM_STA_H1(GM_SA(0, 1), a2, s1);
;             GM_WAIT_V(8); GM_WAIT_L(0); GM_BAR; GM_MMA(0, 0, At, B0); GM_MMA(0, 1, At, B1); GM_BAR; GM_SCHED;
	v_mfma_f32_16x16x32_bf16 v[34:37], v[164:167], v[196:199], v[34:37]
	v_mfma_f32_16x16x32_bf16 v[30:33], v[172:175], v[196:199], v[30:33]
	v_mfma_f32_16x16x32_bf16 v[26:29], v[164:167], v[204:207], v[26:29]
	v_mfma_f32_16x16x32_bf16 v[22:25], v[172:175], v[204:207], v[22:25]
	v_mfma_f32_16x16x32_bf16 v[18:21], v[164:167], v[212:215], v[18:21]
	v_mfma_f32_16x16x32_bf16 v[14:17], v[172:175], v[212:215], v[14:17]
	v_mfma_f32_16x16x32_bf16 v[10:13], v[164:167], v[220:223], v[10:13]
	v_mfma_f32_16x16x32_bf16 v[6:9], v[172:175], v[220:223], v[6:9]
	v_mfma_f32_16x16x32_bf16 v[34:37], v[168:171], v[200:203], v[34:37]
	v_mfma_f32_16x16x32_bf16 v[30:33], v[176:179], v[200:203], v[30:33]
	v_mfma_f32_16x16x32_bf16 v[26:29], v[168:171], v[208:211], v[26:29]
	v_mfma_f32_16x16x32_bf16 v[22:25], v[176:179], v[208:211], v[22:25]
	v_mfma_f32_16x16x32_bf16 v[18:21], v[168:171], v[216:219], v[18:21]
	v_mfma_f32_16x16x32_bf16 v[14:17], v[176:179], v[216:219], v[14:17]
	v_mfma_f32_16x16x32_bf16 v[10:13], v[168:171], v[224:227], v[10:13]
	v_mfma_f32_16x16x32_bf16 v[6:9], v[176:179], v[224:227], v[6:9]
	v_mfma_f32_16x16x32_bf16 v[2:5], v[180:183], v[196:199], v[2:5]
	v_mfma_f32_16x16x32_bf16 v[102:105], v[188:191], v[196:199], v[102:105]
	v_mfma_f32_16x16x32_bf16 v[106:109], v[180:183], v[204:207], v[106:109]
	v_mfma_f32_16x16x32_bf16 v[110:113], v[188:191], v[204:207], v[110:113]
	v_mfma_f32_16x16x32_bf16 v[114:117], v[180:183], v[212:215], v[114:117]
	v_mfma_f32_16x16x32_bf16 v[118:121], v[188:191], v[212:215], v[118:121]
	v_mfma_f32_16x16x32_bf16 v[122:125], v[180:183], v[220:223], v[122:125]
	v_mfma_f32_16x16x32_bf16 v[126:129], v[188:191], v[220:223], v[126:129]
	v_mfma_f32_16x16x32_bf16 v[2:5], v[184:187], v[200:203], v[2:5]
	v_mfma_f32_16x16x32_bf16 v[102:105], v[192:195], v[200:203], v[102:105]
	v_mfma_f32_16x16x32_bf16 v[106:109], v[184:187], v[208:211], v[106:109]
	v_mfma_f32_16x16x32_bf16 v[110:113], v[192:195], v[208:211], v[110:113]
	v_mfma_f32_16x16x32_bf16 v[114:117], v[184:187], v[216:219], v[114:117]
	v_mfma_f32_16x16x32_bf16 v[118:121], v[192:195], v[216:219], v[118:121]
	v_mfma_f32_16x16x32_bf16 v[122:125], v[184:187], v[224:227], v[122:125]
	v_mfma_f32_16x16x32_bf16 v[126:129], v[192:195], v[224:227], v[126:129]
	s_barrier
	s_mov_b32 m0, s30
	s_nop 0
	global_load_lds_dwordx4 v141, s[24:25]
	s_mov_b32 m0, s31
	s_nop 0
	global_load_lds_dwordx4 v145, s[24:25]
	s_mov_b32 s45, 0x1c000
	s_mov_b32 s44, 0x18000
	v_add_u32_e32 v245, s44, v156
	ds_read_b128 v[164:167], v245
	ds_read_b128 v[168:171], v245 offset:1024
	ds_read_b128 v[172:175], v245 offset:2048
	ds_read_b128 v[176:179], v245 offset:3072
	v_add_u32_e32 v245, s45, v156
	ds_read_b128 v[180:183], v245
	ds_read_b128 v[184:187], v245 offset:1024
	ds_read_b128 v[188:191], v245 offset:2048
	ds_read_b128 v[192:195], v245 offset:3072
	ds_read_b128 v[196:199], v147 offset:32768
	ds_read_b128 v[200:203], v147 offset:33792
	ds_read_b128 v[204:207], v147 offset:34816
	ds_read_b128 v[208:211], v147 offset:35840
	ds_read_b128 v[212:215], v147 offset:36864
	ds_read_b128 v[216:219], v147 offset:37888
	ds_read_b128 v[220:223], v147 offset:38912
	ds_read_b128 v[224:227], v147 offset:39936
	s_waitcnt vmcnt(8)
	s_waitcnt lgkmcnt(0)
	s_barrier
	v_mfma_f32_16x16x32_bf16 v[98:101], v[164:167], v[196:199], v[98:101]
	v_mfma_f32_16x16x32_bf16 v[94:97], v[172:175], v[196:199], v[94:97]
	v_mfma_f32_16x16x32_bf16 v[90:93], v[164:167], v[204:207], v[90:93]
	v_mfma_f32_16x16x32_bf16 v[86:89], v[172:175], v[204:207], v[86:89]
	v_mfma_f32_16x16x32_bf16 v[82:85], v[164:167], v[212:215], v[82:85]
	v_mfma_f32_16x16x32_bf16 v[78:81], v[172:175], v[212:215], v[78:81]
	v_mfma_f32_16x16x32_bf16 v[74:77], v[164:167], v[220:223], v[74:77]
	v_mfma_f32_16x16x32_bf16 v[70:73], v[172:175], v[220:223], v[70:73]
	v_mfma_f32_16x16x32_bf16 v[98:101], v[168:171], v[200:203], v[98:101]
	v_mfma_f32_16x16x32_bf16 v[94:97], v[176:179], v[200:203], v[94:97]
	v_mfma_f32_16x16x32_bf16 v[90:93], v[168:171], v[208:211], v[90:93]
	v_mfma_f32_16x16x32_bf16 v[86:89], v[176:179], v[208:211], v[86:89]
	v_mfma_f32_16x16x32_bf16 v[82:85], v[168:171], v[216:219], v[82:85]
	v_mfma_f32_16x16x32_bf16 v[78:81], v[176:179], v[216:219], v[78:81]
	v_mfma_f32_16x16x32_bf16 v[74:77], v[168:171], v[224:227], v[74:77]
	v_mfma_f32_16x16x32_bf16 v[70:73], v[176:179], v[224:227], v[70:73]
	v_mfma_f32_16x16x32_bf16 v[66:69], v[180:183], v[196:199], v[66:69]
	v_mfma_f32_16x16x32_bf16 v[62:65], v[188:191], v[196:199], v[62:65]
	v_mfma_f32_16x16x32_bf16 v[58:61], v[180:183], v[204:207], v[58:61]
	v_mfma_f32_16x16x32_bf16 v[54:57], v[188:191], v[204:207], v[54:57]
	v_mfma_f32_16x16x32_bf16 v[50:53], v[180:183], v[212:215], v[50:53]
	v_mfma_f32_16x16x32_bf16 v[46:49], v[188:191], v[212:215], v[46:49]
	v_mfma_f32_16x16x32_bf16 v[42:45], v[180:183], v[220:223], v[42:45]
	v_mfma_f32_16x16x32_bf16 v[38:41], v[188:191], v[220:223], v[38:41]
	v_mfma_f32_16x16x32_bf16 v[66:69], v[184:187], v[200:203], v[66:69]
	v_mfma_f32_16x16x32_bf16 v[62:65], v[192:195], v[200:203], v[62:65]
	v_mfma_f32_16x16x32_bf16 v[58:61], v[184:187], v[208:211], v[58:61]
	v_mfma_f32_16x16x32_bf16 v[54:57], v[192:195], v[208:211], v[54:57]
	v_mfma_f32_16x16x32_bf16 v[50:53], v[184:187], v[216:219], v[50:53]
	v_mfma_f32_16x16x32_bf16 v[46:49], v[192:195], v[216:219], v[46:49]
	v_mfma_f32_16x16x32_bf16 v[42:45], v[184:187], v[224:227], v[42:45]
	v_mfma_f32_16x16x32_bf16 v[38:41], v[192:195], v[224:227], v[38:41]
	s_barrier
; #define GM_STAGE(bufoff, gbase, voff) do { _Pragma("unroll") for (int _i = 0; _i < 2; ++_i) \
;         __builtin_amdgcn_global_load_lds((const unsigned*)((const char*)(gbase) + (voff)[_i]), (LAS unsigned*)(lds + (bufoff) + ldsw + _i * 8192), 16, 0, 0); } while (0)
; #define GM_LDA(dst, b, h) do { _Pragma("unroll") for (int m = 0; m < 4; ++m) _Pragma("unroll") for (int k = 0; k < 2; ++k) dst[m][k] = *(const LAS s16x8*)(lds + GM_SA(b, h) + aoff + m * 2048 + k * 1024); } while (0)
; #define GM_MMA(ai, bj, At, Bt) do { __builtin_amdgcn_s_setprio(1); _Pragma("unroll") for (int m = 0; m < 4; ++m) _Pragma("unroll") for (int n = 0; n < 2; ++n) _Pragma("unroll") for (int k = 0; k < 2; ++k) \
;         acc[ai][bj][m][n] = mma16<BF>(Bt[n][k], At[m][k], acc[ai][bj][m][n]); __builtin_amdgcn_s_setprio(0); } while (0)
; #define GM_WAIT_V(n) asm volatile("s_waitcnt vmcnt(" #n ")" ::: "memory")
; #define GM_WAIT_L(n) asm volatile("s_waitcnt lgkmcnt(" #n ")" ::: "memory")
; #define GM_BAR __builtin_amdgcn_s_barrier()
; #define GM_SCHED __builtin_amdgcn_sched_barrier(0)
; #define GM_STA_H0(buf, p, o0) do { if constexpr (GATHER) GM_STAGE(buf, p, o0); else GM_STAGE(buf, p, voffA); } while (0)
; template <bool BF, bool GATHER = false, class Epi, class Hook>
; __device__ __forceinline__ void gemm_phase(LAS unsigned char* lds, const Gemm g, const Order& S, const Epi& E, Hook& HK) {
;     ...
;             GM_LDA(At, 1, 1); GM_STAGE(GM_SB(1, 0), b3, voffB); GM_STAGE(GM_SB(1, 1), b3 + hstepB, voffB); GM_STA_H0(GM_SA(1, 0), a3, s0);
;             GM_WAIT_V(8); GM_WAIT_L(0); GM_BAR; GM_MMA(1, 0, At, B0); GM_MMA(1, 1, At, B1); GM_BAR; GM_SCHED;
;         }
;         if (wr == 0) GM_BAR;
	s_add_i32 s24, s44, s11
	s_mov_b32 m0, s24
	v_lshl_add_u64 v[230:231], v[230:231], 0, s[14:15]
	global_load_lds_dwordx4 v[230:231], off
	s_add_i32 m0, s24, 0x2000
	s_add_u32 s22, s22, 0x40080
	v_lshl_add_u64 v[230:231], v[232:233], 0, s[14:15]
	s_addc_u32 s23, s23, 0
	s_add_i32 s24, s45, s11
	global_load_lds_dwordx4 v[230:231], off
	v_lshl_add_u64 v[230:231], s[22:23], 0, v[130:131]
	s_mov_b32 m0, s24
	v_lshl_add_u64 v[228:229], v[228:229], 0, s[14:15]
	global_load_lds_dwordx4 v[230:231], off
	s_add_i32 m0, s24, 0x2000
	v_lshl_add_u64 v[230:231], s[22:23], 0, v[132:133]
	global_load_lds_dwordx4 v[230:231], off
	s_mov_b32 m0, s33
	v_lshl_add_u64 v[230:231], v[234:235], 0, s[14:15]
	global_load_lds_dwordx4 v[230:231], off
	s_mov_b32 m0, s34
	s_nop 0
	global_load_lds_dwordx4 v[228:229], off
	ds_read_b128 v[196:199], v147 offset:49152
	ds_read_b128 v[200:203], v147 offset:50176
	ds_read_b128 v[204:207], v147 offset:51200
	ds_read_b128 v[208:211], v147 offset:52224
	ds_read_b128 v[212:215], v147 offset:53248
	ds_read_b128 v[216:219], v147 offset:54272
	ds_read_b128 v[220:223], v147 offset:55296
	ds_read_b128 v[224:227], v147 offset:56320
	s_waitcnt vmcnt(8)
	s_waitcnt lgkmcnt(0)
	s_barrier
	v_mfma_f32_16x16x32_bf16 v[34:37], v[164:167], v[196:199], v[34:37]
	v_mfma_f32_16x16x32_bf16 v[30:33], v[172:175], v[196:199], v[30:33]
	v_mfma_f32_16x16x32_bf16 v[26:29], v[164:167], v[204:207], v[26:29]
	v_mfma_f32_16x16x32_bf16 v[22:25], v[172:175], v[204:207], v[22:25]
	v_mfma_f32_16x16x32_bf16 v[18:21], v[164:167], v[212:215], v[18:21]
	v_mfma_f32_16x16x32_bf16 v[14:17], v[172:175], v[212:215], v[14:17]
	v_mfma_f32_16x16x32_bf16 v[10:13], v[164:167], v[220:223], v[10:13]
	v_mfma_f32_16x16x32_bf16 v[6:9], v[172:175], v[220:223], v[6:9]
	v_mfma_f32_16x16x32_bf16 v[34:37], v[168:171], v[200:203], v[34:37]
	v_mfma_f32_16x16x32_bf16 v[30:33], v[176:179], v[200:203], v[30:33]
	v_mfma_f32_16x16x32_bf16 v[26:29], v[168:171], v[208:211], v[26:29]
	v_mfma_f32_16x16x32_bf16 v[22:25], v[176:179], v[208:211], v[22:25]
	v_mfma_f32_16x16x32_bf16 v[18:21], v[168:171], v[216:219], v[18:21]
	v_mfma_f32_16x16x32_bf16 v[14:17], v[176:179], v[216:219], v[14:17]
	v_mfma_f32_16x16x32_bf16 v[10:13], v[168:171], v[224:227], v[10:13]
	v_mfma_f32_16x16x32_bf16 v[6:9], v[176:179], v[224:227], v[6:9]
	v_mfma_f32_16x16x32_bf16 v[2:5], v[180:183], v[196:199], v[2:5]
	v_mfma_f32_16x16x32_bf16 v[102:105], v[188:191], v[196:199], v[102:105]
	v_mfma_f32_16x16x32_bf16 v[106:109], v[180:183], v[204:207], v[106:109]
	v_mfma_f32_16x16x32_bf16 v[110:113], v[188:191], v[204:207], v[110:113]
	v_mfma_f32_16x16x32_bf16 v[114:117], v[180:183], v[212:215], v[114:117]
	v_mfma_f32_16x16x32_bf16 v[118:121], v[188:191], v[212:215], v[118:121]
	v_mfma_f32_16x16x32_bf16 v[122:125], v[180:183], v[220:223], v[122:125]
	v_mfma_f32_16x16x32_bf16 v[126:129], v[188:191], v[220:223], v[126:129]
	v_mfma_f32_16x16x32_bf16 v[2:5], v[184:187], v[200:203], v[2:5]
	v_mfma_f32_16x16x32_bf16 v[102:105], v[192:195], v[200:203], v[102:105]
	v_mfma_f32_16x16x32_bf16 v[106:109], v[184:187], v[208:211], v[106:109]
	v_mfma_f32_16x16x32_bf16 v[110:113], v[192:195], v[208:211], v[110:113]
	v_mfma_f32_16x16x32_bf16 v[114:117], v[184:187], v[216:219], v[114:117]
	v_mfma_f32_16x16x32_bf16 v[118:121], v[192:195], v[216:219], v[118:121]
	v_mfma_f32_16x16x32_bf16 v[122:125], v[184:187], v[224:227], v[122:125]
	v_mfma_f32_16x16x32_bf16 v[126:129], v[192:195], v[224:227], v[126:129]
	s_barrier
	s_add_i32 s43, s43, 2
	s_add_u32 s2, s2, 0x100
	s_addc_u32 s3, s3, 0
	s_cmp_gt_u32 s43, 13
	s_cbranch_scc0 .LBB0_1011
	s_and_b64 vcc, exec, s[18:19]
	s_cbranch_vccz .LBB0_1014
	s_barrier

; #define GM_STAGE(bufoff, gbase, voff) do { _Pragma("unroll") for (int _i = 0; _i < 2; ++_i) \
;         __builtin_amdgcn_global_load_lds((const unsigned*)((const char*)(gbase) + (voff)[_i]), (LAS unsigned*)(lds + (bufoff) + ldsw + _i * 8192), 16, 0, 0); } while (0)
; #define GM_LDA(dst, b, h) do { _Pragma("unroll") for (int m = 0; m < 4; ++m) _Pragma("unroll") for (int k = 0; k < 2; ++k) dst[m][k] = *(const LAS s16x8*)(lds + GM_SA(b, h) + aoff + m * 2048 + k * 1024); } while (0)
; #define GM_LDB(dst, b, h) do { _Pragma("unroll") for (int n = 0; n < 2; ++n) _Pragma("unroll") for (int k = 0; k < 2; ++k) dst[n][k] = *(const LAS s16x8*)(lds + GM_SB(b, h) + boff + n * 2048 + k * 1024); } while (0)
; #define GM_MMA(ai, bj, At, Bt) do { __builtin_amdgcn_s_setprio(1); _Pragma("unroll") for (int m = 0; m < 4; ++m) _Pragma("unroll") for (int n = 0; n < 2; ++n) _Pragma("unroll") for (int k = 0; k < 2; ++k) \
;         acc[ai][bj][m][n] = mma16<BF>(Bt[n][k], At[m][k], acc[ai][bj][m][n]); __builtin_amdgcn_s_setprio(0); } while (0)
; #define GM_WAIT_V(n) asm volatile("s_waitcnt vmcnt(" #n ")" ::: "memory")
; #define GM_WAIT_L(n) asm volatile("s_waitcnt lgkmcnt(" #n ")" ::: "memory")
; #define GM_BAR __builtin_amdgcn_s_barrier()
; template <bool BF, bool GATHER = false, class Epi, class Hook>
; __device__ __forceinline__ void gemm_phase(LAS unsigned char* lds, const Gemm g, const Order& S, const Epi& E, Hook& HK) {
;     ...
;         for (int t = 0; t < nt; t += 2) {
;             const bool last = (t == nt - 2);
;             const char* a1 = cA + (size_t)(t + 1) * kstep;
;             const char* a2 = last ? nA : cA + (size_t)(t + 2) * kstep; const char* b2 = last ? nB : cB + (size_t)(t + 2) * kstep;
;             const char* a3 = a2 + kstep; const char* b3 = b2 + kstep;
;             unsigned s0[2], s1[2];
;             if constexpr (GATHER) { s0[0] = last ? nA0[0] : gA0[0]; s0[1] = last ? nA0[1] : gA0[1]; s1[0] = last ? nA1[0] : gA1[0]; s1[1] = last ? nA1[1] : gA1[1]; }
;             GM_LDB(B0, 0, 0); GM_LDB(B1, 0, 1); GM_SCHED; GM_LDA(At, 0, 0); GM_STA_H1(GM_SA(1, 1), a1, gA1);
;             GM_WAIT_V(8); GM_WAIT_L(0); GM_BAR; GM_MMA(0, 0, At, B0); GM_MMA(0, 1, At, B1); GM_BAR; GM_SCHED;
;             GM_LDA(At, 0, 1); GM_STAGE(GM_SB(0, 0), b2, voffB); GM_STAGE(GM_SB(0, 1), b2 + hstepB, voffB); GM_STA_H0(GM_SA(0, 0), a2, s0);
.LBB0_1102:
	s_add_u32 s22, s2, 0x100
	s_addc_u32 s23, s3, 0
	s_cmp_eq_u32 s51, 40
	s_cselect_b32 s27, s7, s23
	s_cselect_b32 s26, s6, s22
	s_cselect_b32 s25, s21, s50
	s_cselect_b32 s24, s20, s49
	s_add_i32 m0, s29, 0xc000
	v_lshl_add_u64 v[216:217], s[2:3], 0, v[138:139]
	global_load_lds_dwordx4 v[216:217], off
	s_add_i32 m0, s29, 0xe000
	v_lshl_add_u64 v[216:217], s[2:3], 0, v[140:141]
	global_load_lds_dwordx4 v[216:217], off
	ds_read_b128 v[146:149], v153
	ds_read_b128 v[156:159], v153 offset:1024
	ds_read_b128 v[160:163], v153 offset:2048
	ds_read_b128 v[164:167], v153 offset:3072
	ds_read_b128 v[168:171], v154
	ds_read_b128 v[172:175], v154 offset:1024
	ds_read_b128 v[176:179], v154 offset:2048
	ds_read_b128 v[180:183], v154 offset:3072
	ds_read_b128 v[184:187], v155
	ds_read_b128 v[188:191], v155 offset:1024
	ds_read_b128 v[192:195], v155 offset:2048
	ds_read_b128 v[196:199], v155 offset:3072
	ds_read_b128 v[200:203], v155 offset:4096
	ds_read_b128 v[204:207], v155 offset:5120
	ds_read_b128 v[208:211], v155 offset:6144
	ds_read_b128 v[212:215], v155 offset:7168
	s_waitcnt vmcnt(8)
	s_waitcnt lgkmcnt(0)
	s_barrier
	v_mfma_f32_16x16x32_bf16 v[126:129], v[146:149], v[184:187], v[126:129]
	v_mfma_f32_16x16x32_bf16 v[122:125], v[160:163], v[184:187], v[122:125]
	v_mfma_f32_16x16x32_bf16 v[110:113], v[146:149], v[192:195], v[110:113]
	v_mfma_f32_16x16x32_bf16 v[106:109], v[160:163], v[192:195], v[106:109]
	v_mfma_f32_16x16x32_bf16 v[94:97], v[146:149], v[200:203], v[94:97]
	v_mfma_f32_16x16x32_bf16 v[90:93], v[160:163], v[200:203], v[90:93]
	v_mfma_f32_16x16x32_bf16 v[78:81], v[146:149], v[208:211], v[78:81]
	v_mfma_f32_16x16x32_bf16 v[74:77], v[160:163], v[208:211], v[74:77]
	v_mfma_f32_16x16x32_bf16 v[126:129], v[156:159], v[188:191], v[126:129]
	v_mfma_f32_16x16x32_bf16 v[122:125], v[164:167], v[188:191], v[122:125]
	v_mfma_f32_16x16x32_bf16 v[110:113], v[156:159], v[196:199], v[110:113]
	v_mfma_f32_16x16x32_bf16 v[106:109], v[164:167], v[196:199], v[106:109]
	v_mfma_f32_16x16x32_bf16 v[94:97], v[156:159], v[204:207], v[94:97]
	v_mfma_f32_16x16x32_bf16 v[90:93], v[164:167], v[204:207], v[90:93]
	v_mfma_f32_16x16x32_bf16 v[78:81], v[156:159], v[212:215], v[78:81]
	v_mfma_f32_16x16x32_bf16 v[74:77], v[164:167], v[212:215], v[74:77]
	v_mfma_f32_16x16x32_bf16 v[118:121], v[168:171], v[184:187], v[118:121]
	v_mfma_f32_16x16x32_bf16 v[114:117], v[176:179], v[184:187], v[114:117]
	v_mfma_f32_16x16x32_bf16 v[102:105], v[168:171], v[192:195], v[102:105]
	v_mfma_f32_16x16x32_bf16 v[98:101], v[176:179], v[192:195], v[98:101]
	v_mfma_f32_16x16x32_bf16 v[86:89], v[168:171], v[200:203], v[86:89]
	v_mfma_f32_16x16x32_bf16 v[82:85], v[176:179], v[200:203], v[82:85]
	v_mfma_f32_16x16x32_bf16 v[70:73], v[168:171], v[208:211], v[70:73]
	v_mfma_f32_16x16x32_bf16 v[66:69], v[176:179], v[208:211], v[66:69]
	v_mfma_f32_16x16x32_bf16 v[118:121], v[172:175], v[188:191], v[118:121]
	v_mfma_f32_16x16x32_bf16 v[114:117], v[180:183], v[188:191], v[114:117]
	v_mfma_f32_16x16x32_bf16 v[102:105], v[172:175], v[196:199], v[102:105]
	v_mfma_f32_16x16x32_bf16 v[98:101], v[180:183], v[196:199], v[98:101]
	v_mfma_f32_16x16x32_bf16 v[86:89], v[172:175], v[204:207], v[86:89]
	v_mfma_f32_16x16x32_bf16 v[82:85], v[180:183], v[204:207], v[82:85]
	v_mfma_f32_16x16x32_bf16 v[70:73], v[172:175], v[212:215], v[70:73]
	v_mfma_f32_16x16x32_bf16 v[66:69], v[180:183], v[212:215], v[66:69]
	s_barrier
	s_add_i32 s2, s42, s28
	s_mov_b32 m0, s2
	v_lshl_add_u64 v[216:217], s[24:25], 0, v[132:133]
	global_load_lds_dwordx4 v[216:217], off
	s_add_i32 m0, s2, 0x2000
	s_add_u32 s2, s24, 0xb0000
	v_lshl_add_u64 v[218:219], s[24:25], 0, v[136:137]
	s_addc_u32 s3, s25, 0
	s_add_i32 s52, s43, s28
	global_load_lds_dwordx4 v[218:219], off
	v_lshl_add_u64 v[220:221], s[2:3], 0, v[132:133]
	s_mov_b32 m0, s52
	v_lshl_add_u64 v[222:223], s[26:27], 0, v[134:135]
	global_load_lds_dwordx4 v[220:221], off
	s_add_i32 m0, s52, 0x2000
	v_lshl_add_u64 v[220:221], s[2:3], 0, v[136:137]
	global_load_lds_dwordx4 v[220:221], off
	s_mov_b32 m0, s29
	v_lshl_add_u64 v[220:221], s[26:27], 0, v[130:131]
	global_load_lds_dwordx4 v[220:221], off
	s_mov_b32 m0, s30
	s_nop 0
	global_load_lds_dwordx4 v[222:223], off
	ds_read_b128 v[184:187], v155 offset:16384
	ds_read_b128 v[188:191], v155 offset:17408
	ds_read_b128 v[192:195], v155 offset:18432
	ds_read_b128 v[196:199], v155 offset:19456
	ds_read_b128 v[200:203], v155 offset:20480
	ds_read_b128 v[204:207], v155 offset:21504
	ds_read_b128 v[208:211], v155 offset:22528
	ds_read_b128 v[212:215], v155 offset:23552
	s_waitcnt vmcnt(8)
	s_waitcnt lgkmcnt(0)
	s_barrier
; #define GM_LDA(dst, b, h) do { _Pragma("unroll") for (int m = 0; m < 4; ++m) _Pragma("unroll") for (int k = 0; k < 2; ++k) dst[m][k] = *(const LAS s16x8*)(lds + GM_SA(b, h) + aoff + m * 2048 + k * 1024); } while (0)
; #define GM_LDB(dst, b, h) do { _Pragma("unroll") for (int n = 0; n < 2; ++n) _Pragma("unroll") for (int k = 0; k < 2; ++k) dst[n][k] = *(const LAS s16x8*)(lds + GM_SB(b, h) + boff + n * 2048 + k * 1024); } while (0)
; #define GM_MMA(ai, bj, At, Bt) do { __builtin_amdgcn_s_setprio(1); _Pragma("unroll") for (int m = 0; m < 4; ++m) _Pragma("unroll") for (int n = 0; n < 2; ++n) _Pragma("unroll") for (int k = 0; k < 2; ++k) \
;         acc[ai][bj][m][n] = mma16<BF>(Bt[n][k], At[m][k], acc[ai][bj][m][n]); __builtin_amdgcn_s_setprio(0); } while (0)
; #define GM_WAIT_V(n) asm volatile("s_waitcnt vmcnt(" #n ")" ::: "memory")
; #define GM_WAIT_L(n) asm volatile("s_waitcnt lgkmcnt(" #n ")" ::: "memory")
; #define GM_BAR __builtin_amdgcn_s_barrier()
; #define GM_SCHED __builtin_amdgcn_sched_barrier(0)
; #define GM_STA_H1(buf, p, o1) do { if constexpr (GATHER) GM_STAGE(buf, p, o1); else GM_STAGE(buf, (p) + hstepB, voffA); } while (0)
; template <bool BF, bool GATHER = false, class Epi, class Hook>
; __device__ __forceinline__ void gemm_phase(LAS unsigned char* lds, const Gemm g, const Order& S, const Epi& E, Hook& HK) {
;     ...
;             GM_WAIT_V(8); GM_WAIT_L(0); GM_BAR; GM_MMA(1, 0, At, B0); GM_MMA(1, 1, At, B1); GM_BAR; GM_SCHED;
;             GM_LDB(B0, 1, 0); GM_LDB(B1, 1, 1); GM_SCHED; GM_LDA(At, 1, 0); GM_STA_H1(GM_SA(0, 1), a2, s1);
;             GM_WAIT_V(8); GM_WAIT_L(0); GM_BAR; GM_MMA(0, 0, At, B0); GM_MMA(0, 1, At, B1); GM_BAR; GM_SCHED;
	v_mfma_f32_16x16x32_bf16 v[62:65], v[146:149], v[184:187], v[62:65]
	v_mfma_f32_16x16x32_bf16 v[58:61], v[160:163], v[184:187], v[58:61]
	v_mfma_f32_16x16x32_bf16 v[46:49], v[146:149], v[192:195], v[46:49]
	v_mfma_f32_16x16x32_bf16 v[42:45], v[160:163], v[192:195], v[42:45]
	v_mfma_f32_16x16x32_bf16 v[30:33], v[146:149], v[200:203], v[30:33]
	v_mfma_f32_16x16x32_bf16 v[26:29], v[160:163], v[200:203], v[26:29]
	v_mfma_f32_16x16x32_bf16 v[14:17], v[146:149], v[208:211], v[14:17]
	v_mfma_f32_16x16x32_bf16 v[10:13], v[160:163], v[208:211], v[10:13]
	v_mfma_f32_16x16x32_bf16 v[62:65], v[156:159], v[188:191], v[62:65]
	v_mfma_f32_16x16x32_bf16 v[58:61], v[164:167], v[188:191], v[58:61]
	v_mfma_f32_16x16x32_bf16 v[46:49], v[156:159], v[196:199], v[46:49]
	v_mfma_f32_16x16x32_bf16 v[42:45], v[164:167], v[196:199], v[42:45]
	v_mfma_f32_16x16x32_bf16 v[30:33], v[156:159], v[204:207], v[30:33]
	v_mfma_f32_16x16x32_bf16 v[26:29], v[164:167], v[204:207], v[26:29]
	v_mfma_f32_16x16x32_bf16 v[14:17], v[156:159], v[212:215], v[14:17]
	v_mfma_f32_16x16x32_bf16 v[10:13], v[164:167], v[212:215], v[10:13]
	v_mfma_f32_16x16x32_bf16 v[54:57], v[168:171], v[184:187], v[54:57]
	v_mfma_f32_16x16x32_bf16 v[50:53], v[176:179], v[184:187], v[50:53]
	v_mfma_f32_16x16x32_bf16 v[38:41], v[168:171], v[192:195], v[38:41]
	v_mfma_f32_16x16x32_bf16 v[34:37], v[176:179], v[192:195], v[34:37]
	v_mfma_f32_16x16x32_bf16 v[22:25], v[168:171], v[200:203], v[22:25]
	v_mfma_f32_16x16x32_bf16 v[18:21], v[176:179], v[200:203], v[18:21]
	v_mfma_f32_16x16x32_bf16 v[6:9], v[168:171], v[208:211], v[6:9]
	v_mfma_f32_16x16x32_bf16 v[2:5], v[176:179], v[208:211], v[2:5]
	v_mfma_f32_16x16x32_bf16 v[54:57], v[172:175], v[188:191], v[54:57]
	v_mfma_f32_16x16x32_bf16 v[50:53], v[180:183], v[188:191], v[50:53]
	v_mfma_f32_16x16x32_bf16 v[38:41], v[172:175], v[196:199], v[38:41]
	v_mfma_f32_16x16x32_bf16 v[34:37], v[180:183], v[196:199], v[34:37]
	v_mfma_f32_16x16x32_bf16 v[22:25], v[172:175], v[204:207], v[22:25]
	v_mfma_f32_16x16x32_bf16 v[18:21], v[180:183], v[204:207], v[18:21]
	v_mfma_f32_16x16x32_bf16 v[6:9], v[172:175], v[212:215], v[6:9]
	v_mfma_f32_16x16x32_bf16 v[2:5], v[180:183], v[212:215], v[2:5]
	s_barrier
	s_add_u32 s2, s26, 0xb0000
	s_addc_u32 s3, s27, 0
	s_mov_b32 m0, s31
	v_lshl_add_u64 v[224:225], s[2:3], 0, v[130:131]
	global_load_lds_dwordx4 v[224:225], off
	s_mov_b32 m0, s33
	v_lshl_add_u64 v[224:225], s[2:3], 0, v[134:135]
	global_load_lds_dwordx4 v[224:225], off
	s_mov_b32 s53, 0x1c000
	s_mov_b32 s52, 0x18000
	v_add_u32_e32 v244, s52, v150
	v_add_u32_e32 v245, s53, v150
	ds_read_b128 v[146:149], v244
	ds_read_b128 v[156:159], v244 offset:1024
	ds_read_b128 v[160:163], v244 offset:2048
	ds_read_b128 v[164:167], v244 offset:3072
	ds_read_b128 v[168:171], v245
	ds_read_b128 v[172:175], v245 offset:1024
	ds_read_b128 v[176:179], v245 offset:2048
	ds_read_b128 v[180:183], v245 offset:3072
	ds_read_b128 v[184:187], v155 offset:32768
	ds_read_b128 v[188:191], v155 offset:33792
	ds_read_b128 v[192:195], v155 offset:34816
	ds_read_b128 v[196:199], v155 offset:35840
	ds_read_b128 v[200:203], v155 offset:36864
	ds_read_b128 v[204:207], v155 offset:37888
	ds_read_b128 v[208:211], v155 offset:38912
	ds_read_b128 v[212:215], v155 offset:39936
	s_waitcnt vmcnt(8)
	s_waitcnt lgkmcnt(0)
	s_barrier
	v_mfma_f32_16x16x32_bf16 v[126:129], v[146:149], v[184:187], v[126:129]
	v_mfma_f32_16x16x32_bf16 v[122:125], v[160:163], v[184:187], v[122:125]
	v_mfma_f32_16x16x32_bf16 v[110:113], v[146:149], v[192:195], v[110:113]
	v_mfma_f32_16x16x32_bf16 v[106:109], v[160:163], v[192:195], v[106:109]
	v_mfma_f32_16x16x32_bf16 v[94:97], v[146:149], v[200:203], v[94:97]
	v_mfma_f32_16x16x32_bf16 v[90:93], v[160:163], v[200:203], v[90:93]
	v_mfma_f32_16x16x32_bf16 v[78:81], v[146:149], v[208:211], v[78:81]
	v_mfma_f32_16x16x32_bf16 v[74:77], v[160:163], v[208:211], v[74:77]
	v_mfma_f32_16x16x32_bf16 v[126:129], v[156:159], v[188:191], v[126:129]
	v_mfma_f32_16x16x32_bf16 v[122:125], v[164:167], v[188:191], v[122:125]
	v_mfma_f32_16x16x32_bf16 v[110:113], v[156:159], v[196:199], v[110:113]
	v_mfma_f32_16x16x32_bf16 v[106:109], v[164:167], v[196:199], v[106:109]
	v_mfma_f32_16x16x32_bf16 v[94:97], v[156:159], v[204:207], v[94:97]
	v_mfma_f32_16x16x32_bf16 v[90:93], v[164:167], v[204:207], v[90:93]
	v_mfma_f32_16x16x32_bf16 v[78:81], v[156:159], v[212:215], v[78:81]
	v_mfma_f32_16x16x32_bf16 v[74:77], v[164:167], v[212:215], v[74:77]
	v_mfma_f32_16x16x32_bf16 v[118:121], v[168:171], v[184:187], v[118:121]
	v_mfma_f32_16x16x32_bf16 v[114:117], v[176:179], v[184:187], v[114:117]
	v_mfma_f32_16x16x32_bf16 v[102:105], v[168:171], v[192:195], v[102:105]
	v_mfma_f32_16x16x32_bf16 v[98:101], v[176:179], v[192:195], v[98:101]
	v_mfma_f32_16x16x32_bf16 v[86:89], v[168:171], v[200:203], v[86:89]
	v_mfma_f32_16x16x32_bf16 v[82:85], v[176:179], v[200:203], v[82:85]
	v_mfma_f32_16x16x32_bf16 v[70:73], v[168:171], v[208:211], v[70:73]
	v_mfma_f32_16x16x32_bf16 v[66:69], v[176:179], v[208:211], v[66:69]
	v_mfma_f32_16x16x32_bf16 v[118:121], v[172:175], v[188:191], v[118:121]
	v_mfma_f32_16x16x32_bf16 v[114:117], v[180:183], v[188:191], v[114:117]
	v_mfma_f32_16x16x32_bf16 v[102:105], v[172:175], v[196:199], v[102:105]
	v_mfma_f32_16x16x32_bf16 v[98:101], v[180:183], v[196:199], v[98:101]
	v_mfma_f32_16x16x32_bf16 v[86:89], v[172:175], v[204:207], v[86:89]
	v_mfma_f32_16x16x32_bf16 v[82:85], v[180:183], v[204:207], v[82:85]
	v_mfma_f32_16x16x32_bf16 v[70:73], v[172:175], v[212:215], v[70:73]
	v_mfma_f32_16x16x32_bf16 v[66:69], v[180:183], v[212:215], v[66:69]
	s_barrier
; #define GM_STAGE(bufoff, gbase, voff) do { _Pragma("unroll") for (int _i = 0; _i < 2; ++_i) \
;         __builtin_amdgcn_global_load_lds((const unsigned*)((const char*)(gbase) + (voff)[_i]), (LAS unsigned*)(lds + (bufoff) + ldsw + _i * 8192), 16, 0, 0); } while (0)
; #define GM_LDA(dst, b, h) do { _Pragma("unroll") for (int m = 0; m < 4; ++m) _Pragma("unroll") for (int k = 0; k < 2; ++k) dst[m][k] = *(const LAS s16x8*)(lds + GM_SA(b, h) + aoff + m * 2048 + k * 1024); } while (0)
; #define GM_MMA(ai, bj, At, Bt) do { __builtin_amdgcn_s_setprio(1); _Pragma("unroll") for (int m = 0; m < 4; ++m) _Pragma("unroll") for (int n = 0; n < 2; ++n) _Pragma("unroll") for (int k = 0; k < 2; ++k) \
;         acc[ai][bj][m][n] = mma16<BF>(Bt[n][k], At[m][k], acc[ai][bj][m][n]); __builtin_amdgcn_s_setprio(0); } while (0)
; #define GM_WAIT_V(n) asm volatile("s_waitcnt vmcnt(" #n ")" ::: "memory")
; #define GM_WAIT_L(n) asm volatile("s_waitcnt lgkmcnt(" #n ")" ::: "memory")
; #define GM_BAR __builtin_amdgcn_s_barrier()
; #define GM_SCHED __builtin_amdgcn_sched_barrier(0)
; #define GM_STA_H0(buf, p, o0) do { if constexpr (GATHER) GM_STAGE(buf, p, o0); else GM_STAGE(buf, p, voffA); } while (0)
; template <bool BF, bool GATHER = false, class Epi, class Hook>
; __device__ __forceinline__ void gemm_phase(LAS unsigned char* lds, const Gemm g, const Order& S, const Epi& E, Hook& HK) {
;     ...
;             GM_LDA(At, 1, 1); GM_STAGE(GM_SB(1, 0), b3, voffB); GM_STAGE(GM_SB(1, 1), b3 + hstepB, voffB); GM_STA_H0(GM_SA(1, 0), a3, s0);
;             GM_WAIT_V(8); GM_WAIT_L(0); GM_BAR; GM_MMA(1, 0, At, B0); GM_MMA(1, 1, At, B1); GM_BAR; GM_SCHED;
;         }
;         if (wr == 0) GM_BAR;
	s_add_i32 s2, s52, s28
	s_mov_b32 m0, s2
	v_lshl_add_u64 v[216:217], v[216:217], 0, s[12:13]
	global_load_lds_dwordx4 v[216:217], off
	s_add_i32 m0, s2, 0x2000
	s_add_u32 s2, s24, 0xb0080
	v_lshl_add_u64 v[216:217], v[218:219], 0, s[12:13]
	s_addc_u32 s3, s25, 0
	s_add_i32 s24, s53, s28
	global_load_lds_dwordx4 v[216:217], off
	s_mov_b32 m0, s24
	v_lshl_add_u64 v[216:217], s[2:3], 0, v[132:133]
	global_load_lds_dwordx4 v[216:217], off
	s_add_i32 m0, s24, 0x2000
	v_lshl_add_u64 v[216:217], s[2:3], 0, v[136:137]
	global_load_lds_dwordx4 v[216:217], off
	s_mov_b32 m0, s36
	v_lshl_add_u64 v[216:217], v[220:221], 0, s[12:13]
	global_load_lds_dwordx4 v[216:217], off
	s_mov_b32 m0, s37
	v_lshl_add_u64 v[216:217], v[222:223], 0, s[12:13]
	global_load_lds_dwordx4 v[216:217], off
	ds_read_b128 v[184:187], v155 offset:49152
	ds_read_b128 v[188:191], v155 offset:50176
	ds_read_b128 v[192:195], v155 offset:51200
	ds_read_b128 v[196:199], v155 offset:52224
	ds_read_b128 v[200:203], v155 offset:53248
	ds_read_b128 v[204:207], v155 offset:54272
	ds_read_b128 v[208:211], v155 offset:55296
	ds_read_b128 v[212:215], v155 offset:56320
	s_waitcnt vmcnt(8)
	s_waitcnt lgkmcnt(0)
	s_barrier
	v_mfma_f32_16x16x32_bf16 v[62:65], v[146:149], v[184:187], v[62:65]
	v_mfma_f32_16x16x32_bf16 v[58:61], v[160:163], v[184:187], v[58:61]
	v_mfma_f32_16x16x32_bf16 v[46:49], v[146:149], v[192:195], v[46:49]
	v_mfma_f32_16x16x32_bf16 v[42:45], v[160:163], v[192:195], v[42:45]
	v_mfma_f32_16x16x32_bf16 v[30:33], v[146:149], v[200:203], v[30:33]
	v_mfma_f32_16x16x32_bf16 v[26:29], v[160:163], v[200:203], v[26:29]
	v_mfma_f32_16x16x32_bf16 v[14:17], v[146:149], v[208:211], v[14:17]
	v_mfma_f32_16x16x32_bf16 v[10:13], v[160:163], v[208:211], v[10:13]
	v_mfma_f32_16x16x32_bf16 v[62:65], v[156:159], v[188:191], v[62:65]
	v_mfma_f32_16x16x32_bf16 v[58:61], v[164:167], v[188:191], v[58:61]
	v_mfma_f32_16x16x32_bf16 v[46:49], v[156:159], v[196:199], v[46:49]
	v_mfma_f32_16x16x32_bf16 v[42:45], v[164:167], v[196:199], v[42:45]
	v_mfma_f32_16x16x32_bf16 v[30:33], v[156:159], v[204:207], v[30:33]
	v_mfma_f32_16x16x32_bf16 v[26:29], v[164:167], v[204:207], v[26:29]
	v_mfma_f32_16x16x32_bf16 v[14:17], v[156:159], v[212:215], v[14:17]
	v_mfma_f32_16x16x32_bf16 v[10:13], v[164:167], v[212:215], v[10:13]
	v_mfma_f32_16x16x32_bf16 v[54:57], v[168:171], v[184:187], v[54:57]
	v_mfma_f32_16x16x32_bf16 v[50:53], v[176:179], v[184:187], v[50:53]
	v_mfma_f32_16x16x32_bf16 v[38:41], v[168:171], v[192:195], v[38:41]
	v_mfma_f32_16x16x32_bf16 v[34:37], v[176:179], v[192:195], v[34:37]
	v_mfma_f32_16x16x32_bf16 v[22:25], v[168:171], v[200:203], v[22:25]
	v_mfma_f32_16x16x32_bf16 v[18:21], v[176:179], v[200:203], v[18:21]
	v_mfma_f32_16x16x32_bf16 v[6:9], v[168:171], v[208:211], v[6:9]
	v_mfma_f32_16x16x32_bf16 v[2:5], v[176:179], v[208:211], v[2:5]
	v_mfma_f32_16x16x32_bf16 v[54:57], v[172:175], v[188:191], v[54:57]
	v_mfma_f32_16x16x32_bf16 v[50:53], v[180:183], v[188:191], v[50:53]
	v_mfma_f32_16x16x32_bf16 v[38:41], v[172:175], v[196:199], v[38:41]
	v_mfma_f32_16x16x32_bf16 v[34:37], v[180:183], v[196:199], v[34:37]
	v_mfma_f32_16x16x32_bf16 v[22:25], v[172:175], v[204:207], v[22:25]
	v_mfma_f32_16x16x32_bf16 v[18:21], v[180:183], v[204:207], v[18:21]
	v_mfma_f32_16x16x32_bf16 v[6:9], v[172:175], v[212:215], v[6:9]
	v_mfma_f32_16x16x32_bf16 v[2:5], v[180:183], v[212:215], v[2:5]
	s_barrier
	s_add_i32 s51, s51, 2
	s_add_u32 s49, s49, 0x100
	s_addc_u32 s50, s50, 0
	s_cmp_gt_u32 s51, 41
	s_mov_b64 s[2:3], s[22:23]
	s_cbranch_scc0 .LBB0_1102
	s_and_b64 vcc, exec, s[14:15]
	s_cbranch_vccz .LBB0_1105
	s_barrier

; #define GM_STAGE(bufoff, gbase, voff) do { _Pragma("unroll") for (int _i = 0; _i < 2; ++_i) \
;         __builtin_amdgcn_global_load_lds((const unsigned*)((const char*)(gbase) + (voff)[_i]), (LAS unsigned*)(lds + (bufoff) + ldsw + _i * 8192), 16, 0, 0); } while (0)
; #define GM_LDA(dst, b, h) do { _Pragma("unroll") for (int m = 0; m < 4; ++m) _Pragma("unroll") for (int k = 0; k < 2; ++k) dst[m][k] = *(const LAS s16x8*)(lds + GM_SA(b, h) + aoff + m * 2048 + k * 1024); } while (0)
; #define GM_LDB(dst, b, h) do { _Pragma("unroll") for (int n = 0; n < 2; ++n) _Pragma("unroll") for (int k = 0; k < 2; ++k) dst[n][k] = *(const LAS s16x8*)(lds + GM_SB(b, h) + boff + n * 2048 + k * 1024); } while (0)
; #define GM_MMA(ai, bj, At, Bt) do { __builtin_amdgcn_s_setprio(1); _Pragma("unroll") for (int m = 0; m < 4; ++m) _Pragma("unroll") for (int n = 0; n < 2; ++n) _Pragma("unroll") for (int k = 0; k < 2; ++k) \
;         acc[ai][bj][m][n] = mma16<BF>(Bt[n][k], At[m][k], acc[ai][bj][m][n]); __builtin_amdgcn_s_setprio(0); } while (0)
; #define GM_WAIT_V(n) asm volatile("s_waitcnt vmcnt(" #n ")" ::: "memory")
; #define GM_WAIT_L(n) asm volatile("s_waitcnt lgkmcnt(" #n ")" ::: "memory")
; #define GM_BAR __builtin_amdgcn_s_barrier()
; template <bool BF, bool GATHER = false, class Epi, class Hook>
; __device__ __forceinline__ void gemm_phase(LAS unsigned char* lds, const Gemm g, const Order& S, const Epi& E, Hook& HK) {
;     ...
;         for (int t = 0; t < nt; t += 2) {
;             const bool last = (t == nt - 2);
;             const char* a1 = cA + (size_t)(t + 1) * kstep;
;             const char* a2 = last ? nA : cA + (size_t)(t + 2) * kstep; const char* b2 = last ? nB : cB + (size_t)(t + 2) * kstep;
;             const char* a3 = a2 + kstep; const char* b3 = b2 + kstep;
;             unsigned s0[2], s1[2];
;             if constexpr (GATHER) { s0[0] = last ? nA0[0] : gA0[0]; s0[1] = last ? nA0[1] : gA0[1]; s1[0] = last ? nA1[0] : gA1[0]; s1[1] = last ? nA1[1] : gA1[1]; }
;             GM_LDB(B0, 0, 0); GM_LDB(B1, 0, 1); GM_SCHED; GM_LDA(At, 0, 0); GM_STA_H1(GM_SA(1, 1), a1, gA1);
;             GM_WAIT_V(8); GM_WAIT_L(0); GM_BAR; GM_MMA(0, 0, At, B0); GM_MMA(0, 1, At, B1); GM_BAR; GM_SCHED;
;             GM_LDA(At, 0, 1); GM_STAGE(GM_SB(0, 0), b2, voffB); GM_STAGE(GM_SB(0, 1), b2 + hstepB, voffB); GM_STA_H0(GM_SA(0, 0), a2, s0);
.LBB0_1281:
	s_add_u32 s22, s20, 0xfffc0080
	s_addc_u32 s23, s21, -1
	s_cmp_eq_u32 s47, 12
	s_cselect_b32 s25, s3, s23
	s_cselect_b32 s24, s13, s22
	s_cselect_b32 s23, s15, s46
	s_cselect_b32 s22, s44, s45
	s_add_i32 m0, s30, 0xc000
	v_lshl_add_u64 v[218:219], s[20:21], 0, v[140:141]
	global_load_lds_dwordx4 v[218:219], off
	s_add_i32 m0, s30, 0xe000
	v_lshl_add_u64 v[218:219], s[20:21], 0, v[142:143]
	global_load_lds_dwordx4 v[218:219], off
	ds_read_b128 v[154:157], v151
	ds_read_b128 v[158:161], v151 offset:1024
	ds_read_b128 v[162:165], v151 offset:2048
	ds_read_b128 v[166:169], v151 offset:3072
	ds_read_b128 v[170:173], v152
	ds_read_b128 v[174:177], v152 offset:1024
	ds_read_b128 v[178:181], v152 offset:2048
	ds_read_b128 v[182:185], v152 offset:3072
	ds_read_b128 v[186:189], v153
	ds_read_b128 v[190:193], v153 offset:1024
	ds_read_b128 v[194:197], v153 offset:2048
	ds_read_b128 v[198:201], v153 offset:3072
	ds_read_b128 v[202:205], v153 offset:4096
	ds_read_b128 v[206:209], v153 offset:5120
	ds_read_b128 v[210:213], v153 offset:6144
	ds_read_b128 v[214:217], v153 offset:7168
	s_waitcnt vmcnt(8)
	s_waitcnt lgkmcnt(0)
	s_barrier
	v_mfma_f32_16x16x32_f16 v[126:129], v[154:157], v[186:189], v[126:129]
	v_mfma_f32_16x16x32_f16 v[118:121], v[162:165], v[186:189], v[118:121]
	v_mfma_f32_16x16x32_f16 v[110:113], v[154:157], v[194:197], v[110:113]
	v_mfma_f32_16x16x32_f16 v[102:105], v[162:165], v[194:197], v[102:105]
	v_mfma_f32_16x16x32_f16 v[94:97], v[154:157], v[202:205], v[94:97]
	v_mfma_f32_16x16x32_f16 v[86:89], v[162:165], v[202:205], v[86:89]
	v_mfma_f32_16x16x32_f16 v[78:81], v[154:157], v[210:213], v[78:81]
	v_mfma_f32_16x16x32_f16 v[70:73], v[162:165], v[210:213], v[70:73]
	v_mfma_f32_16x16x32_f16 v[126:129], v[158:161], v[190:193], v[126:129]
	v_mfma_f32_16x16x32_f16 v[118:121], v[166:169], v[190:193], v[118:121]
	v_mfma_f32_16x16x32_f16 v[110:113], v[158:161], v[198:201], v[110:113]
	v_mfma_f32_16x16x32_f16 v[102:105], v[166:169], v[198:201], v[102:105]
	v_mfma_f32_16x16x32_f16 v[94:97], v[158:161], v[206:209], v[94:97]
	v_mfma_f32_16x16x32_f16 v[86:89], v[166:169], v[206:209], v[86:89]
	v_mfma_f32_16x16x32_f16 v[78:81], v[158:161], v[214:217], v[78:81]
	v_mfma_f32_16x16x32_f16 v[70:73], v[166:169], v[214:217], v[70:73]
	v_mfma_f32_16x16x32_f16 v[122:125], v[170:173], v[186:189], v[122:125]
	v_mfma_f32_16x16x32_f16 v[114:117], v[178:181], v[186:189], v[114:117]
	v_mfma_f32_16x16x32_f16 v[106:109], v[170:173], v[194:197], v[106:109]
	v_mfma_f32_16x16x32_f16 v[98:101], v[178:181], v[194:197], v[98:101]
	v_mfma_f32_16x16x32_f16 v[90:93], v[170:173], v[202:205], v[90:93]
	v_mfma_f32_16x16x32_f16 v[82:85], v[178:181], v[202:205], v[82:85]
	v_mfma_f32_16x16x32_f16 v[74:77], v[170:173], v[210:213], v[74:77]
	v_mfma_f32_16x16x32_f16 v[66:69], v[178:181], v[210:213], v[66:69]
	v_mfma_f32_16x16x32_f16 v[122:125], v[174:177], v[190:193], v[122:125]
	v_mfma_f32_16x16x32_f16 v[114:117], v[182:185], v[190:193], v[114:117]
	v_mfma_f32_16x16x32_f16 v[106:109], v[174:177], v[198:201], v[106:109]
	v_mfma_f32_16x16x32_f16 v[98:101], v[182:185], v[198:201], v[98:101]
	v_mfma_f32_16x16x32_f16 v[90:93], v[174:177], v[206:209], v[90:93]
	v_mfma_f32_16x16x32_f16 v[82:85], v[182:185], v[206:209], v[82:85]
	v_mfma_f32_16x16x32_f16 v[74:77], v[174:177], v[214:217], v[74:77]
	v_mfma_f32_16x16x32_f16 v[66:69], v[182:185], v[214:217], v[66:69]
	s_barrier
	s_add_i32 s48, s40, s28
	s_mov_b32 m0, s48
	v_lshl_add_u64 v[218:219], s[22:23], 0, v[134:135]
	global_load_lds_dwordx4 v[218:219], off
	s_add_i32 m0, s48, 0x2000
	s_add_u32 s48, s22, 0x40000
	v_lshl_add_u64 v[220:221], s[22:23], 0, v[130:131]
	s_addc_u32 s49, s23, 0
	s_add_i32 s50, s41, s28
	global_load_lds_dwordx4 v[220:221], off
	v_lshl_add_u64 v[222:223], s[48:49], 0, v[134:135]
	s_mov_b32 m0, s50
	v_lshl_add_u64 v[224:225], s[24:25], 0, v[132:133]
	global_load_lds_dwordx4 v[222:223], off
	s_add_i32 m0, s50, 0x2000
	v_lshl_add_u64 v[222:223], s[48:49], 0, v[130:131]
	global_load_lds_dwordx4 v[222:223], off
	s_mov_b32 m0, s30
	v_lshl_add_u64 v[222:223], s[24:25], 0, v[136:137]
	global_load_lds_dwordx4 v[222:223], off
	s_mov_b32 m0, s31
	s_nop 0
	global_load_lds_dwordx4 v[224:225], off
	ds_read_b128 v[186:189], v153 offset:16384
	ds_read_b128 v[190:193], v153 offset:17408
	ds_read_b128 v[194:197], v153 offset:18432
	ds_read_b128 v[198:201], v153 offset:19456
	ds_read_b128 v[202:205], v153 offset:20480
	ds_read_b128 v[206:209], v153 offset:21504
	ds_read_b128 v[210:213], v153 offset:22528
	ds_read_b128 v[214:217], v153 offset:23552
	s_waitcnt vmcnt(8)
	s_waitcnt lgkmcnt(0)
	s_barrier
; #define GM_LDA(dst, b, h) do { _Pragma("unroll") for (int m = 0; m < 4; ++m) _Pragma("unroll") for (int k = 0; k < 2; ++k) dst[m][k] = *(const LAS s16x8*)(lds + GM_SA(b, h) + aoff + m * 2048 + k * 1024); } while (0)
; #define GM_LDB(dst, b, h) do { _Pragma("unroll") for (int n = 0; n < 2; ++n) _Pragma("unroll") for (int k = 0; k < 2; ++k) dst[n][k] = *(const LAS s16x8*)(lds + GM_SB(b, h) + boff + n * 2048 + k * 1024); } while (0)
; #define GM_MMA(ai, bj, At, Bt) do { __builtin_amdgcn_s_setprio(1); _Pragma("unroll") for (int m = 0; m < 4; ++m) _Pragma("unroll") for (int n = 0; n < 2; ++n) _Pragma("unroll") for (int k = 0; k < 2; ++k) \
;         acc[ai][bj][m][n] = mma16<BF>(Bt[n][k], At[m][k], acc[ai][bj][m][n]); __builtin_amdgcn_s_setprio(0); } while (0)
; #define GM_WAIT_V(n) asm volatile("s_waitcnt vmcnt(" #n ")" ::: "memory")
; #define GM_WAIT_L(n) asm volatile("s_waitcnt lgkmcnt(" #n ")" ::: "memory")
; #define GM_BAR __builtin_amdgcn_s_barrier()
; #define GM_SCHED __builtin_amdgcn_sched_barrier(0)
; #define GM_STA_H1(buf, p, o1) do { if constexpr (GATHER) GM_STAGE(buf, p, o1); else GM_STAGE(buf, (p) + hstepB, voffA); } while (0)
; template <bool BF, bool GATHER = false, class Epi, class Hook>
; __device__ __forceinline__ void gemm_phase(LAS unsigned char* lds, const Gemm g, const Order& S, const Epi& E, Hook& HK) {
;     ...
;             GM_WAIT_V(8); GM_WAIT_L(0); GM_BAR; GM_MMA(1, 0, At, B0); GM_MMA(1, 1, At, B1); GM_BAR; GM_SCHED;
;             GM_LDB(B0, 1, 0); GM_LDB(B1, 1, 1); GM_SCHED; GM_LDA(At, 1, 0); GM_STA_H1(GM_SA(0, 1), a2, s1);
;             GM_WAIT_V(8); GM_WAIT_L(0); GM_BAR; GM_MMA(0, 0, At, B0); GM_MMA(0, 1, At, B1); GM_BAR; GM_SCHED;
	v_mfma_f32_16x16x32_f16 v[62:65], v[154:157], v[186:189], v[62:65]
	v_mfma_f32_16x16x32_f16 v[54:57], v[162:165], v[186:189], v[54:57]
	v_mfma_f32_16x16x32_f16 v[46:49], v[154:157], v[194:197], v[46:49]
	v_mfma_f32_16x16x32_f16 v[38:41], v[162:165], v[194:197], v[38:41]
	v_mfma_f32_16x16x32_f16 v[30:33], v[154:157], v[202:205], v[30:33]
	v_mfma_f32_16x16x32_f16 v[22:25], v[162:165], v[202:205], v[22:25]
	v_mfma_f32_16x16x32_f16 v[14:17], v[154:157], v[210:213], v[14:17]
	v_mfma_f32_16x16x32_f16 v[6:9], v[162:165], v[210:213], v[6:9]
	v_mfma_f32_16x16x32_f16 v[62:65], v[158:161], v[190:193], v[62:65]
	v_mfma_f32_16x16x32_f16 v[54:57], v[166:169], v[190:193], v[54:57]
	v_mfma_f32_16x16x32_f16 v[46:49], v[158:161], v[198:201], v[46:49]
	v_mfma_f32_16x16x32_f16 v[38:41], v[166:169], v[198:201], v[38:41]
	v_mfma_f32_16x16x32_f16 v[30:33], v[158:161], v[206:209], v[30:33]
	v_mfma_f32_16x16x32_f16 v[22:25], v[166:169], v[206:209], v[22:25]
	v_mfma_f32_16x16x32_f16 v[14:17], v[158:161], v[214:217], v[14:17]
	v_mfma_f32_16x16x32_f16 v[6:9], v[166:169], v[214:217], v[6:9]
	v_mfma_f32_16x16x32_f16 v[58:61], v[170:173], v[186:189], v[58:61]
	v_mfma_f32_16x16x32_f16 v[50:53], v[178:181], v[186:189], v[50:53]
	v_mfma_f32_16x16x32_f16 v[42:45], v[170:173], v[194:197], v[42:45]
	v_mfma_f32_16x16x32_f16 v[34:37], v[178:181], v[194:197], v[34:37]
	v_mfma_f32_16x16x32_f16 v[26:29], v[170:173], v[202:205], v[26:29]
	v_mfma_f32_16x16x32_f16 v[18:21], v[178:181], v[202:205], v[18:21]
	v_mfma_f32_16x16x32_f16 v[10:13], v[170:173], v[210:213], v[10:13]
	v_mfma_f32_16x16x32_f16 v[2:5], v[178:181], v[210:213], v[2:5]
	v_mfma_f32_16x16x32_f16 v[58:61], v[174:177], v[190:193], v[58:61]
	v_mfma_f32_16x16x32_f16 v[50:53], v[182:185], v[190:193], v[50:53]
	v_mfma_f32_16x16x32_f16 v[42:45], v[174:177], v[198:201], v[42:45]
	v_mfma_f32_16x16x32_f16 v[34:37], v[182:185], v[198:201], v[34:37]
	v_mfma_f32_16x16x32_f16 v[26:29], v[174:177], v[206:209], v[26:29]
	v_mfma_f32_16x16x32_f16 v[18:21], v[182:185], v[206:209], v[18:21]
	v_mfma_f32_16x16x32_f16 v[10:13], v[174:177], v[214:217], v[10:13]
	v_mfma_f32_16x16x32_f16 v[2:5], v[182:185], v[214:217], v[2:5]
	s_barrier
	s_add_u32 s24, s24, 0x40000
	s_addc_u32 s25, s25, 0
	s_mov_b32 m0, s33
	v_lshl_add_u64 v[226:227], s[24:25], 0, v[136:137]
	global_load_lds_dwordx4 v[226:227], off
	s_mov_b32 m0, s34
	v_lshl_add_u64 v[226:227], s[24:25], 0, v[132:133]
	global_load_lds_dwordx4 v[226:227], off
	s_mov_b32 s49, 0x1c000
	s_mov_b32 s48, 0x18000
	v_add_u32_e32 v244, s48, v148
	ds_read_b128 v[154:157], v244
	ds_read_b128 v[158:161], v244 offset:1024
	ds_read_b128 v[162:165], v244 offset:2048
	ds_read_b128 v[166:169], v244 offset:3072
	v_add_u32_e32 v244, s49, v148
	ds_read_b128 v[170:173], v244
	ds_read_b128 v[174:177], v244 offset:1024
	ds_read_b128 v[178:181], v244 offset:2048
	ds_read_b128 v[182:185], v244 offset:3072
	ds_read_b128 v[186:189], v153 offset:32768
	ds_read_b128 v[190:193], v153 offset:33792
	ds_read_b128 v[194:197], v153 offset:34816
	ds_read_b128 v[198:201], v153 offset:35840
	ds_read_b128 v[202:205], v153 offset:36864
	ds_read_b128 v[206:209], v153 offset:37888
	ds_read_b128 v[210:213], v153 offset:38912
	ds_read_b128 v[214:217], v153 offset:39936
	s_waitcnt vmcnt(8)
	s_waitcnt lgkmcnt(0)
	s_barrier
	v_mfma_f32_16x16x32_f16 v[126:129], v[154:157], v[186:189], v[126:129]
	v_mfma_f32_16x16x32_f16 v[118:121], v[162:165], v[186:189], v[118:121]
	v_mfma_f32_16x16x32_f16 v[110:113], v[154:157], v[194:197], v[110:113]
	v_mfma_f32_16x16x32_f16 v[102:105], v[162:165], v[194:197], v[102:105]
	v_mfma_f32_16x16x32_f16 v[94:97], v[154:157], v[202:205], v[94:97]
	v_mfma_f32_16x16x32_f16 v[86:89], v[162:165], v[202:205], v[86:89]
	v_mfma_f32_16x16x32_f16 v[78:81], v[154:157], v[210:213], v[78:81]
	v_mfma_f32_16x16x32_f16 v[70:73], v[162:165], v[210:213], v[70:73]
	v_mfma_f32_16x16x32_f16 v[126:129], v[158:161], v[190:193], v[126:129]
	v_mfma_f32_16x16x32_f16 v[118:121], v[166:169], v[190:193], v[118:121]
	v_mfma_f32_16x16x32_f16 v[110:113], v[158:161], v[198:201], v[110:113]
	v_mfma_f32_16x16x32_f16 v[102:105], v[166:169], v[198:201], v[102:105]
	v_mfma_f32_16x16x32_f16 v[94:97], v[158:161], v[206:209], v[94:97]
	v_mfma_f32_16x16x32_f16 v[86:89], v[166:169], v[206:209], v[86:89]
	v_mfma_f32_16x16x32_f16 v[78:81], v[158:161], v[214:217], v[78:81]
	v_mfma_f32_16x16x32_f16 v[70:73], v[166:169], v[214:217], v[70:73]
	v_mfma_f32_16x16x32_f16 v[122:125], v[170:173], v[186:189], v[122:125]
	v_mfma_f32_16x16x32_f16 v[114:117], v[178:181], v[186:189], v[114:117]
	v_mfma_f32_16x16x32_f16 v[106:109], v[170:173], v[194:197], v[106:109]
	v_mfma_f32_16x16x32_f16 v[98:101], v[178:181], v[194:197], v[98:101]
	v_mfma_f32_16x16x32_f16 v[90:93], v[170:173], v[202:205], v[90:93]
	v_mfma_f32_16x16x32_f16 v[82:85], v[178:181], v[202:205], v[82:85]
	v_mfma_f32_16x16x32_f16 v[74:77], v[170:173], v[210:213], v[74:77]
	v_mfma_f32_16x16x32_f16 v[66:69], v[178:181], v[210:213], v[66:69]
	v_mfma_f32_16x16x32_f16 v[122:125], v[174:177], v[190:193], v[122:125]
	v_mfma_f32_16x16x32_f16 v[114:117], v[182:185], v[190:193], v[114:117]
	v_mfma_f32_16x16x32_f16 v[106:109], v[174:177], v[198:201], v[106:109]
	v_mfma_f32_16x16x32_f16 v[98:101], v[182:185], v[198:201], v[98:101]
	v_mfma_f32_16x16x32_f16 v[90:93], v[174:177], v[206:209], v[90:93]
	v_mfma_f32_16x16x32_f16 v[82:85], v[182:185], v[206:209], v[82:85]
	v_mfma_f32_16x16x32_f16 v[74:77], v[174:177], v[214:217], v[74:77]
	v_mfma_f32_16x16x32_f16 v[66:69], v[182:185], v[214:217], v[66:69]
	s_barrier
; #define GM_STAGE(bufoff, gbase, voff) do { _Pragma("unroll") for (int _i = 0; _i < 2; ++_i) \
;         __builtin_amdgcn_global_load_lds((const unsigned*)((const char*)(gbase) + (voff)[_i]), (LAS unsigned*)(lds + (bufoff) + ldsw + _i * 8192), 16, 0, 0); } while (0)
; #define GM_LDA(dst, b, h) do { _Pragma("unroll") for (int m = 0; m < 4; ++m) _Pragma("unroll") for (int k = 0; k < 2; ++k) dst[m][k] = *(const LAS s16x8*)(lds + GM_SA(b, h) + aoff + m * 2048 + k * 1024); } while (0)
; #define GM_MMA(ai, bj, At, Bt) do { __builtin_amdgcn_s_setprio(1); _Pragma("unroll") for (int m = 0; m < 4; ++m) _Pragma("unroll") for (int n = 0; n < 2; ++n) _Pragma("unroll") for (int k = 0; k < 2; ++k) \
;         acc[ai][bj][m][n] = mma16<BF>(Bt[n][k], At[m][k], acc[ai][bj][m][n]); __builtin_amdgcn_s_setprio(0); } while (0)
; #define GM_WAIT_V(n) asm volatile("s_waitcnt vmcnt(" #n ")" ::: "memory")
; #define GM_WAIT_L(n) asm volatile("s_waitcnt lgkmcnt(" #n ")" ::: "memory")
; #define GM_BAR __builtin_amdgcn_s_barrier()
; #define GM_SCHED __builtin_amdgcn_sched_barrier(0)
; #define GM_STA_H0(buf, p, o0) do { if constexpr (GATHER) GM_STAGE(buf, p, o0); else GM_STAGE(buf, p, voffA); } while (0)
;     __device__ __forceinline__ void operator()() { if (cnt == turn) run_all(tid_); ++cnt; }
;     __device__ __forceinline__ void operator()(const Acc& acc, const Unit& u, int wr, int wc, int fr, int fq) const {
;         const int row0 = u.pm * BM + wr * 64 + fr;
;         if (u.pn < 8) {
;             const int col0 = (u.pn < 4 ? 0 : 512) + 128 * (u.pn & 3) + wc * 32 + 8 * fq; const bool glu = u.pn >= 4;
; template <bool BF, bool GATHER = false, class Epi, class Hook>
; __device__ __forceinline__ void gemm_phase(LAS unsigned char* lds, const Gemm g, const Order& S, const Epi& E, Hook& HK) {
;     ...
;             GM_LDA(At, 1, 1); GM_STAGE(GM_SB(1, 0), b3, voffB); GM_STAGE(GM_SB(1, 1), b3 + hstepB, voffB); GM_STA_H0(GM_SA(1, 0), a3, s0);
;             GM_WAIT_V(8); GM_WAIT_L(0); GM_BAR; GM_MMA(1, 0, At, B0); GM_MMA(1, 1, At, B1); GM_BAR; GM_SCHED;
;         }
;         if (wr == 0) GM_BAR;
	s_add_i32 s24, s48, s28
	s_mov_b32 m0, s24
	v_lshl_add_u64 v[218:219], v[218:219], 0, s[8:9]
	global_load_lds_dwordx4 v[218:219], off
	s_add_i32 m0, s24, 0x2000
	s_add_u32 s22, s22, 0x40080
	v_lshl_add_u64 v[218:219], v[220:221], 0, s[8:9]
	s_addc_u32 s23, s23, 0
	s_add_i32 s24, s49, s28
	global_load_lds_dwordx4 v[218:219], off
	s_mov_b32 m0, s24
	v_lshl_add_u64 v[218:219], s[22:23], 0, v[134:135]
	global_load_lds_dwordx4 v[218:219], off
	s_add_i32 m0, s24, 0x2000
	v_lshl_add_u64 v[218:219], s[22:23], 0, v[130:131]
	global_load_lds_dwordx4 v[218:219], off
	s_mov_b32 m0, s37
	v_lshl_add_u64 v[218:219], v[222:223], 0, s[8:9]
	global_load_lds_dwordx4 v[218:219], off
	s_mov_b32 m0, s38
	v_lshl_add_u64 v[218:219], v[224:225], 0, s[8:9]
	global_load_lds_dwordx4 v[218:219], off
	ds_read_b128 v[186:189], v153 offset:49152
	ds_read_b128 v[190:193], v153 offset:50176
	ds_read_b128 v[194:197], v153 offset:51200
	ds_read_b128 v[198:201], v153 offset:52224
	ds_read_b128 v[202:205], v153 offset:53248
	ds_read_b128 v[206:209], v153 offset:54272
	ds_read_b128 v[210:213], v153 offset:55296
	ds_read_b128 v[214:217], v153 offset:56320
	s_waitcnt vmcnt(8)
	s_waitcnt lgkmcnt(0)
	s_barrier
	v_mfma_f32_16x16x32_f16 v[62:65], v[154:157], v[186:189], v[62:65]
	v_mfma_f32_16x16x32_f16 v[54:57], v[162:165], v[186:189], v[54:57]
	v_mfma_f32_16x16x32_f16 v[46:49], v[154:157], v[194:197], v[46:49]
	v_mfma_f32_16x16x32_f16 v[38:41], v[162:165], v[194:197], v[38:41]
	v_mfma_f32_16x16x32_f16 v[30:33], v[154:157], v[202:205], v[30:33]
	v_mfma_f32_16x16x32_f16 v[22:25], v[162:165], v[202:205], v[22:25]
	v_mfma_f32_16x16x32_f16 v[14:17], v[154:157], v[210:213], v[14:17]
	v_mfma_f32_16x16x32_f16 v[6:9], v[162:165], v[210:213], v[6:9]
	v_mfma_f32_16x16x32_f16 v[62:65], v[158:161], v[190:193], v[62:65]
	v_mfma_f32_16x16x32_f16 v[54:57], v[166:169], v[190:193], v[54:57]
	v_mfma_f32_16x16x32_f16 v[46:49], v[158:161], v[198:201], v[46:49]
	v_mfma_f32_16x16x32_f16 v[38:41], v[166:169], v[198:201], v[38:41]
	v_mfma_f32_16x16x32_f16 v[30:33], v[158:161], v[206:209], v[30:33]
	v_mfma_f32_16x16x32_f16 v[22:25], v[166:169], v[206:209], v[22:25]
	v_mfma_f32_16x16x32_f16 v[14:17], v[158:161], v[214:217], v[14:17]
	v_mfma_f32_16x16x32_f16 v[6:9], v[166:169], v[214:217], v[6:9]
	v_mfma_f32_16x16x32_f16 v[58:61], v[170:173], v[186:189], v[58:61]
	v_mfma_f32_16x16x32_f16 v[50:53], v[178:181], v[186:189], v[50:53]
	v_mfma_f32_16x16x32_f16 v[42:45], v[170:173], v[194:197], v[42:45]
	v_mfma_f32_16x16x32_f16 v[34:37], v[178:181], v[194:197], v[34:37]
	v_mfma_f32_16x16x32_f16 v[26:29], v[170:173], v[202:205], v[26:29]
	v_mfma_f32_16x16x32_f16 v[18:21], v[178:181], v[202:205], v[18:21]
	v_mfma_f32_16x16x32_f16 v[10:13], v[170:173], v[210:213], v[10:13]
	v_mfma_f32_16x16x32_f16 v[2:5], v[178:181], v[210:213], v[2:5]
	v_mfma_f32_16x16x32_f16 v[58:61], v[174:177], v[190:193], v[58:61]
	v_mfma_f32_16x16x32_f16 v[50:53], v[182:185], v[190:193], v[50:53]
	v_mfma_f32_16x16x32_f16 v[42:45], v[174:177], v[198:201], v[42:45]
	v_mfma_f32_16x16x32_f16 v[34:37], v[182:185], v[198:201], v[34:37]
	v_mfma_f32_16x16x32_f16 v[26:29], v[174:177], v[206:209], v[26:29]
	v_mfma_f32_16x16x32_f16 v[18:21], v[182:185], v[206:209], v[18:21]
	v_mfma_f32_16x16x32_f16 v[10:13], v[174:177], v[214:217], v[10:13]
	v_mfma_f32_16x16x32_f16 v[2:5], v[182:185], v[214:217], v[2:5]
	s_barrier
	s_add_i32 s47, s47, 2
	s_add_u32 s20, s20, 0x100
	s_addc_u32 s21, s21, 0
	s_add_u32 s45, s45, 0x100
	s_addc_u32 s46, s46, 0
	s_cmp_gt_u32 s47, 13
	s_cbranch_scc0 .LBB0_1281
	s_and_b64 vcc, exec, s[10:11]
	s_cbranch_vccnz .LBB0_1286
	v_lshl_add_u32 v154, s2, 8, v1
	s_cmp_gt_i32 s43, 7
	s_mov_b64 s[2:3], -1
	s_cbranch_scc1 .LBB0_1287

; #define GM_STAGE(bufoff, gbase, voff) do { _Pragma("unroll") for (int _i = 0; _i < 2; ++_i) \
;         __builtin_amdgcn_global_load_lds((const unsigned*)((const char*)(gbase) + (voff)[_i]), (LAS unsigned*)(lds + (bufoff) + ldsw + _i * 8192), 16, 0, 0); } while (0)
; #define GM_LDA(dst, b, h) do { _Pragma("unroll") for (int m = 0; m < 4; ++m) _Pragma("unroll") for (int k = 0; k < 2; ++k) dst[m][k] = *(const LAS s16x8*)(lds + GM_SA(b, h) + aoff + m * 2048 + k * 1024); } while (0)
; #define GM_LDB(dst, b, h) do { _Pragma("unroll") for (int n = 0; n < 2; ++n) _Pragma("unroll") for (int k = 0; k < 2; ++k) dst[n][k] = *(const LAS s16x8*)(lds + GM_SB(b, h) + boff + n * 2048 + k * 1024); } while (0)
; #define GM_MMA(ai, bj, At, Bt) do { __builtin_amdgcn_s_setprio(1); _Pragma("unroll") for (int m = 0; m < 4; ++m) _Pragma("unroll") for (int n = 0; n < 2; ++n) _Pragma("unroll") for (int k = 0; k < 2; ++k) \
;         acc[ai][bj][m][n] = mma16<BF>(Bt[n][k], At[m][k], acc[ai][bj][m][n]); __builtin_amdgcn_s_setprio(0); } while (0)
; #define GM_WAIT_V(n) asm volatile("s_waitcnt vmcnt(" #n ")" ::: "memory")
; #define GM_WAIT_L(n) asm volatile("s_waitcnt lgkmcnt(" #n ")" ::: "memory")
; #define GM_BAR __builtin_amdgcn_s_barrier()
; template <bool BF, bool GATHER = false, class Epi, class Hook>
; __device__ __forceinline__ void gemm_phase(LAS unsigned char* lds, const Gemm g, const Order& S, const Epi& E, Hook& HK) {
;     ...
;         for (int t = 0; t < nt; t += 2) {
;             const bool last = (t == nt - 2);
;             const char* a1 = cA + (size_t)(t + 1) * kstep;
;             const char* a2 = last ? nA : cA + (size_t)(t + 2) * kstep; const char* b2 = last ? nB : cB + (size_t)(t + 2) * kstep;
;             const char* a3 = a2 + kstep; const char* b3 = b2 + kstep;
;             unsigned s0[2], s1[2];
;             if constexpr (GATHER) { s0[0] = last ? nA0[0] : gA0[0]; s0[1] = last ? nA0[1] : gA0[1]; s1[0] = last ? nA1[0] : gA1[0]; s1[1] = last ? nA1[1] : gA1[1]; }
;             GM_LDB(B0, 0, 0); GM_LDB(B1, 0, 1); GM_SCHED; GM_LDA(At, 0, 0); GM_STA_H1(GM_SA(1, 1), a1, gA1);
;             GM_WAIT_V(8); GM_WAIT_L(0); GM_BAR; GM_MMA(0, 0, At, B0); GM_MMA(0, 1, At, B1); GM_BAR; GM_SCHED;
;             GM_LDA(At, 0, 1); GM_STAGE(GM_SB(0, 0), b2, voffB); GM_STAGE(GM_SB(0, 1), b2 + hstepB, voffB); GM_STA_H0(GM_SA(0, 0), a2, s0);
.LBB0_1480:
	s_add_u32 s24, s22, 0xfffc0080
	s_addc_u32 s25, s23, -1
	s_cmp_eq_u32 s49, 12
	s_cselect_b32 s27, s15, s25
	s_cselect_b32 s26, s45, s24
	s_cselect_b32 s25, s17, s48
	s_cselect_b32 s24, s46, s47
	s_add_i32 m0, s33, 0xc000
	v_lshl_add_u64 v[216:217], s[22:23], 0, v[154:155]
	global_load_lds_dwordx4 v[216:217], off
	s_add_i32 m0, s33, 0xe000
	v_lshl_add_u64 v[216:217], s[22:23], 0, v[156:157]
	global_load_lds_dwordx4 v[216:217], off
	ds_read_b128 v[122:125], v168
	ds_read_b128 v[126:129], v168 offset:1024
	ds_read_b128 v[130:133], v168 offset:2048
	ds_read_b128 v[134:137], v168 offset:3072
	ds_read_b128 v[162:165], v169
	ds_read_b128 v[172:175], v169 offset:1024
	ds_read_b128 v[176:179], v169 offset:2048
	ds_read_b128 v[180:183], v169 offset:3072
	ds_read_b128 v[184:187], v170
	ds_read_b128 v[188:191], v170 offset:1024
	ds_read_b128 v[192:195], v170 offset:2048
	ds_read_b128 v[196:199], v170 offset:3072
	ds_read_b128 v[200:203], v170 offset:4096
	ds_read_b128 v[204:207], v170 offset:5120
	ds_read_b128 v[208:211], v170 offset:6144
	ds_read_b128 v[212:215], v170 offset:7168
	s_waitcnt vmcnt(8)
	s_waitcnt lgkmcnt(0)
	s_barrier
	v_mfma_f32_16x16x32_f16 v[142:145], v[122:125], v[184:187], v[142:145]
	v_mfma_f32_16x16x32_f16 v[138:141], v[130:133], v[184:187], v[138:141]
	v_mfma_f32_16x16x32_f16 v[110:113], v[122:125], v[192:195], v[110:113]
	v_mfma_f32_16x16x32_f16 v[106:109], v[130:133], v[192:195], v[106:109]
	v_mfma_f32_16x16x32_f16 v[94:97], v[122:125], v[200:203], v[94:97]
	v_mfma_f32_16x16x32_f16 v[90:93], v[130:133], v[200:203], v[90:93]
	v_mfma_f32_16x16x32_f16 v[78:81], v[122:125], v[208:211], v[78:81]
	v_mfma_f32_16x16x32_f16 v[74:77], v[130:133], v[208:211], v[74:77]
	v_mfma_f32_16x16x32_f16 v[142:145], v[126:129], v[188:191], v[142:145]
	v_mfma_f32_16x16x32_f16 v[138:141], v[134:137], v[188:191], v[138:141]
	v_mfma_f32_16x16x32_f16 v[110:113], v[126:129], v[196:199], v[110:113]
	v_mfma_f32_16x16x32_f16 v[106:109], v[134:137], v[196:199], v[106:109]
	v_mfma_f32_16x16x32_f16 v[94:97], v[126:129], v[204:207], v[94:97]
	v_mfma_f32_16x16x32_f16 v[90:93], v[134:137], v[204:207], v[90:93]
	v_mfma_f32_16x16x32_f16 v[78:81], v[126:129], v[212:215], v[78:81]
	v_mfma_f32_16x16x32_f16 v[74:77], v[134:137], v[212:215], v[74:77]
	v_mfma_f32_16x16x32_f16 v[118:121], v[162:165], v[184:187], v[118:121]
	v_mfma_f32_16x16x32_f16 v[114:117], v[176:179], v[184:187], v[114:117]
	v_mfma_f32_16x16x32_f16 v[102:105], v[162:165], v[192:195], v[102:105]
	v_mfma_f32_16x16x32_f16 v[98:101], v[176:179], v[192:195], v[98:101]
	v_mfma_f32_16x16x32_f16 v[86:89], v[162:165], v[200:203], v[86:89]
	v_mfma_f32_16x16x32_f16 v[82:85], v[176:179], v[200:203], v[82:85]
	v_mfma_f32_16x16x32_f16 v[70:73], v[162:165], v[208:211], v[70:73]
	v_mfma_f32_16x16x32_f16 v[66:69], v[176:179], v[208:211], v[66:69]
	v_mfma_f32_16x16x32_f16 v[118:121], v[172:175], v[188:191], v[118:121]
	v_mfma_f32_16x16x32_f16 v[114:117], v[180:183], v[188:191], v[114:117]
	v_mfma_f32_16x16x32_f16 v[102:105], v[172:175], v[196:199], v[102:105]
	v_mfma_f32_16x16x32_f16 v[98:101], v[180:183], v[196:199], v[98:101]
	v_mfma_f32_16x16x32_f16 v[86:89], v[172:175], v[204:207], v[86:89]
	v_mfma_f32_16x16x32_f16 v[82:85], v[180:183], v[204:207], v[82:85]
	v_mfma_f32_16x16x32_f16 v[70:73], v[172:175], v[212:215], v[70:73]
	v_mfma_f32_16x16x32_f16 v[66:69], v[180:183], v[212:215], v[66:69]
	s_barrier
	s_add_i32 s50, s43, s31
	s_mov_b32 m0, s50
	v_lshl_add_u64 v[216:217], s[24:25], 0, v[148:149]
	global_load_lds_dwordx4 v[216:217], off
	s_add_i32 m0, s50, 0x2000
	s_add_u32 s50, s24, 0x40000
	v_lshl_add_u64 v[218:219], s[24:25], 0, v[152:153]
	s_addc_u32 s51, s25, 0
	s_add_i32 s52, s44, s31
	global_load_lds_dwordx4 v[218:219], off
	v_lshl_add_u64 v[220:221], s[50:51], 0, v[148:149]
	s_mov_b32 m0, s52
	v_lshl_add_u64 v[222:223], s[26:27], 0, v[150:151]
	global_load_lds_dwordx4 v[220:221], off
	s_add_i32 m0, s52, 0x2000
	v_lshl_add_u64 v[220:221], s[50:51], 0, v[152:153]
	global_load_lds_dwordx4 v[220:221], off
	s_mov_b32 m0, s33
	v_lshl_add_u64 v[220:221], s[26:27], 0, v[146:147]
	global_load_lds_dwordx4 v[220:221], off
	s_mov_b32 m0, s34
	s_nop 0
	global_load_lds_dwordx4 v[222:223], off
	ds_read_b128 v[184:187], v170 offset:16384
	ds_read_b128 v[188:191], v170 offset:17408
	ds_read_b128 v[192:195], v170 offset:18432
	ds_read_b128 v[196:199], v170 offset:19456
	ds_read_b128 v[200:203], v170 offset:20480
	ds_read_b128 v[204:207], v170 offset:21504
	ds_read_b128 v[208:211], v170 offset:22528
	ds_read_b128 v[212:215], v170 offset:23552
	s_waitcnt vmcnt(8)
	s_waitcnt lgkmcnt(0)
	s_barrier
; #define GM_LDA(dst, b, h) do { _Pragma("unroll") for (int m = 0; m < 4; ++m) _Pragma("unroll") for (int k = 0; k < 2; ++k) dst[m][k] = *(const LAS s16x8*)(lds + GM_SA(b, h) + aoff + m * 2048 + k * 1024); } while (0)
; #define GM_LDB(dst, b, h) do { _Pragma("unroll") for (int n = 0; n < 2; ++n) _Pragma("unroll") for (int k = 0; k < 2; ++k) dst[n][k] = *(const LAS s16x8*)(lds + GM_SB(b, h) + boff + n * 2048 + k * 1024); } while (0)
; #define GM_MMA(ai, bj, At, Bt) do { __builtin_amdgcn_s_setprio(1); _Pragma("unroll") for (int m = 0; m < 4; ++m) _Pragma("unroll") for (int n = 0; n < 2; ++n) _Pragma("unroll") for (int k = 0; k < 2; ++k) \
;         acc[ai][bj][m][n] = mma16<BF>(Bt[n][k], At[m][k], acc[ai][bj][m][n]); __builtin_amdgcn_s_setprio(0); } while (0)
; #define GM_WAIT_V(n) asm volatile("s_waitcnt vmcnt(" #n ")" ::: "memory")
; #define GM_WAIT_L(n) asm volatile("s_waitcnt lgkmcnt(" #n ")" ::: "memory")
; #define GM_BAR __builtin_amdgcn_s_barrier()
; #define GM_SCHED __builtin_amdgcn_sched_barrier(0)
; #define GM_STA_H1(buf, p, o1) do { if constexpr (GATHER) GM_STAGE(buf, p, o1); else GM_STAGE(buf, (p) + hstepB, voffA); } while (0)
; template <bool BF, bool GATHER = false, class Epi, class Hook>
; __device__ __forceinline__ void gemm_phase(LAS unsigned char* lds, const Gemm g, const Order& S, const Epi& E, Hook& HK) {
;     ...
;             GM_WAIT_V(8); GM_WAIT_L(0); GM_BAR; GM_MMA(1, 0, At, B0); GM_MMA(1, 1, At, B1); GM_BAR; GM_SCHED;
;             GM_LDB(B0, 1, 0); GM_LDB(B1, 1, 1); GM_SCHED; GM_LDA(At, 1, 0); GM_STA_H1(GM_SA(0, 1), a2, s1);
;             GM_WAIT_V(8); GM_WAIT_L(0); GM_BAR; GM_MMA(0, 0, At, B0); GM_MMA(0, 1, At, B1); GM_BAR; GM_SCHED;
	v_mfma_f32_16x16x32_f16 v[62:65], v[122:125], v[184:187], v[62:65]
	v_mfma_f32_16x16x32_f16 v[58:61], v[130:133], v[184:187], v[58:61]
	v_mfma_f32_16x16x32_f16 v[46:49], v[122:125], v[192:195], v[46:49]
	v_mfma_f32_16x16x32_f16 v[42:45], v[130:133], v[192:195], v[42:45]
	v_mfma_f32_16x16x32_f16 v[30:33], v[122:125], v[200:203], v[30:33]
	v_mfma_f32_16x16x32_f16 v[26:29], v[130:133], v[200:203], v[26:29]
	v_mfma_f32_16x16x32_f16 v[14:17], v[122:125], v[208:211], v[14:17]
	v_mfma_f32_16x16x32_f16 v[10:13], v[130:133], v[208:211], v[10:13]
	v_mfma_f32_16x16x32_f16 v[62:65], v[126:129], v[188:191], v[62:65]
	v_mfma_f32_16x16x32_f16 v[58:61], v[134:137], v[188:191], v[58:61]
	v_mfma_f32_16x16x32_f16 v[46:49], v[126:129], v[196:199], v[46:49]
	v_mfma_f32_16x16x32_f16 v[42:45], v[134:137], v[196:199], v[42:45]
	v_mfma_f32_16x16x32_f16 v[30:33], v[126:129], v[204:207], v[30:33]
	v_mfma_f32_16x16x32_f16 v[26:29], v[134:137], v[204:207], v[26:29]
	v_mfma_f32_16x16x32_f16 v[14:17], v[126:129], v[212:215], v[14:17]
	v_mfma_f32_16x16x32_f16 v[10:13], v[134:137], v[212:215], v[10:13]
	v_mfma_f32_16x16x32_f16 v[54:57], v[162:165], v[184:187], v[54:57]
	v_mfma_f32_16x16x32_f16 v[50:53], v[176:179], v[184:187], v[50:53]
	v_mfma_f32_16x16x32_f16 v[38:41], v[162:165], v[192:195], v[38:41]
	v_mfma_f32_16x16x32_f16 v[34:37], v[176:179], v[192:195], v[34:37]
	v_mfma_f32_16x16x32_f16 v[22:25], v[162:165], v[200:203], v[22:25]
	v_mfma_f32_16x16x32_f16 v[18:21], v[176:179], v[200:203], v[18:21]
	v_mfma_f32_16x16x32_f16 v[6:9], v[162:165], v[208:211], v[6:9]
	v_mfma_f32_16x16x32_f16 v[2:5], v[176:179], v[208:211], v[2:5]
	v_mfma_f32_16x16x32_f16 v[54:57], v[172:175], v[188:191], v[54:57]
	v_mfma_f32_16x16x32_f16 v[50:53], v[180:183], v[188:191], v[50:53]
	v_mfma_f32_16x16x32_f16 v[38:41], v[172:175], v[196:199], v[38:41]
	v_mfma_f32_16x16x32_f16 v[34:37], v[180:183], v[196:199], v[34:37]
	v_mfma_f32_16x16x32_f16 v[22:25], v[172:175], v[204:207], v[22:25]
	v_mfma_f32_16x16x32_f16 v[18:21], v[180:183], v[204:207], v[18:21]
	v_mfma_f32_16x16x32_f16 v[6:9], v[172:175], v[212:215], v[6:9]
	v_mfma_f32_16x16x32_f16 v[2:5], v[180:183], v[212:215], v[2:5]
	s_barrier
	s_add_u32 s26, s26, 0x40000
	s_addc_u32 s27, s27, 0
	s_mov_b32 m0, s35
	v_lshl_add_u64 v[224:225], s[26:27], 0, v[146:147]
	global_load_lds_dwordx4 v[224:225], off
	s_mov_b32 m0, s36
	v_lshl_add_u64 v[224:225], s[26:27], 0, v[150:151]
	global_load_lds_dwordx4 v[224:225], off
	s_mov_b32 s51, 0x1c000
	s_mov_b32 s50, 0x18000
	v_add_u32_e32 v244, s50, v166
	v_add_u32_e32 v245, s51, v166
	ds_read_b128 v[122:125], v244
	ds_read_b128 v[126:129], v244 offset:1024
	ds_read_b128 v[130:133], v244 offset:2048
	ds_read_b128 v[134:137], v244 offset:3072
	ds_read_b128 v[162:165], v245
	ds_read_b128 v[172:175], v245 offset:1024
	ds_read_b128 v[176:179], v245 offset:2048
	ds_read_b128 v[180:183], v245 offset:3072
	ds_read_b128 v[184:187], v170 offset:32768
	ds_read_b128 v[188:191], v170 offset:33792
	ds_read_b128 v[192:195], v170 offset:34816
	ds_read_b128 v[196:199], v170 offset:35840
	ds_read_b128 v[200:203], v170 offset:36864
	ds_read_b128 v[204:207], v170 offset:37888
	ds_read_b128 v[208:211], v170 offset:38912
	ds_read_b128 v[212:215], v170 offset:39936
	s_waitcnt vmcnt(8)
	s_waitcnt lgkmcnt(0)
	s_barrier
	v_mfma_f32_16x16x32_f16 v[142:145], v[122:125], v[184:187], v[142:145]
	v_mfma_f32_16x16x32_f16 v[138:141], v[130:133], v[184:187], v[138:141]
	v_mfma_f32_16x16x32_f16 v[110:113], v[122:125], v[192:195], v[110:113]
	v_mfma_f32_16x16x32_f16 v[106:109], v[130:133], v[192:195], v[106:109]
	v_mfma_f32_16x16x32_f16 v[94:97], v[122:125], v[200:203], v[94:97]
	v_mfma_f32_16x16x32_f16 v[90:93], v[130:133], v[200:203], v[90:93]
	v_mfma_f32_16x16x32_f16 v[78:81], v[122:125], v[208:211], v[78:81]
	v_mfma_f32_16x16x32_f16 v[74:77], v[130:133], v[208:211], v[74:77]
	v_mfma_f32_16x16x32_f16 v[142:145], v[126:129], v[188:191], v[142:145]
	v_mfma_f32_16x16x32_f16 v[138:141], v[134:137], v[188:191], v[138:141]
	v_mfma_f32_16x16x32_f16 v[110:113], v[126:129], v[196:199], v[110:113]
	v_mfma_f32_16x16x32_f16 v[106:109], v[134:137], v[196:199], v[106:109]
	v_mfma_f32_16x16x32_f16 v[94:97], v[126:129], v[204:207], v[94:97]
	v_mfma_f32_16x16x32_f16 v[90:93], v[134:137], v[204:207], v[90:93]
	v_mfma_f32_16x16x32_f16 v[78:81], v[126:129], v[212:215], v[78:81]
	v_mfma_f32_16x16x32_f16 v[74:77], v[134:137], v[212:215], v[74:77]
	v_mfma_f32_16x16x32_f16 v[118:121], v[162:165], v[184:187], v[118:121]
	v_mfma_f32_16x16x32_f16 v[114:117], v[176:179], v[184:187], v[114:117]
	v_mfma_f32_16x16x32_f16 v[102:105], v[162:165], v[192:195], v[102:105]
	v_mfma_f32_16x16x32_f16 v[98:101], v[176:179], v[192:195], v[98:101]
	v_mfma_f32_16x16x32_f16 v[86:89], v[162:165], v[200:203], v[86:89]
	v_mfma_f32_16x16x32_f16 v[82:85], v[176:179], v[200:203], v[82:85]
	v_mfma_f32_16x16x32_f16 v[70:73], v[162:165], v[208:211], v[70:73]
	v_mfma_f32_16x16x32_f16 v[66:69], v[176:179], v[208:211], v[66:69]
	v_mfma_f32_16x16x32_f16 v[118:121], v[172:175], v[188:191], v[118:121]
	v_mfma_f32_16x16x32_f16 v[114:117], v[180:183], v[188:191], v[114:117]
	v_mfma_f32_16x16x32_f16 v[102:105], v[172:175], v[196:199], v[102:105]
	v_mfma_f32_16x16x32_f16 v[98:101], v[180:183], v[196:199], v[98:101]
	v_mfma_f32_16x16x32_f16 v[86:89], v[172:175], v[204:207], v[86:89]
	v_mfma_f32_16x16x32_f16 v[82:85], v[180:183], v[204:207], v[82:85]
	v_mfma_f32_16x16x32_f16 v[70:73], v[172:175], v[212:215], v[70:73]
	v_mfma_f32_16x16x32_f16 v[66:69], v[180:183], v[212:215], v[66:69]
	s_barrier
; #define GM_STAGE(bufoff, gbase, voff) do { _Pragma("unroll") for (int _i = 0; _i < 2; ++_i) \
;         __builtin_amdgcn_global_load_lds((const unsigned*)((const char*)(gbase) + (voff)[_i]), (LAS unsigned*)(lds + (bufoff) + ldsw + _i * 8192), 16, 0, 0); } while (0)
; #define GM_LDA(dst, b, h) do { _Pragma("unroll") for (int m = 0; m < 4; ++m) _Pragma("unroll") for (int k = 0; k < 2; ++k) dst[m][k] = *(const LAS s16x8*)(lds + GM_SA(b, h) + aoff + m * 2048 + k * 1024); } while (0)
; #define GM_MMA(ai, bj, At, Bt) do { __builtin_amdgcn_s_setprio(1); _Pragma("unroll") for (int m = 0; m < 4; ++m) _Pragma("unroll") for (int n = 0; n < 2; ++n) _Pragma("unroll") for (int k = 0; k < 2; ++k) \
;         acc[ai][bj][m][n] = mma16<BF>(Bt[n][k], At[m][k], acc[ai][bj][m][n]); __builtin_amdgcn_s_setprio(0); } while (0)
; #define GM_WAIT_V(n) asm volatile("s_waitcnt vmcnt(" #n ")" ::: "memory")
; #define GM_WAIT_L(n) asm volatile("s_waitcnt lgkmcnt(" #n ")" ::: "memory")
; #define GM_BAR __builtin_amdgcn_s_barrier()
; #define GM_SCHED __builtin_amdgcn_sched_barrier(0)
; #define GM_STA_H0(buf, p, o0) do { if constexpr (GATHER) GM_STAGE(buf, p, o0); else GM_STAGE(buf, p, voffA); } while (0)
; template <bool BF, bool GATHER = false, class Epi, class Hook>
; __device__ __forceinline__ void gemm_phase(LAS unsigned char* lds, const Gemm g, const Order& S, const Epi& E, Hook& HK) {
;     ...
;             GM_LDA(At, 1, 1); GM_STAGE(GM_SB(1, 0), b3, voffB); GM_STAGE(GM_SB(1, 1), b3 + hstepB, voffB); GM_STA_H0(GM_SA(1, 0), a3, s0);
;             GM_WAIT_V(8); GM_WAIT_L(0); GM_BAR; GM_MMA(1, 0, At, B0); GM_MMA(1, 1, At, B1); GM_BAR; GM_SCHED;
;         }
;         if (wr == 0) GM_BAR;
	s_add_i32 s26, s50, s31
	s_mov_b32 m0, s26
	v_lshl_add_u64 v[216:217], v[216:217], 0, s[10:11]
	global_load_lds_dwordx4 v[216:217], off
	s_add_i32 m0, s26, 0x2000
	s_add_u32 s24, s24, 0x40080
	v_lshl_add_u64 v[216:217], v[218:219], 0, s[10:11]
	s_addc_u32 s25, s25, 0
	s_add_i32 s26, s51, s31
	global_load_lds_dwordx4 v[216:217], off
	s_mov_b32 m0, s26
	v_lshl_add_u64 v[216:217], s[24:25], 0, v[148:149]
	global_load_lds_dwordx4 v[216:217], off
	s_add_i32 m0, s26, 0x2000
	v_lshl_add_u64 v[216:217], s[24:25], 0, v[152:153]
	global_load_lds_dwordx4 v[216:217], off
	s_mov_b32 m0, s40
	v_lshl_add_u64 v[216:217], v[220:221], 0, s[10:11]
	global_load_lds_dwordx4 v[216:217], off
	s_mov_b32 m0, s41
	v_lshl_add_u64 v[216:217], v[222:223], 0, s[10:11]
	global_load_lds_dwordx4 v[216:217], off
	ds_read_b128 v[184:187], v170 offset:49152
	ds_read_b128 v[188:191], v170 offset:50176
	ds_read_b128 v[192:195], v170 offset:51200
	ds_read_b128 v[196:199], v170 offset:52224
	ds_read_b128 v[200:203], v170 offset:53248
	ds_read_b128 v[204:207], v170 offset:54272
	ds_read_b128 v[208:211], v170 offset:55296
	ds_read_b128 v[212:215], v170 offset:56320
	s_waitcnt vmcnt(8)
	s_waitcnt lgkmcnt(0)
	s_barrier
	v_mfma_f32_16x16x32_f16 v[62:65], v[122:125], v[184:187], v[62:65]
	v_mfma_f32_16x16x32_f16 v[58:61], v[130:133], v[184:187], v[58:61]
	v_mfma_f32_16x16x32_f16 v[46:49], v[122:125], v[192:195], v[46:49]
	v_mfma_f32_16x16x32_f16 v[42:45], v[130:133], v[192:195], v[42:45]
	v_mfma_f32_16x16x32_f16 v[30:33], v[122:125], v[200:203], v[30:33]
	v_mfma_f32_16x16x32_f16 v[26:29], v[130:133], v[200:203], v[26:29]
	v_mfma_f32_16x16x32_f16 v[14:17], v[122:125], v[208:211], v[14:17]
	v_mfma_f32_16x16x32_f16 v[10:13], v[130:133], v[208:211], v[10:13]
	v_mfma_f32_16x16x32_f16 v[62:65], v[126:129], v[188:191], v[62:65]
	v_mfma_f32_16x16x32_f16 v[58:61], v[134:137], v[188:191], v[58:61]
	v_mfma_f32_16x16x32_f16 v[46:49], v[126:129], v[196:199], v[46:49]
	v_mfma_f32_16x16x32_f16 v[42:45], v[134:137], v[196:199], v[42:45]
	v_mfma_f32_16x16x32_f16 v[30:33], v[126:129], v[204:207], v[30:33]
	v_mfma_f32_16x16x32_f16 v[26:29], v[134:137], v[204:207], v[26:29]
	v_mfma_f32_16x16x32_f16 v[14:17], v[126:129], v[212:215], v[14:17]
	v_mfma_f32_16x16x32_f16 v[10:13], v[134:137], v[212:215], v[10:13]
	v_mfma_f32_16x16x32_f16 v[54:57], v[162:165], v[184:187], v[54:57]
	v_mfma_f32_16x16x32_f16 v[50:53], v[176:179], v[184:187], v[50:53]
	v_mfma_f32_16x16x32_f16 v[38:41], v[162:165], v[192:195], v[38:41]
	v_mfma_f32_16x16x32_f16 v[34:37], v[176:179], v[192:195], v[34:37]
	v_mfma_f32_16x16x32_f16 v[22:25], v[162:165], v[200:203], v[22:25]
	v_mfma_f32_16x16x32_f16 v[18:21], v[176:179], v[200:203], v[18:21]
	v_mfma_f32_16x16x32_f16 v[6:9], v[162:165], v[208:211], v[6:9]
	v_mfma_f32_16x16x32_f16 v[2:5], v[176:179], v[208:211], v[2:5]
	v_mfma_f32_16x16x32_f16 v[54:57], v[172:175], v[188:191], v[54:57]
	v_mfma_f32_16x16x32_f16 v[50:53], v[180:183], v[188:191], v[50:53]
	v_mfma_f32_16x16x32_f16 v[38:41], v[172:175], v[196:199], v[38:41]
	v_mfma_f32_16x16x32_f16 v[34:37], v[180:183], v[196:199], v[34:37]
	v_mfma_f32_16x16x32_f16 v[22:25], v[172:175], v[204:207], v[22:25]
	v_mfma_f32_16x16x32_f16 v[18:21], v[180:183], v[204:207], v[18:21]
	v_mfma_f32_16x16x32_f16 v[6:9], v[172:175], v[212:215], v[6:9]
	v_mfma_f32_16x16x32_f16 v[2:5], v[180:183], v[212:215], v[2:5]
	s_barrier
	s_add_i32 s49, s49, 2
	s_add_u32 s22, s22, 0x100
	s_addc_u32 s23, s23, 0
	s_add_u32 s47, s47, 0x100
	s_addc_u32 s48, s48, 0
	s_cmp_gt_u32 s49, 13
	s_cbranch_scc0 .LBB0_1480
	s_and_b64 vcc, exec, s[12:13]
	s_cbranch_vccz .LBB0_1483
	s_barrier

; #define GM_STAGE(bufoff, gbase, voff) do { _Pragma("unroll") for (int _i = 0; _i < 2; ++_i) \
;         __builtin_amdgcn_global_load_lds((const unsigned*)((const char*)(gbase) + (voff)[_i]), (LAS unsigned*)(lds + (bufoff) + ldsw + _i * 8192), 16, 0, 0); } while (0)
; #define GM_LDA(dst, b, h) do { _Pragma("unroll") for (int m = 0; m < 4; ++m) _Pragma("unroll") for (int k = 0; k < 2; ++k) dst[m][k] = *(const LAS s16x8*)(lds + GM_SA(b, h) + aoff + m * 2048 + k * 1024); } while (0)
; #define GM_LDB(dst, b, h) do { _Pragma("unroll") for (int n = 0; n < 2; ++n) _Pragma("unroll") for (int k = 0; k < 2; ++k) dst[n][k] = *(const LAS s16x8*)(lds + GM_SB(b, h) + boff + n * 2048 + k * 1024); } while (0)
; #define GM_MMA(ai, bj, At, Bt) do { __builtin_amdgcn_s_setprio(1); _Pragma("unroll") for (int m = 0; m < 4; ++m) _Pragma("unroll") for (int n = 0; n < 2; ++n) _Pragma("unroll") for (int k = 0; k < 2; ++k) \
;         acc[ai][bj][m][n] = mma16<BF>(Bt[n][k], At[m][k], acc[ai][bj][m][n]); __builtin_amdgcn_s_setprio(0); } while (0)
; #define GM_WAIT_V(n) asm volatile("s_waitcnt vmcnt(" #n ")" ::: "memory")
; #define GM_BAR __builtin_amdgcn_s_barrier()
; template <bool BF, bool GATHER = false, class Epi, class Hook>
; __device__ __forceinline__ void gemm_phase(LAS unsigned char* lds, const Gemm g, const Order& S, const Epi& E, Hook& HK) {
;     ...
;         for (int t = 0; t < nt; t += 2) {
;             const bool last = (t == nt - 2);
;             const char* a1 = cA + (size_t)(t + 1) * kstep;
;             const char* a2 = last ? nA : cA + (size_t)(t + 2) * kstep; const char* b2 = last ? nB : cB + (size_t)(t + 2) * kstep;
;             const char* a3 = a2 + kstep; const char* b3 = b2 + kstep;
;             unsigned s0[2], s1[2];
;             if constexpr (GATHER) { s0[0] = last ? nA0[0] : gA0[0]; s0[1] = last ? nA0[1] : gA0[1]; s1[0] = last ? nA1[0] : gA1[0]; s1[1] = last ? nA1[1] : gA1[1]; }
;             GM_LDB(B0, 0, 0); GM_LDB(B1, 0, 1); GM_SCHED; GM_LDA(At, 0, 0); GM_STA_H1(GM_SA(1, 1), a1, gA1);
;             GM_WAIT_V(8); GM_WAIT_L(0); GM_BAR; GM_MMA(0, 0, At, B0); GM_MMA(0, 1, At, B1); GM_BAR; GM_SCHED;
;             GM_LDA(At, 0, 1); GM_STAGE(GM_SB(0, 0), b2, voffB); GM_STAGE(GM_SB(0, 1), b2 + hstepB, voffB); GM_STA_H0(GM_SA(0, 0), a2, s0);
;             GM_WAIT_V(8); GM_WAIT_L(0); GM_BAR; GM_MMA(1, 0, At, B0); GM_MMA(1, 1, At, B1); GM_BAR; GM_SCHED;
.LBB0_1867:
	s_add_u32 s22, s2, 0x100
	s_addc_u32 s23, s3, 0
	s_cmp_eq_u32 s52, 40
	s_cselect_b32 s27, s7, s23
	s_cselect_b32 s26, s6, s22
	s_cselect_b32 s25, s21, s51
	s_cselect_b32 s24, s20, s50
	s_add_i32 m0, s29, 0xc000
	v_lshl_add_u64 v[216:217], s[2:3], 0, v[138:139]
	global_load_lds_dwordx4 v[216:217], off
	s_add_i32 m0, s29, 0xe000
	v_lshl_add_u64 v[216:217], s[2:3], 0, v[140:141]
	global_load_lds_dwordx4 v[216:217], off
	ds_read_b128 v[146:149], v153
	ds_read_b128 v[156:159], v153 offset:1024
	ds_read_b128 v[160:163], v153 offset:2048
	ds_read_b128 v[164:167], v153 offset:3072
	ds_read_b128 v[168:171], v154
	ds_read_b128 v[172:175], v154 offset:1024
	ds_read_b128 v[176:179], v154 offset:2048
	ds_read_b128 v[180:183], v154 offset:3072
	ds_read_b128 v[184:187], v155
	ds_read_b128 v[188:191], v155 offset:1024
	ds_read_b128 v[192:195], v155 offset:2048
	ds_read_b128 v[196:199], v155 offset:3072
	ds_read_b128 v[200:203], v155 offset:4096
	ds_read_b128 v[204:207], v155 offset:5120
	ds_read_b128 v[208:211], v155 offset:6144
	ds_read_b128 v[212:215], v155 offset:7168
	s_waitcnt vmcnt(8)
	s_waitcnt lgkmcnt(0)
	s_barrier
	v_mfma_f32_16x16x32_bf16 v[126:129], v[146:149], v[184:187], v[126:129]
	v_mfma_f32_16x16x32_bf16 v[122:125], v[160:163], v[184:187], v[122:125]
	v_mfma_f32_16x16x32_bf16 v[110:113], v[146:149], v[192:195], v[110:113]
	v_mfma_f32_16x16x32_bf16 v[106:109], v[160:163], v[192:195], v[106:109]
	v_mfma_f32_16x16x32_bf16 v[94:97], v[146:149], v[200:203], v[94:97]
	v_mfma_f32_16x16x32_bf16 v[90:93], v[160:163], v[200:203], v[90:93]
	v_mfma_f32_16x16x32_bf16 v[78:81], v[146:149], v[208:211], v[78:81]
	v_mfma_f32_16x16x32_bf16 v[74:77], v[160:163], v[208:211], v[74:77]
	v_mfma_f32_16x16x32_bf16 v[126:129], v[156:159], v[188:191], v[126:129]
	v_mfma_f32_16x16x32_bf16 v[122:125], v[164:167], v[188:191], v[122:125]
	v_mfma_f32_16x16x32_bf16 v[110:113], v[156:159], v[196:199], v[110:113]
	v_mfma_f32_16x16x32_bf16 v[106:109], v[164:167], v[196:199], v[106:109]
	v_mfma_f32_16x16x32_bf16 v[94:97], v[156:159], v[204:207], v[94:97]
	v_mfma_f32_16x16x32_bf16 v[90:93], v[164:167], v[204:207], v[90:93]
	v_mfma_f32_16x16x32_bf16 v[78:81], v[156:159], v[212:215], v[78:81]
	v_mfma_f32_16x16x32_bf16 v[74:77], v[164:167], v[212:215], v[74:77]
	v_mfma_f32_16x16x32_bf16 v[118:121], v[168:171], v[184:187], v[118:121]
	v_mfma_f32_16x16x32_bf16 v[114:117], v[176:179], v[184:187], v[114:117]
	v_mfma_f32_16x16x32_bf16 v[102:105], v[168:171], v[192:195], v[102:105]
	v_mfma_f32_16x16x32_bf16 v[98:101], v[176:179], v[192:195], v[98:101]
	v_mfma_f32_16x16x32_bf16 v[86:89], v[168:171], v[200:203], v[86:89]
	v_mfma_f32_16x16x32_bf16 v[82:85], v[176:179], v[200:203], v[82:85]
	v_mfma_f32_16x16x32_bf16 v[70:73], v[168:171], v[208:211], v[70:73]
	v_mfma_f32_16x16x32_bf16 v[66:69], v[176:179], v[208:211], v[66:69]
	v_mfma_f32_16x16x32_bf16 v[118:121], v[172:175], v[188:191], v[118:121]
	v_mfma_f32_16x16x32_bf16 v[114:117], v[180:183], v[188:191], v[114:117]
	v_mfma_f32_16x16x32_bf16 v[102:105], v[172:175], v[196:199], v[102:105]
	v_mfma_f32_16x16x32_bf16 v[98:101], v[180:183], v[196:199], v[98:101]
	v_mfma_f32_16x16x32_bf16 v[86:89], v[172:175], v[204:207], v[86:89]
	v_mfma_f32_16x16x32_bf16 v[82:85], v[180:183], v[204:207], v[82:85]
	v_mfma_f32_16x16x32_bf16 v[70:73], v[172:175], v[212:215], v[70:73]
	v_mfma_f32_16x16x32_bf16 v[66:69], v[180:183], v[212:215], v[66:69]
	s_barrier
	s_add_i32 s2, s43, s28
	s_mov_b32 m0, s2
	v_lshl_add_u64 v[216:217], s[24:25], 0, v[132:133]
	global_load_lds_dwordx4 v[216:217], off
	s_add_i32 m0, s2, 0x2000
	s_add_u32 s2, s24, 0xb0000
	v_lshl_add_u64 v[218:219], s[24:25], 0, v[136:137]
	s_addc_u32 s3, s25, 0
	s_add_i32 s53, s44, s28
	global_load_lds_dwordx4 v[218:219], off
	v_lshl_add_u64 v[220:221], s[2:3], 0, v[132:133]
	s_mov_b32 m0, s53
	v_lshl_add_u64 v[222:223], s[26:27], 0, v[134:135]
	global_load_lds_dwordx4 v[220:221], off
	s_add_i32 m0, s53, 0x2000
	v_lshl_add_u64 v[220:221], s[2:3], 0, v[136:137]
	global_load_lds_dwordx4 v[220:221], off
	s_mov_b32 m0, s29
	v_lshl_add_u64 v[220:221], s[26:27], 0, v[130:131]
	global_load_lds_dwordx4 v[220:221], off
	s_mov_b32 m0, s30
	s_nop 0
	global_load_lds_dwordx4 v[222:223], off
	ds_read_b128 v[184:187], v155 offset:16384
	ds_read_b128 v[188:191], v155 offset:17408
	ds_read_b128 v[192:195], v155 offset:18432
	ds_read_b128 v[196:199], v155 offset:19456
	ds_read_b128 v[200:203], v155 offset:20480
	ds_read_b128 v[204:207], v155 offset:21504
	ds_read_b128 v[208:211], v155 offset:22528
	ds_read_b128 v[212:215], v155 offset:23552
	s_waitcnt vmcnt(8)
	s_waitcnt lgkmcnt(0)
	s_barrier
; #define GM_LDA(dst, b, h) do { _Pragma("unroll") for (int m = 0; m < 4; ++m) _Pragma("unroll") for (int k = 0; k < 2; ++k) dst[m][k] = *(const LAS s16x8*)(lds + GM_SA(b, h) + aoff + m * 2048 + k * 1024); } while (0)
; #define GM_LDB(dst, b, h) do { _Pragma("unroll") for (int n = 0; n < 2; ++n) _Pragma("unroll") for (int k = 0; k < 2; ++k) dst[n][k] = *(const LAS s16x8*)(lds + GM_SB(b, h) + boff + n * 2048 + k * 1024); } while (0)
; #define GM_MMA(ai, bj, At, Bt) do { __builtin_amdgcn_s_setprio(1); _Pragma("unroll") for (int m = 0; m < 4; ++m) _Pragma("unroll") for (int n = 0; n < 2; ++n) _Pragma("unroll") for (int k = 0; k < 2; ++k) \
;         acc[ai][bj][m][n] = mma16<BF>(Bt[n][k], At[m][k], acc[ai][bj][m][n]); __builtin_amdgcn_s_setprio(0); } while (0)
; #define GM_WAIT_V(n) asm volatile("s_waitcnt vmcnt(" #n ")" ::: "memory")
; #define GM_WAIT_L(n) asm volatile("s_waitcnt lgkmcnt(" #n ")" ::: "memory")
; #define GM_BAR __builtin_amdgcn_s_barrier()
; #define GM_SCHED __builtin_amdgcn_sched_barrier(0)
; #define GM_STA_H1(buf, p, o1) do { if constexpr (GATHER) GM_STAGE(buf, p, o1); else GM_STAGE(buf, (p) + hstepB, voffA); } while (0)
; template <bool BF, bool GATHER = false, class Epi, class Hook>
; __device__ __forceinline__ void gemm_phase(LAS unsigned char* lds, const Gemm g, const Order& S, const Epi& E, Hook& HK) {
;     ...
;             GM_WAIT_V(8); GM_WAIT_L(0); GM_BAR; GM_MMA(1, 0, At, B0); GM_MMA(1, 1, At, B1); GM_BAR; GM_SCHED;
;             GM_LDB(B0, 1, 0); GM_LDB(B1, 1, 1); GM_SCHED; GM_LDA(At, 1, 0); GM_STA_H1(GM_SA(0, 1), a2, s1);
;             GM_WAIT_V(8); GM_WAIT_L(0); GM_BAR; GM_MMA(0, 0, At, B0); GM_MMA(0, 1, At, B1); GM_BAR; GM_SCHED;
	v_mfma_f32_16x16x32_bf16 v[62:65], v[146:149], v[184:187], v[62:65]
	v_mfma_f32_16x16x32_bf16 v[58:61], v[160:163], v[184:187], v[58:61]
	v_mfma_f32_16x16x32_bf16 v[46:49], v[146:149], v[192:195], v[46:49]
	v_mfma_f32_16x16x32_bf16 v[42:45], v[160:163], v[192:195], v[42:45]
	v_mfma_f32_16x16x32_bf16 v[30:33], v[146:149], v[200:203], v[30:33]
	v_mfma_f32_16x16x32_bf16 v[26:29], v[160:163], v[200:203], v[26:29]
	v_mfma_f32_16x16x32_bf16 v[14:17], v[146:149], v[208:211], v[14:17]
	v_mfma_f32_16x16x32_bf16 v[10:13], v[160:163], v[208:211], v[10:13]
	v_mfma_f32_16x16x32_bf16 v[62:65], v[156:159], v[188:191], v[62:65]
	v_mfma_f32_16x16x32_bf16 v[58:61], v[164:167], v[188:191], v[58:61]
	v_mfma_f32_16x16x32_bf16 v[46:49], v[156:159], v[196:199], v[46:49]
	v_mfma_f32_16x16x32_bf16 v[42:45], v[164:167], v[196:199], v[42:45]
	v_mfma_f32_16x16x32_bf16 v[30:33], v[156:159], v[204:207], v[30:33]
	v_mfma_f32_16x16x32_bf16 v[26:29], v[164:167], v[204:207], v[26:29]
	v_mfma_f32_16x16x32_bf16 v[14:17], v[156:159], v[212:215], v[14:17]
	v_mfma_f32_16x16x32_bf16 v[10:13], v[164:167], v[212:215], v[10:13]
	v_mfma_f32_16x16x32_bf16 v[54:57], v[168:171], v[184:187], v[54:57]
	v_mfma_f32_16x16x32_bf16 v[50:53], v[176:179], v[184:187], v[50:53]
	v_mfma_f32_16x16x32_bf16 v[38:41], v[168:171], v[192:195], v[38:41]
	v_mfma_f32_16x16x32_bf16 v[34:37], v[176:179], v[192:195], v[34:37]
	v_mfma_f32_16x16x32_bf16 v[22:25], v[168:171], v[200:203], v[22:25]
	v_mfma_f32_16x16x32_bf16 v[18:21], v[176:179], v[200:203], v[18:21]
	v_mfma_f32_16x16x32_bf16 v[6:9], v[168:171], v[208:211], v[6:9]
	v_mfma_f32_16x16x32_bf16 v[2:5], v[176:179], v[208:211], v[2:5]
	v_mfma_f32_16x16x32_bf16 v[54:57], v[172:175], v[188:191], v[54:57]
	v_mfma_f32_16x16x32_bf16 v[50:53], v[180:183], v[188:191], v[50:53]
	v_mfma_f32_16x16x32_bf16 v[38:41], v[172:175], v[196:199], v[38:41]
	v_mfma_f32_16x16x32_bf16 v[34:37], v[180:183], v[196:199], v[34:37]
	v_mfma_f32_16x16x32_bf16 v[22:25], v[172:175], v[204:207], v[22:25]
	v_mfma_f32_16x16x32_bf16 v[18:21], v[180:183], v[204:207], v[18:21]
	v_mfma_f32_16x16x32_bf16 v[6:9], v[172:175], v[212:215], v[6:9]
	v_mfma_f32_16x16x32_bf16 v[2:5], v[180:183], v[212:215], v[2:5]
	s_barrier
	s_add_u32 s2, s26, 0xb0000
	s_addc_u32 s3, s27, 0
	s_mov_b32 m0, s31
	v_lshl_add_u64 v[224:225], s[2:3], 0, v[130:131]
	global_load_lds_dwordx4 v[224:225], off
	s_mov_b32 m0, s33
	v_lshl_add_u64 v[224:225], s[2:3], 0, v[134:135]
	global_load_lds_dwordx4 v[224:225], off
	s_mov_b32 s54, 0x1c000
	s_mov_b32 s53, 0x18000
	v_add_u32_e32 v244, s53, v150
	v_add_u32_e32 v245, s54, v150
	ds_read_b128 v[146:149], v244
	ds_read_b128 v[156:159], v244 offset:1024
	ds_read_b128 v[160:163], v244 offset:2048
	ds_read_b128 v[164:167], v244 offset:3072
	ds_read_b128 v[168:171], v245
	ds_read_b128 v[172:175], v245 offset:1024
	ds_read_b128 v[176:179], v245 offset:2048
	ds_read_b128 v[180:183], v245 offset:3072
	ds_read_b128 v[184:187], v155 offset:32768
	ds_read_b128 v[188:191], v155 offset:33792
	ds_read_b128 v[192:195], v155 offset:34816
	ds_read_b128 v[196:199], v155 offset:35840
	ds_read_b128 v[200:203], v155 offset:36864
	ds_read_b128 v[204:207], v155 offset:37888
	ds_read_b128 v[208:211], v155 offset:38912
	ds_read_b128 v[212:215], v155 offset:39936
	s_waitcnt vmcnt(8)
	s_waitcnt lgkmcnt(0)
	s_barrier
	v_mfma_f32_16x16x32_bf16 v[126:129], v[146:149], v[184:187], v[126:129]
	v_mfma_f32_16x16x32_bf16 v[122:125], v[160:163], v[184:187], v[122:125]
	v_mfma_f32_16x16x32_bf16 v[110:113], v[146:149], v[192:195], v[110:113]
	v_mfma_f32_16x16x32_bf16 v[106:109], v[160:163], v[192:195], v[106:109]
	v_mfma_f32_16x16x32_bf16 v[94:97], v[146:149], v[200:203], v[94:97]
	v_mfma_f32_16x16x32_bf16 v[90:93], v[160:163], v[200:203], v[90:93]
	v_mfma_f32_16x16x32_bf16 v[78:81], v[146:149], v[208:211], v[78:81]
	v_mfma_f32_16x16x32_bf16 v[74:77], v[160:163], v[208:211], v[74:77]
	v_mfma_f32_16x16x32_bf16 v[126:129], v[156:159], v[188:191], v[126:129]
	v_mfma_f32_16x16x32_bf16 v[122:125], v[164:167], v[188:191], v[122:125]
	v_mfma_f32_16x16x32_bf16 v[110:113], v[156:159], v[196:199], v[110:113]
	v_mfma_f32_16x16x32_bf16 v[106:109], v[164:167], v[196:199], v[106:109]
	v_mfma_f32_16x16x32_bf16 v[94:97], v[156:159], v[204:207], v[94:97]
	v_mfma_f32_16x16x32_bf16 v[90:93], v[164:167], v[204:207], v[90:93]
	v_mfma_f32_16x16x32_bf16 v[78:81], v[156:159], v[212:215], v[78:81]
	v_mfma_f32_16x16x32_bf16 v[74:77], v[164:167], v[212:215], v[74:77]
	v_mfma_f32_16x16x32_bf16 v[118:121], v[168:171], v[184:187], v[118:121]
	v_mfma_f32_16x16x32_bf16 v[114:117], v[176:179], v[184:187], v[114:117]
	v_mfma_f32_16x16x32_bf16 v[102:105], v[168:171], v[192:195], v[102:105]
	v_mfma_f32_16x16x32_bf16 v[98:101], v[176:179], v[192:195], v[98:101]
	v_mfma_f32_16x16x32_bf16 v[86:89], v[168:171], v[200:203], v[86:89]
	v_mfma_f32_16x16x32_bf16 v[82:85], v[176:179], v[200:203], v[82:85]
	v_mfma_f32_16x16x32_bf16 v[70:73], v[168:171], v[208:211], v[70:73]
	v_mfma_f32_16x16x32_bf16 v[66:69], v[176:179], v[208:211], v[66:69]
	v_mfma_f32_16x16x32_bf16 v[118:121], v[172:175], v[188:191], v[118:121]
	v_mfma_f32_16x16x32_bf16 v[114:117], v[180:183], v[188:191], v[114:117]
	v_mfma_f32_16x16x32_bf16 v[102:105], v[172:175], v[196:199], v[102:105]
	v_mfma_f32_16x16x32_bf16 v[98:101], v[180:183], v[196:199], v[98:101]
	v_mfma_f32_16x16x32_bf16 v[86:89], v[172:175], v[204:207], v[86:89]
	v_mfma_f32_16x16x32_bf16 v[82:85], v[180:183], v[204:207], v[82:85]
	v_mfma_f32_16x16x32_bf16 v[70:73], v[172:175], v[212:215], v[70:73]
	v_mfma_f32_16x16x32_bf16 v[66:69], v[180:183], v[212:215], v[66:69]
	s_barrier
; #define GM_STAGE(bufoff, gbase, voff) do { _Pragma("unroll") for (int _i = 0; _i < 2; ++_i) \
;         __builtin_amdgcn_global_load_lds((const unsigned*)((const char*)(gbase) + (voff)[_i]), (LAS unsigned*)(lds + (bufoff) + ldsw + _i * 8192), 16, 0, 0); } while (0)
; #define GM_LDA(dst, b, h) do { _Pragma("unroll") for (int m = 0; m < 4; ++m) _Pragma("unroll") for (int k = 0; k < 2; ++k) dst[m][k] = *(const LAS s16x8*)(lds + GM_SA(b, h) + aoff + m * 2048 + k * 1024); } while (0)
; #define GM_MMA(ai, bj, At, Bt) do { __builtin_amdgcn_s_setprio(1); _Pragma("unroll") for (int m = 0; m < 4; ++m) _Pragma("unroll") for (int n = 0; n < 2; ++n) _Pragma("unroll") for (int k = 0; k < 2; ++k) \
;         acc[ai][bj][m][n] = mma16<BF>(Bt[n][k], At[m][k], acc[ai][bj][m][n]); __builtin_amdgcn_s_setprio(0); } while (0)
; #define GM_WAIT_V(n) asm volatile("s_waitcnt vmcnt(" #n ")" ::: "memory")
; #define GM_WAIT_L(n) asm volatile("s_waitcnt lgkmcnt(" #n ")" ::: "memory")
; #define GM_BAR __builtin_amdgcn_s_barrier()
; #define GM_SCHED __builtin_amdgcn_sched_barrier(0)
; #define GM_STA_H0(buf, p, o0) do { if constexpr (GATHER) GM_STAGE(buf, p, o0); else GM_STAGE(buf, p, voffA); } while (0)
; template <bool BF, bool GATHER = false, class Epi, class Hook>
; __device__ __forceinline__ void gemm_phase(LAS unsigned char* lds, const Gemm g, const Order& S, const Epi& E, Hook& HK) {
;     ...
;             GM_LDA(At, 1, 1); GM_STAGE(GM_SB(1, 0), b3, voffB); GM_STAGE(GM_SB(1, 1), b3 + hstepB, voffB); GM_STA_H0(GM_SA(1, 0), a3, s0);
;             GM_WAIT_V(8); GM_WAIT_L(0); GM_BAR; GM_MMA(1, 0, At, B0); GM_MMA(1, 1, At, B1); GM_BAR; GM_SCHED;
;         }
;         if (wr == 0) GM_BAR;
	s_add_i32 s2, s53, s28
	s_mov_b32 m0, s2
	v_lshl_add_u64 v[216:217], v[216:217], 0, s[12:13]
	global_load_lds_dwordx4 v[216:217], off
	s_add_i32 m0, s2, 0x2000
	s_add_u32 s2, s24, 0xb0080
	v_lshl_add_u64 v[216:217], v[218:219], 0, s[12:13]
	s_addc_u32 s3, s25, 0
	s_add_i32 s24, s54, s28
	global_load_lds_dwordx4 v[216:217], off
	s_mov_b32 m0, s24
	v_lshl_add_u64 v[216:217], s[2:3], 0, v[132:133]
	global_load_lds_dwordx4 v[216:217], off
	s_add_i32 m0, s24, 0x2000
	v_lshl_add_u64 v[216:217], s[2:3], 0, v[136:137]
	global_load_lds_dwordx4 v[216:217], off
	s_mov_b32 m0, s36
	v_lshl_add_u64 v[216:217], v[220:221], 0, s[12:13]
	global_load_lds_dwordx4 v[216:217], off
	s_mov_b32 m0, s37
	v_lshl_add_u64 v[216:217], v[222:223], 0, s[12:13]
	global_load_lds_dwordx4 v[216:217], off
	ds_read_b128 v[184:187], v155 offset:49152
	ds_read_b128 v[188:191], v155 offset:50176
	ds_read_b128 v[192:195], v155 offset:51200
	ds_read_b128 v[196:199], v155 offset:52224
	ds_read_b128 v[200:203], v155 offset:53248
	ds_read_b128 v[204:207], v155 offset:54272
	ds_read_b128 v[208:211], v155 offset:55296
	ds_read_b128 v[212:215], v155 offset:56320
	s_waitcnt vmcnt(8)
	s_waitcnt lgkmcnt(0)
	s_barrier
	v_mfma_f32_16x16x32_bf16 v[62:65], v[146:149], v[184:187], v[62:65]
	v_mfma_f32_16x16x32_bf16 v[58:61], v[160:163], v[184:187], v[58:61]
	v_mfma_f32_16x16x32_bf16 v[46:49], v[146:149], v[192:195], v[46:49]
	v_mfma_f32_16x16x32_bf16 v[42:45], v[160:163], v[192:195], v[42:45]
	v_mfma_f32_16x16x32_bf16 v[30:33], v[146:149], v[200:203], v[30:33]
	v_mfma_f32_16x16x32_bf16 v[26:29], v[160:163], v[200:203], v[26:29]
	v_mfma_f32_16x16x32_bf16 v[14:17], v[146:149], v[208:211], v[14:17]
	v_mfma_f32_16x16x32_bf16 v[10:13], v[160:163], v[208:211], v[10:13]
	v_mfma_f32_16x16x32_bf16 v[62:65], v[156:159], v[188:191], v[62:65]
	v_mfma_f32_16x16x32_bf16 v[58:61], v[164:167], v[188:191], v[58:61]
	v_mfma_f32_16x16x32_bf16 v[46:49], v[156:159], v[196:199], v[46:49]
	v_mfma_f32_16x16x32_bf16 v[42:45], v[164:167], v[196:199], v[42:45]
	v_mfma_f32_16x16x32_bf16 v[30:33], v[156:159], v[204:207], v[30:33]
	v_mfma_f32_16x16x32_bf16 v[26:29], v[164:167], v[204:207], v[26:29]
	v_mfma_f32_16x16x32_bf16 v[14:17], v[156:159], v[212:215], v[14:17]
	v_mfma_f32_16x16x32_bf16 v[10:13], v[164:167], v[212:215], v[10:13]
	v_mfma_f32_16x16x32_bf16 v[54:57], v[168:171], v[184:187], v[54:57]
	v_mfma_f32_16x16x32_bf16 v[50:53], v[176:179], v[184:187], v[50:53]
	v_mfma_f32_16x16x32_bf16 v[38:41], v[168:171], v[192:195], v[38:41]
	v_mfma_f32_16x16x32_bf16 v[34:37], v[176:179], v[192:195], v[34:37]
	v_mfma_f32_16x16x32_bf16 v[22:25], v[168:171], v[200:203], v[22:25]
	v_mfma_f32_16x16x32_bf16 v[18:21], v[176:179], v[200:203], v[18:21]
	v_mfma_f32_16x16x32_bf16 v[6:9], v[168:171], v[208:211], v[6:9]
	v_mfma_f32_16x16x32_bf16 v[2:5], v[176:179], v[208:211], v[2:5]
	v_mfma_f32_16x16x32_bf16 v[54:57], v[172:175], v[188:191], v[54:57]
	v_mfma_f32_16x16x32_bf16 v[50:53], v[180:183], v[188:191], v[50:53]
	v_mfma_f32_16x16x32_bf16 v[38:41], v[172:175], v[196:199], v[38:41]
	v_mfma_f32_16x16x32_bf16 v[34:37], v[180:183], v[196:199], v[34:37]
	v_mfma_f32_16x16x32_bf16 v[22:25], v[172:175], v[204:207], v[22:25]
	v_mfma_f32_16x16x32_bf16 v[18:21], v[180:183], v[204:207], v[18:21]
	v_mfma_f32_16x16x32_bf16 v[6:9], v[172:175], v[212:215], v[6:9]
	v_mfma_f32_16x16x32_bf16 v[2:5], v[180:183], v[212:215], v[2:5]
	s_barrier
	s_add_i32 s52, s52, 2
	s_add_u32 s50, s50, 0x100
	s_addc_u32 s51, s51, 0
	s_cmp_gt_u32 s52, 41
	s_mov_b64 s[2:3], s[22:23]
	s_cbranch_scc0 .LBB0_1867
	s_and_b64 vcc, exec, s[14:15]
	s_cbranch_vccz .LBB0_1870
	s_barrier
